# E1 and E2 item loops now chain items: next work-queue index requested two tokens before the item ends and the next item's ids and first gathers issued during the last tokens, removing the dequeue and
# speedup vs baseline: 1.0309x; 1.0073x over previous
.Le1_loop:
	s_waitcnt vmcnt(1)
	v_and_b32_e32 v194, 0xffff, v170
	v_lshrrev_b32_e32 v195, 16, v170
	v_lshl_add_u32 v194, v194, 7, v218
	v_lshl_add_u32 v195, v195, 7, v218
	global_load_dwordx4 v[66:69], v194, s[10:11]
	global_load_dwordx4 v[70:73], v195, s[10:11]
	v_and_b32_e32 v194, 0xffff, v171
	v_lshrrev_b32_e32 v195, 16, v171
	v_lshl_add_u32 v194, v194, 7, v218
	v_lshl_add_u32 v195, v195, 7, v218
	global_load_dwordx4 v[74:77], v194, s[10:11]
	global_load_dwordx4 v[78:81], v195, s[10:11]
	v_and_b32_e32 v194, 0xffff, v172
	v_lshrrev_b32_e32 v195, 16, v172
	v_lshl_add_u32 v194, v194, 7, v218
	v_lshl_add_u32 v195, v195, 7, v218
	global_load_dwordx4 v[82:85], v194, s[10:11]
	global_load_dwordx4 v[86:89], v195, s[10:11]
	v_and_b32_e32 v194, 0xffff, v173
	v_lshrrev_b32_e32 v195, 16, v173
	v_lshl_add_u32 v194, v194, 7, v218
	v_lshl_add_u32 v195, v195, 7, v218
	global_load_dwordx4 v[90:93], v194, s[10:11]
	global_load_dwordx4 v[94:97], v195, s[10:11]
	v_and_b32_e32 v194, 0xffff, v174
	v_lshrrev_b32_e32 v195, 16, v174
	v_lshl_add_u32 v194, v194, 7, v218
	v_lshl_add_u32 v195, v195, 7, v218
	global_load_dwordx4 v[98:101], v194, s[10:11]
	global_load_dwordx4 v[102:105], v195, s[10:11]
	v_and_b32_e32 v194, 0xffff, v175
	v_lshrrev_b32_e32 v195, 16, v175
	v_lshl_add_u32 v194, v194, 7, v218
	v_lshl_add_u32 v195, v195, 7, v218
	global_load_dwordx4 v[106:109], v194, s[10:11]
	global_load_dwordx4 v[110:113], v195, s[10:11]
	v_and_b32_e32 v194, 0xffff, v176
	v_lshrrev_b32_e32 v195, 16, v176
	v_lshl_add_u32 v194, v194, 7, v218
	v_lshl_add_u32 v195, v195, 7, v218
	global_load_dwordx4 v[114:117], v194, s[10:11]
	global_load_dwordx4 v[118:121], v195, s[10:11]
	v_and_b32_e32 v194, 0xffff, v177
	v_lshrrev_b32_e32 v195, 16, v177
	v_lshl_add_u32 v194, v194, 7, v218
	v_lshl_add_u32 v195, v195, 7, v218
	global_load_dwordx4 v[122:125], v194, s[10:11]
	global_load_dwordx4 v[126:129], v195, s[10:11]
	v_add_u32_e32 v196, 0x1000, v226
	global_load_dwordx4 v[146:149], v196, s[2:3]
	global_load_dwordx4 v[150:153], v196, s[2:3] offset:16
	global_load_dwordx4 v[154:157], v196, s[2:3] offset:32
	global_load_dwordx4 v[158:161], v196, s[2:3] offset:48
	s_cmp_lt_u32 s34, 6
	s_cbranch_scc0 .Le1_A_last
	global_load_dwordx4 v[162:165], v219, s[22:23]
	global_load_dwordx4 v[166:169], v219, s[22:23] offset:16
	s_cmp_eq_u32 s34, 4
	s_cbranch_scc0 .Le1_A_done
	s_barrier
	s_and_saveexec_b64 s[24:25], s[44:45]
	s_cbranch_execz .Le1_A_noatom
	global_atomic_add v250, v211, v1, s[0:1] sc0
.Le1_A_noatom:
	s_or_b64 exec, exec, s[24:25]
	s_branch .Le1_A_done
.Le1_A_last:
	v_mov_b32_e32 v196, s92
	ds_read_b32 v196, v196
	s_waitcnt lgkmcnt(0)
	v_readfirstlane_b32 s35, v196
	s_cmp_ge_i32 s35, s60
	s_cbranch_scc1 .Le1_A_nonext
	s_lshl_b32 s98, s35, 6
	s_and_b32 s99, s35, 0xffffff00
	s_add_i32 s99, s99, 0x100
	s_and_b64 s[24:25], s[30:31], exec
	s_cselect_b32 s99, 0, s99
	s_add_i32 s98, s98, s99
	v_and_b32_e32 v233, 63, v0
	v_lshrrev_b32_e32 v234, 6, v0
	v_and_b32_e32 v235, 7, v0
	v_bfe_u32 v236, v0, 3, 3
	v_lshl_add_u32 v237, v234, 3, s98
	v_lshlrev_b32_e32 v219, 8, v237
	v_lshl_add_u32 v251, v233, 2, v219
	v_lshl_add_u32 v219, v236, 5, v219
	v_lshlrev_b32_e32 v226, 12, v237
	v_lshl_add_u32 v226, v235, 6, v226
	v_add_u32_e32 v226, s76, v226
	v_add_u32_e32 v226, 0xffffe000, v226
	global_load_dwordx4 v[162:165], v219, s[22:23]
	global_load_dwordx4 v[166:169], v219, s[22:23] offset:16
	global_load_dwordx4 v[170:173], v219, s[22:23] offset:256
	global_load_dwordx4 v[174:177], v219, s[22:23] offset:272
	v_add_u32_e32 v219, 0x200, v219
	s_branch .Le1_A_done
.Le1_A_nonext:
	s_mov_b32 s35, -1
.Le1_A_done:
	v_lshlrev_b32_e32 v194, 16, v130
	v_and_b32_e32 v195, 0xffff0000, v130
	v_cvt_pk_f16_f32 v130, v194, v195
	v_lshlrev_b32_e32 v194, 16, v131
	v_and_b32_e32 v195, 0xffff0000, v131
	v_cvt_pk_f16_f32 v131, v194, v195
	v_lshlrev_b32_e32 v194, 16, v132
	v_and_b32_e32 v195, 0xffff0000, v132
	v_cvt_pk_f16_f32 v132, v194, v195
	v_lshlrev_b32_e32 v194, 16, v133
	v_and_b32_e32 v195, 0xffff0000, v133
	v_cvt_pk_f16_f32 v133, v194, v195
	v_lshlrev_b32_e32 v194, 16, v134
	v_and_b32_e32 v195, 0xffff0000, v134
	v_cvt_pk_f16_f32 v134, v194, v195
	v_lshlrev_b32_e32 v194, 16, v135
	v_and_b32_e32 v195, 0xffff0000, v135
	v_cvt_pk_f16_f32 v135, v194, v195
	v_lshlrev_b32_e32 v194, 16, v136
	v_and_b32_e32 v195, 0xffff0000, v136
	v_cvt_pk_f16_f32 v136, v194, v195
	v_lshlrev_b32_e32 v194, 16, v137
	v_and_b32_e32 v195, 0xffff0000, v137
	v_cvt_pk_f16_f32 v137, v194, v195
	v_lshlrev_b32_e32 v194, 16, v138
	v_and_b32_e32 v195, 0xffff0000, v138
	v_cvt_pk_f16_f32 v138, v194, v195
	v_lshlrev_b32_e32 v194, 16, v139
	v_and_b32_e32 v195, 0xffff0000, v139
	v_cvt_pk_f16_f32 v139, v194, v195
	v_lshlrev_b32_e32 v194, 16, v140
	v_and_b32_e32 v195, 0xffff0000, v140
	v_cvt_pk_f16_f32 v140, v194, v195
	v_lshlrev_b32_e32 v194, 16, v141
	v_and_b32_e32 v195, 0xffff0000, v141
	v_cvt_pk_f16_f32 v141, v194, v195
	v_lshlrev_b32_e32 v194, 16, v142
	v_and_b32_e32 v195, 0xffff0000, v142
	v_cvt_pk_f16_f32 v142, v194, v195
	v_lshlrev_b32_e32 v194, 16, v143
	v_and_b32_e32 v195, 0xffff0000, v143
	v_cvt_pk_f16_f32 v143, v194, v195
	v_lshlrev_b32_e32 v194, 16, v144
	v_and_b32_e32 v195, 0xffff0000, v144
	v_cvt_pk_f16_f32 v144, v194, v195
	v_lshlrev_b32_e32 v194, 16, v145
	v_and_b32_e32 v195, 0xffff0000, v145
	v_cvt_pk_f16_f32 v145, v194, v195
	v_cvt_scalef32_pk_f16_fp4 v198, v2, 1.0
	v_cvt_scalef32_pk_f16_fp4 v199, v6, 1.0
	v_cvt_scalef32_pk_f16_fp4 v200, v10, 1.0
	v_cvt_scalef32_pk_f16_fp4 v201, v14, 1.0
	v_dot2_f32_f16 v178, v198, v130, 0
	v_dot2_f32_f16 v179, v199, v130, 0
	v_dot2_f32_f16 v180, v200, v130, 0
	v_dot2_f32_f16 v181, v201, v130, 0
	v_cvt_scalef32_pk_f16_fp4 v198, v2, 1.0 op_sel:[1,0,0]
	v_cvt_scalef32_pk_f16_fp4 v199, v6, 1.0 op_sel:[1,0,0]
	v_cvt_scalef32_pk_f16_fp4 v200, v10, 1.0 op_sel:[1,0,0]
	v_cvt_scalef32_pk_f16_fp4 v201, v14, 1.0 op_sel:[1,0,0]
	v_dot2c_f32_f16_e32 v178, v198, v131
	v_dot2c_f32_f16_e32 v179, v199, v131
	v_dot2c_f32_f16_e32 v180, v200, v131
	v_dot2c_f32_f16_e32 v181, v201, v131
	v_cvt_scalef32_pk_f16_fp4 v198, v2, 1.0 op_sel:[0,1,0]
	v_cvt_scalef32_pk_f16_fp4 v199, v6, 1.0 op_sel:[0,1,0]
	v_cvt_scalef32_pk_f16_fp4 v200, v10, 1.0 op_sel:[0,1,0]
	v_cvt_scalef32_pk_f16_fp4 v201, v14, 1.0 op_sel:[0,1,0]
	v_dot2c_f32_f16_e32 v178, v198, v132
	v_dot2c_f32_f16_e32 v179, v199, v132
	v_dot2c_f32_f16_e32 v180, v200, v132
	v_dot2c_f32_f16_e32 v181, v201, v132
	v_cvt_scalef32_pk_f16_fp4 v198, v2, 1.0 op_sel:[1,1,0]
	v_cvt_scalef32_pk_f16_fp4 v199, v6, 1.0 op_sel:[1,1,0]
	v_cvt_scalef32_pk_f16_fp4 v200, v10, 1.0 op_sel:[1,1,0]
	v_cvt_scalef32_pk_f16_fp4 v201, v14, 1.0 op_sel:[1,1,0]
	v_dot2c_f32_f16_e32 v178, v198, v133
	v_dot2c_f32_f16_e32 v179, v199, v133
	v_dot2c_f32_f16_e32 v180, v200, v133
	v_dot2c_f32_f16_e32 v181, v201, v133
	v_cvt_scalef32_pk_f16_fp4 v198, v3, 1.0
	v_cvt_scalef32_pk_f16_fp4 v199, v7, 1.0
	v_cvt_scalef32_pk_f16_fp4 v200, v11, 1.0
	v_cvt_scalef32_pk_f16_fp4 v201, v15, 1.0
	v_dot2c_f32_f16_e32 v178, v198, v134
	v_dot2c_f32_f16_e32 v179, v199, v134
	v_dot2c_f32_f16_e32 v180, v200, v134
	v_dot2c_f32_f16_e32 v181, v201, v134
	v_cvt_scalef32_pk_f16_fp4 v198, v3, 1.0 op_sel:[1,0,0]
	v_cvt_scalef32_pk_f16_fp4 v199, v7, 1.0 op_sel:[1,0,0]
	v_cvt_scalef32_pk_f16_fp4 v200, v11, 1.0 op_sel:[1,0,0]
	v_cvt_scalef32_pk_f16_fp4 v201, v15, 1.0 op_sel:[1,0,0]
	v_dot2c_f32_f16_e32 v178, v198, v135
	v_dot2c_f32_f16_e32 v179, v199, v135
	v_dot2c_f32_f16_e32 v180, v200, v135
	v_dot2c_f32_f16_e32 v181, v201, v135
	v_cvt_scalef32_pk_f16_fp4 v198, v3, 1.0 op_sel:[0,1,0]
	v_cvt_scalef32_pk_f16_fp4 v199, v7, 1.0 op_sel:[0,1,0]
	v_cvt_scalef32_pk_f16_fp4 v200, v11, 1.0 op_sel:[0,1,0]
	v_cvt_scalef32_pk_f16_fp4 v201, v15, 1.0 op_sel:[0,1,0]
	v_dot2c_f32_f16_e32 v178, v198, v136
	v_dot2c_f32_f16_e32 v179, v199, v136
	v_dot2c_f32_f16_e32 v180, v200, v136
	v_dot2c_f32_f16_e32 v181, v201, v136
	v_cvt_scalef32_pk_f16_fp4 v198, v3, 1.0 op_sel:[1,1,0]
	v_cvt_scalef32_pk_f16_fp4 v199, v7, 1.0 op_sel:[1,1,0]
	v_cvt_scalef32_pk_f16_fp4 v200, v11, 1.0 op_sel:[1,1,0]
	v_cvt_scalef32_pk_f16_fp4 v201, v15, 1.0 op_sel:[1,1,0]
	v_dot2c_f32_f16_e32 v178, v198, v137
	v_dot2c_f32_f16_e32 v179, v199, v137
	v_dot2c_f32_f16_e32 v180, v200, v137
	v_dot2c_f32_f16_e32 v181, v201, v137
	v_cvt_scalef32_pk_f16_fp4 v198, v4, 1.0
	v_cvt_scalef32_pk_f16_fp4 v199, v8, 1.0
	v_cvt_scalef32_pk_f16_fp4 v200, v12, 1.0
	v_cvt_scalef32_pk_f16_fp4 v201, v16, 1.0
	v_dot2c_f32_f16_e32 v178, v198, v138
	v_dot2c_f32_f16_e32 v179, v199, v138
	v_dot2c_f32_f16_e32 v180, v200, v138
	v_dot2c_f32_f16_e32 v181, v201, v138
	v_cvt_scalef32_pk_f16_fp4 v198, v4, 1.0 op_sel:[1,0,0]
	v_cvt_scalef32_pk_f16_fp4 v199, v8, 1.0 op_sel:[1,0,0]
	v_cvt_scalef32_pk_f16_fp4 v200, v12, 1.0 op_sel:[1,0,0]
	v_cvt_scalef32_pk_f16_fp4 v201, v16, 1.0 op_sel:[1,0,0]
	v_dot2c_f32_f16_e32 v178, v198, v139
	v_dot2c_f32_f16_e32 v179, v199, v139
	v_dot2c_f32_f16_e32 v180, v200, v139
	v_dot2c_f32_f16_e32 v181, v201, v139
	v_cvt_scalef32_pk_f16_fp4 v198, v4, 1.0 op_sel:[0,1,0]
	v_cvt_scalef32_pk_f16_fp4 v199, v8, 1.0 op_sel:[0,1,0]
	v_cvt_scalef32_pk_f16_fp4 v200, v12, 1.0 op_sel:[0,1,0]
	v_cvt_scalef32_pk_f16_fp4 v201, v16, 1.0 op_sel:[0,1,0]
	v_dot2c_f32_f16_e32 v178, v198, v140
	v_dot2c_f32_f16_e32 v179, v199, v140
	v_dot2c_f32_f16_e32 v180, v200, v140
	v_dot2c_f32_f16_e32 v181, v201, v140
	v_cvt_scalef32_pk_f16_fp4 v198, v4, 1.0 op_sel:[1,1,0]
	v_cvt_scalef32_pk_f16_fp4 v199, v8, 1.0 op_sel:[1,1,0]
	v_cvt_scalef32_pk_f16_fp4 v200, v12, 1.0 op_sel:[1,1,0]
	v_cvt_scalef32_pk_f16_fp4 v201, v16, 1.0 op_sel:[1,1,0]
	v_dot2c_f32_f16_e32 v178, v198, v141
	v_dot2c_f32_f16_e32 v179, v199, v141
	v_dot2c_f32_f16_e32 v180, v200, v141
	v_dot2c_f32_f16_e32 v181, v201, v141
	v_cvt_scalef32_pk_f16_fp4 v198, v5, 1.0
	v_cvt_scalef32_pk_f16_fp4 v199, v9, 1.0
	v_cvt_scalef32_pk_f16_fp4 v200, v13, 1.0
	v_cvt_scalef32_pk_f16_fp4 v201, v17, 1.0
	v_dot2c_f32_f16_e32 v178, v198, v142
	v_dot2c_f32_f16_e32 v179, v199, v142
	v_dot2c_f32_f16_e32 v180, v200, v142
	v_dot2c_f32_f16_e32 v181, v201, v142
	v_cvt_scalef32_pk_f16_fp4 v198, v5, 1.0 op_sel:[1,0,0]
	v_cvt_scalef32_pk_f16_fp4 v199, v9, 1.0 op_sel:[1,0,0]
	v_cvt_scalef32_pk_f16_fp4 v200, v13, 1.0 op_sel:[1,0,0]
	v_cvt_scalef32_pk_f16_fp4 v201, v17, 1.0 op_sel:[1,0,0]
	v_dot2c_f32_f16_e32 v178, v198, v143
	v_dot2c_f32_f16_e32 v179, v199, v143
	v_dot2c_f32_f16_e32 v180, v200, v143
	v_dot2c_f32_f16_e32 v181, v201, v143
	v_cvt_scalef32_pk_f16_fp4 v198, v5, 1.0 op_sel:[0,1,0]
	v_cvt_scalef32_pk_f16_fp4 v199, v9, 1.0 op_sel:[0,1,0]
	v_cvt_scalef32_pk_f16_fp4 v200, v13, 1.0 op_sel:[0,1,0]
	v_cvt_scalef32_pk_f16_fp4 v201, v17, 1.0 op_sel:[0,1,0]
	v_dot2c_f32_f16_e32 v178, v198, v144
	v_dot2c_f32_f16_e32 v179, v199, v144
	v_dot2c_f32_f16_e32 v180, v200, v144
	v_dot2c_f32_f16_e32 v181, v201, v144
	v_cvt_scalef32_pk_f16_fp4 v198, v5, 1.0 op_sel:[1,1,0]
	v_cvt_scalef32_pk_f16_fp4 v199, v9, 1.0 op_sel:[1,1,0]
	v_cvt_scalef32_pk_f16_fp4 v200, v13, 1.0 op_sel:[1,1,0]
	v_cvt_scalef32_pk_f16_fp4 v201, v17, 1.0 op_sel:[1,1,0]
	v_dot2c_f32_f16_e32 v178, v198, v145
	v_dot2c_f32_f16_e32 v179, v199, v145
	v_dot2c_f32_f16_e32 v180, v200, v145
	v_dot2c_f32_f16_e32 v181, v201, v145
	v_cvt_scalef32_pk_f16_fp4 v198, v18, 1.0
	v_cvt_scalef32_pk_f16_fp4 v199, v22, 1.0
	v_cvt_scalef32_pk_f16_fp4 v200, v26, 1.0
	v_cvt_scalef32_pk_f16_fp4 v201, v30, 1.0
	v_dot2_f32_f16 v182, v198, v130, 0
	v_dot2_f32_f16 v183, v199, v130, 0
	v_dot2_f32_f16 v184, v200, v130, 0
	v_dot2_f32_f16 v185, v201, v130, 0
	v_cvt_scalef32_pk_f16_fp4 v198, v18, 1.0 op_sel:[1,0,0]
	v_cvt_scalef32_pk_f16_fp4 v199, v22, 1.0 op_sel:[1,0,0]
	v_cvt_scalef32_pk_f16_fp4 v200, v26, 1.0 op_sel:[1,0,0]
	v_cvt_scalef32_pk_f16_fp4 v201, v30, 1.0 op_sel:[1,0,0]
	v_dot2c_f32_f16_e32 v182, v198, v131
	v_dot2c_f32_f16_e32 v183, v199, v131
	v_dot2c_f32_f16_e32 v184, v200, v131
	v_dot2c_f32_f16_e32 v185, v201, v131
	v_cvt_scalef32_pk_f16_fp4 v198, v18, 1.0 op_sel:[0,1,0]
	v_cvt_scalef32_pk_f16_fp4 v199, v22, 1.0 op_sel:[0,1,0]
	v_cvt_scalef32_pk_f16_fp4 v200, v26, 1.0 op_sel:[0,1,0]
	v_cvt_scalef32_pk_f16_fp4 v201, v30, 1.0 op_sel:[0,1,0]
	v_dot2c_f32_f16_e32 v182, v198, v132
	v_dot2c_f32_f16_e32 v183, v199, v132
	v_dot2c_f32_f16_e32 v184, v200, v132
	v_dot2c_f32_f16_e32 v185, v201, v132
	v_cvt_scalef32_pk_f16_fp4 v198, v18, 1.0 op_sel:[1,1,0]
	v_cvt_scalef32_pk_f16_fp4 v199, v22, 1.0 op_sel:[1,1,0]
	v_cvt_scalef32_pk_f16_fp4 v200, v26, 1.0 op_sel:[1,1,0]
	v_cvt_scalef32_pk_f16_fp4 v201, v30, 1.0 op_sel:[1,1,0]
	v_dot2c_f32_f16_e32 v182, v198, v133
	v_dot2c_f32_f16_e32 v183, v199, v133
	v_dot2c_f32_f16_e32 v184, v200, v133
	v_dot2c_f32_f16_e32 v185, v201, v133
	v_cvt_scalef32_pk_f16_fp4 v198, v19, 1.0
	v_cvt_scalef32_pk_f16_fp4 v199, v23, 1.0
	v_cvt_scalef32_pk_f16_fp4 v200, v27, 1.0
	v_cvt_scalef32_pk_f16_fp4 v201, v31, 1.0
	v_dot2c_f32_f16_e32 v182, v198, v134
	v_dot2c_f32_f16_e32 v183, v199, v134
	v_dot2c_f32_f16_e32 v184, v200, v134
	v_dot2c_f32_f16_e32 v185, v201, v134
	v_cvt_scalef32_pk_f16_fp4 v198, v19, 1.0 op_sel:[1,0,0]
	v_cvt_scalef32_pk_f16_fp4 v199, v23, 1.0 op_sel:[1,0,0]
	v_cvt_scalef32_pk_f16_fp4 v200, v27, 1.0 op_sel:[1,0,0]
	v_cvt_scalef32_pk_f16_fp4 v201, v31, 1.0 op_sel:[1,0,0]
	v_dot2c_f32_f16_e32 v182, v198, v135
	v_dot2c_f32_f16_e32 v183, v199, v135
	v_dot2c_f32_f16_e32 v184, v200, v135
	v_dot2c_f32_f16_e32 v185, v201, v135
	v_cvt_scalef32_pk_f16_fp4 v198, v19, 1.0 op_sel:[0,1,0]
	v_cvt_scalef32_pk_f16_fp4 v199, v23, 1.0 op_sel:[0,1,0]
	v_cvt_scalef32_pk_f16_fp4 v200, v27, 1.0 op_sel:[0,1,0]
	v_cvt_scalef32_pk_f16_fp4 v201, v31, 1.0 op_sel:[0,1,0]
	v_dot2c_f32_f16_e32 v182, v198, v136
	v_dot2c_f32_f16_e32 v183, v199, v136
	v_dot2c_f32_f16_e32 v184, v200, v136
	v_dot2c_f32_f16_e32 v185, v201, v136
	v_cvt_scalef32_pk_f16_fp4 v198, v19, 1.0 op_sel:[1,1,0]
	v_cvt_scalef32_pk_f16_fp4 v199, v23, 1.0 op_sel:[1,1,0]
	v_cvt_scalef32_pk_f16_fp4 v200, v27, 1.0 op_sel:[1,1,0]
	v_cvt_scalef32_pk_f16_fp4 v201, v31, 1.0 op_sel:[1,1,0]
	v_dot2c_f32_f16_e32 v182, v198, v137
	v_dot2c_f32_f16_e32 v183, v199, v137
	v_dot2c_f32_f16_e32 v184, v200, v137
	v_dot2c_f32_f16_e32 v185, v201, v137
	v_cvt_scalef32_pk_f16_fp4 v198, v20, 1.0
	v_cvt_scalef32_pk_f16_fp4 v199, v24, 1.0
	v_cvt_scalef32_pk_f16_fp4 v200, v28, 1.0
	v_cvt_scalef32_pk_f16_fp4 v201, v32, 1.0
	v_dot2c_f32_f16_e32 v182, v198, v138
	v_dot2c_f32_f16_e32 v183, v199, v138
	v_dot2c_f32_f16_e32 v184, v200, v138
	v_dot2c_f32_f16_e32 v185, v201, v138
	v_cvt_scalef32_pk_f16_fp4 v198, v20, 1.0 op_sel:[1,0,0]
	v_cvt_scalef32_pk_f16_fp4 v199, v24, 1.0 op_sel:[1,0,0]
	v_cvt_scalef32_pk_f16_fp4 v200, v28, 1.0 op_sel:[1,0,0]
	v_cvt_scalef32_pk_f16_fp4 v201, v32, 1.0 op_sel:[1,0,0]
	v_dot2c_f32_f16_e32 v182, v198, v139
	v_dot2c_f32_f16_e32 v183, v199, v139
	v_dot2c_f32_f16_e32 v184, v200, v139
	v_dot2c_f32_f16_e32 v185, v201, v139
	v_cvt_scalef32_pk_f16_fp4 v198, v20, 1.0 op_sel:[0,1,0]
	v_cvt_scalef32_pk_f16_fp4 v199, v24, 1.0 op_sel:[0,1,0]
	v_cvt_scalef32_pk_f16_fp4 v200, v28, 1.0 op_sel:[0,1,0]
	v_cvt_scalef32_pk_f16_fp4 v201, v32, 1.0 op_sel:[0,1,0]
	v_dot2c_f32_f16_e32 v182, v198, v140
	v_dot2c_f32_f16_e32 v183, v199, v140
	v_dot2c_f32_f16_e32 v184, v200, v140
	v_dot2c_f32_f16_e32 v185, v201, v140
	v_cvt_scalef32_pk_f16_fp4 v198, v20, 1.0 op_sel:[1,1,0]
	v_cvt_scalef32_pk_f16_fp4 v199, v24, 1.0 op_sel:[1,1,0]
	v_cvt_scalef32_pk_f16_fp4 v200, v28, 1.0 op_sel:[1,1,0]
	v_cvt_scalef32_pk_f16_fp4 v201, v32, 1.0 op_sel:[1,1,0]
	v_dot2c_f32_f16_e32 v182, v198, v141
	v_dot2c_f32_f16_e32 v183, v199, v141
	v_dot2c_f32_f16_e32 v184, v200, v141
	v_dot2c_f32_f16_e32 v185, v201, v141
	v_cvt_scalef32_pk_f16_fp4 v198, v21, 1.0
	v_cvt_scalef32_pk_f16_fp4 v199, v25, 1.0
	v_cvt_scalef32_pk_f16_fp4 v200, v29, 1.0
	v_cvt_scalef32_pk_f16_fp4 v201, v33, 1.0
	v_dot2c_f32_f16_e32 v182, v198, v142
	v_dot2c_f32_f16_e32 v183, v199, v142
	v_dot2c_f32_f16_e32 v184, v200, v142
	v_dot2c_f32_f16_e32 v185, v201, v142
	v_cvt_scalef32_pk_f16_fp4 v198, v21, 1.0 op_sel:[1,0,0]
	v_cvt_scalef32_pk_f16_fp4 v199, v25, 1.0 op_sel:[1,0,0]
	v_cvt_scalef32_pk_f16_fp4 v200, v29, 1.0 op_sel:[1,0,0]
	v_cvt_scalef32_pk_f16_fp4 v201, v33, 1.0 op_sel:[1,0,0]
	v_dot2c_f32_f16_e32 v182, v198, v143
	v_dot2c_f32_f16_e32 v183, v199, v143
	v_dot2c_f32_f16_e32 v184, v200, v143
	v_dot2c_f32_f16_e32 v185, v201, v143
	v_cvt_scalef32_pk_f16_fp4 v198, v21, 1.0 op_sel:[0,1,0]
	v_cvt_scalef32_pk_f16_fp4 v199, v25, 1.0 op_sel:[0,1,0]
	v_cvt_scalef32_pk_f16_fp4 v200, v29, 1.0 op_sel:[0,1,0]
	v_cvt_scalef32_pk_f16_fp4 v201, v33, 1.0 op_sel:[0,1,0]
	v_dot2c_f32_f16_e32 v182, v198, v144
	v_dot2c_f32_f16_e32 v183, v199, v144
	v_dot2c_f32_f16_e32 v184, v200, v144
	v_dot2c_f32_f16_e32 v185, v201, v144
	v_cvt_scalef32_pk_f16_fp4 v198, v21, 1.0 op_sel:[1,1,0]
	v_cvt_scalef32_pk_f16_fp4 v199, v25, 1.0 op_sel:[1,1,0]
	v_cvt_scalef32_pk_f16_fp4 v200, v29, 1.0 op_sel:[1,1,0]
	v_cvt_scalef32_pk_f16_fp4 v201, v33, 1.0 op_sel:[1,1,0]
	v_dot2c_f32_f16_e32 v182, v198, v145
	v_dot2c_f32_f16_e32 v183, v199, v145
	v_dot2c_f32_f16_e32 v184, v200, v145
	v_dot2c_f32_f16_e32 v185, v201, v145
	v_cvt_scalef32_pk_f16_fp4 v198, v34, 1.0
	v_cvt_scalef32_pk_f16_fp4 v199, v38, 1.0
	v_cvt_scalef32_pk_f16_fp4 v200, v42, 1.0
	v_cvt_scalef32_pk_f16_fp4 v201, v46, 1.0
	v_dot2_f32_f16 v186, v198, v130, 0
	v_dot2_f32_f16 v187, v199, v130, 0
	v_dot2_f32_f16 v188, v200, v130, 0
	v_dot2_f32_f16 v189, v201, v130, 0
	v_cvt_scalef32_pk_f16_fp4 v198, v34, 1.0 op_sel:[1,0,0]
	v_cvt_scalef32_pk_f16_fp4 v199, v38, 1.0 op_sel:[1,0,0]
	v_cvt_scalef32_pk_f16_fp4 v200, v42, 1.0 op_sel:[1,0,0]
	v_cvt_scalef32_pk_f16_fp4 v201, v46, 1.0 op_sel:[1,0,0]
	v_dot2c_f32_f16_e32 v186, v198, v131
	v_dot2c_f32_f16_e32 v187, v199, v131
	v_dot2c_f32_f16_e32 v188, v200, v131
	v_dot2c_f32_f16_e32 v189, v201, v131
	v_cvt_scalef32_pk_f16_fp4 v198, v34, 1.0 op_sel:[0,1,0]
	v_cvt_scalef32_pk_f16_fp4 v199, v38, 1.0 op_sel:[0,1,0]
	v_cvt_scalef32_pk_f16_fp4 v200, v42, 1.0 op_sel:[0,1,0]
	v_cvt_scalef32_pk_f16_fp4 v201, v46, 1.0 op_sel:[0,1,0]
	v_dot2c_f32_f16_e32 v186, v198, v132
	v_dot2c_f32_f16_e32 v187, v199, v132
	v_dot2c_f32_f16_e32 v188, v200, v132
	v_dot2c_f32_f16_e32 v189, v201, v132
	v_cvt_scalef32_pk_f16_fp4 v198, v34, 1.0 op_sel:[1,1,0]
	v_cvt_scalef32_pk_f16_fp4 v199, v38, 1.0 op_sel:[1,1,0]
	v_cvt_scalef32_pk_f16_fp4 v200, v42, 1.0 op_sel:[1,1,0]
	v_cvt_scalef32_pk_f16_fp4 v201, v46, 1.0 op_sel:[1,1,0]
	v_dot2c_f32_f16_e32 v186, v198, v133
	v_dot2c_f32_f16_e32 v187, v199, v133
	v_dot2c_f32_f16_e32 v188, v200, v133
	v_dot2c_f32_f16_e32 v189, v201, v133
	v_cvt_scalef32_pk_f16_fp4 v198, v35, 1.0
	v_cvt_scalef32_pk_f16_fp4 v199, v39, 1.0
	v_cvt_scalef32_pk_f16_fp4 v200, v43, 1.0
	v_cvt_scalef32_pk_f16_fp4 v201, v47, 1.0
	v_dot2c_f32_f16_e32 v186, v198, v134
	v_dot2c_f32_f16_e32 v187, v199, v134
	v_dot2c_f32_f16_e32 v188, v200, v134
	v_dot2c_f32_f16_e32 v189, v201, v134
	v_cvt_scalef32_pk_f16_fp4 v198, v35, 1.0 op_sel:[1,0,0]
	v_cvt_scalef32_pk_f16_fp4 v199, v39, 1.0 op_sel:[1,0,0]
	v_cvt_scalef32_pk_f16_fp4 v200, v43, 1.0 op_sel:[1,0,0]
	v_cvt_scalef32_pk_f16_fp4 v201, v47, 1.0 op_sel:[1,0,0]
	v_dot2c_f32_f16_e32 v186, v198, v135
	v_dot2c_f32_f16_e32 v187, v199, v135
	v_dot2c_f32_f16_e32 v188, v200, v135
	v_dot2c_f32_f16_e32 v189, v201, v135
	v_cvt_scalef32_pk_f16_fp4 v198, v35, 1.0 op_sel:[0,1,0]
	v_cvt_scalef32_pk_f16_fp4 v199, v39, 1.0 op_sel:[0,1,0]
	v_cvt_scalef32_pk_f16_fp4 v200, v43, 1.0 op_sel:[0,1,0]
	v_cvt_scalef32_pk_f16_fp4 v201, v47, 1.0 op_sel:[0,1,0]
	v_dot2c_f32_f16_e32 v186, v198, v136
	v_dot2c_f32_f16_e32 v187, v199, v136
	v_dot2c_f32_f16_e32 v188, v200, v136
	v_dot2c_f32_f16_e32 v189, v201, v136
	v_cvt_scalef32_pk_f16_fp4 v198, v35, 1.0 op_sel:[1,1,0]
	v_cvt_scalef32_pk_f16_fp4 v199, v39, 1.0 op_sel:[1,1,0]
	v_cvt_scalef32_pk_f16_fp4 v200, v43, 1.0 op_sel:[1,1,0]
	v_cvt_scalef32_pk_f16_fp4 v201, v47, 1.0 op_sel:[1,1,0]
	v_dot2c_f32_f16_e32 v186, v198, v137
	v_dot2c_f32_f16_e32 v187, v199, v137
	v_dot2c_f32_f16_e32 v188, v200, v137
	v_dot2c_f32_f16_e32 v189, v201, v137
	v_cvt_scalef32_pk_f16_fp4 v198, v36, 1.0
	v_cvt_scalef32_pk_f16_fp4 v199, v40, 1.0
	v_cvt_scalef32_pk_f16_fp4 v200, v44, 1.0
	v_cvt_scalef32_pk_f16_fp4 v201, v48, 1.0
	v_dot2c_f32_f16_e32 v186, v198, v138
	v_dot2c_f32_f16_e32 v187, v199, v138
	v_dot2c_f32_f16_e32 v188, v200, v138
	v_dot2c_f32_f16_e32 v189, v201, v138
	v_cvt_scalef32_pk_f16_fp4 v198, v36, 1.0 op_sel:[1,0,0]
	v_cvt_scalef32_pk_f16_fp4 v199, v40, 1.0 op_sel:[1,0,0]
	v_cvt_scalef32_pk_f16_fp4 v200, v44, 1.0 op_sel:[1,0,0]
	v_cvt_scalef32_pk_f16_fp4 v201, v48, 1.0 op_sel:[1,0,0]
	v_dot2c_f32_f16_e32 v186, v198, v139
	v_dot2c_f32_f16_e32 v187, v199, v139
	v_dot2c_f32_f16_e32 v188, v200, v139
	v_dot2c_f32_f16_e32 v189, v201, v139
	v_cvt_scalef32_pk_f16_fp4 v198, v36, 1.0 op_sel:[0,1,0]
	v_cvt_scalef32_pk_f16_fp4 v199, v40, 1.0 op_sel:[0,1,0]
	v_cvt_scalef32_pk_f16_fp4 v200, v44, 1.0 op_sel:[0,1,0]
	v_cvt_scalef32_pk_f16_fp4 v201, v48, 1.0 op_sel:[0,1,0]
	v_dot2c_f32_f16_e32 v186, v198, v140
	v_dot2c_f32_f16_e32 v187, v199, v140
	v_dot2c_f32_f16_e32 v188, v200, v140
	v_dot2c_f32_f16_e32 v189, v201, v140
	v_cvt_scalef32_pk_f16_fp4 v198, v36, 1.0 op_sel:[1,1,0]
	v_cvt_scalef32_pk_f16_fp4 v199, v40, 1.0 op_sel:[1,1,0]
	v_cvt_scalef32_pk_f16_fp4 v200, v44, 1.0 op_sel:[1,1,0]
	v_cvt_scalef32_pk_f16_fp4 v201, v48, 1.0 op_sel:[1,1,0]
	v_dot2c_f32_f16_e32 v186, v198, v141
	v_dot2c_f32_f16_e32 v187, v199, v141
	v_dot2c_f32_f16_e32 v188, v200, v141
	v_dot2c_f32_f16_e32 v189, v201, v141
	v_cvt_scalef32_pk_f16_fp4 v198, v37, 1.0
	v_cvt_scalef32_pk_f16_fp4 v199, v41, 1.0
	v_cvt_scalef32_pk_f16_fp4 v200, v45, 1.0
	v_cvt_scalef32_pk_f16_fp4 v201, v49, 1.0
	v_dot2c_f32_f16_e32 v186, v198, v142
	v_dot2c_f32_f16_e32 v187, v199, v142
	v_dot2c_f32_f16_e32 v188, v200, v142
	v_dot2c_f32_f16_e32 v189, v201, v142
	v_cvt_scalef32_pk_f16_fp4 v198, v37, 1.0 op_sel:[1,0,0]
	v_cvt_scalef32_pk_f16_fp4 v199, v41, 1.0 op_sel:[1,0,0]
	v_cvt_scalef32_pk_f16_fp4 v200, v45, 1.0 op_sel:[1,0,0]
	v_cvt_scalef32_pk_f16_fp4 v201, v49, 1.0 op_sel:[1,0,0]
	v_dot2c_f32_f16_e32 v186, v198, v143
	v_dot2c_f32_f16_e32 v187, v199, v143
	v_dot2c_f32_f16_e32 v188, v200, v143
	v_dot2c_f32_f16_e32 v189, v201, v143
	v_cvt_scalef32_pk_f16_fp4 v198, v37, 1.0 op_sel:[0,1,0]
	v_cvt_scalef32_pk_f16_fp4 v199, v41, 1.0 op_sel:[0,1,0]
	v_cvt_scalef32_pk_f16_fp4 v200, v45, 1.0 op_sel:[0,1,0]
	v_cvt_scalef32_pk_f16_fp4 v201, v49, 1.0 op_sel:[0,1,0]
	v_dot2c_f32_f16_e32 v186, v198, v144
	v_dot2c_f32_f16_e32 v187, v199, v144
	v_dot2c_f32_f16_e32 v188, v200, v144
	v_dot2c_f32_f16_e32 v189, v201, v144
	v_cvt_scalef32_pk_f16_fp4 v198, v37, 1.0 op_sel:[1,1,0]
	v_cvt_scalef32_pk_f16_fp4 v199, v41, 1.0 op_sel:[1,1,0]
	v_cvt_scalef32_pk_f16_fp4 v200, v45, 1.0 op_sel:[1,1,0]
	v_cvt_scalef32_pk_f16_fp4 v201, v49, 1.0 op_sel:[1,1,0]
	v_dot2c_f32_f16_e32 v186, v198, v145
	v_dot2c_f32_f16_e32 v187, v199, v145
	v_dot2c_f32_f16_e32 v188, v200, v145
	v_dot2c_f32_f16_e32 v189, v201, v145
	v_cvt_scalef32_pk_f16_fp4 v198, v50, 1.0
	v_cvt_scalef32_pk_f16_fp4 v199, v54, 1.0
	v_cvt_scalef32_pk_f16_fp4 v200, v58, 1.0
	v_cvt_scalef32_pk_f16_fp4 v201, v62, 1.0
	v_dot2_f32_f16 v190, v198, v130, 0
	v_dot2_f32_f16 v191, v199, v130, 0
	v_dot2_f32_f16 v192, v200, v130, 0
	v_dot2_f32_f16 v193, v201, v130, 0
	v_cvt_scalef32_pk_f16_fp4 v198, v50, 1.0 op_sel:[1,0,0]
	v_cvt_scalef32_pk_f16_fp4 v199, v54, 1.0 op_sel:[1,0,0]
	v_cvt_scalef32_pk_f16_fp4 v200, v58, 1.0 op_sel:[1,0,0]
	v_cvt_scalef32_pk_f16_fp4 v201, v62, 1.0 op_sel:[1,0,0]
	v_dot2c_f32_f16_e32 v190, v198, v131
	v_dot2c_f32_f16_e32 v191, v199, v131
	v_dot2c_f32_f16_e32 v192, v200, v131
	v_dot2c_f32_f16_e32 v193, v201, v131
	v_cvt_scalef32_pk_f16_fp4 v198, v50, 1.0 op_sel:[0,1,0]
	v_cvt_scalef32_pk_f16_fp4 v199, v54, 1.0 op_sel:[0,1,0]
	v_cvt_scalef32_pk_f16_fp4 v200, v58, 1.0 op_sel:[0,1,0]
	v_cvt_scalef32_pk_f16_fp4 v201, v62, 1.0 op_sel:[0,1,0]
	v_dot2c_f32_f16_e32 v190, v198, v132
	v_dot2c_f32_f16_e32 v191, v199, v132
	v_dot2c_f32_f16_e32 v192, v200, v132
	v_dot2c_f32_f16_e32 v193, v201, v132
	v_cvt_scalef32_pk_f16_fp4 v198, v50, 1.0 op_sel:[1,1,0]
	v_cvt_scalef32_pk_f16_fp4 v199, v54, 1.0 op_sel:[1,1,0]
	v_cvt_scalef32_pk_f16_fp4 v200, v58, 1.0 op_sel:[1,1,0]
	v_cvt_scalef32_pk_f16_fp4 v201, v62, 1.0 op_sel:[1,1,0]
	v_dot2c_f32_f16_e32 v190, v198, v133
	v_dot2c_f32_f16_e32 v191, v199, v133
	v_dot2c_f32_f16_e32 v192, v200, v133
	v_dot2c_f32_f16_e32 v193, v201, v133
	v_cvt_scalef32_pk_f16_fp4 v198, v51, 1.0
	v_cvt_scalef32_pk_f16_fp4 v199, v55, 1.0
	v_cvt_scalef32_pk_f16_fp4 v200, v59, 1.0
	v_cvt_scalef32_pk_f16_fp4 v201, v63, 1.0
	v_dot2c_f32_f16_e32 v190, v198, v134
	v_dot2c_f32_f16_e32 v191, v199, v134
	v_dot2c_f32_f16_e32 v192, v200, v134
	v_dot2c_f32_f16_e32 v193, v201, v134
	v_cvt_scalef32_pk_f16_fp4 v198, v51, 1.0 op_sel:[1,0,0]
	v_cvt_scalef32_pk_f16_fp4 v199, v55, 1.0 op_sel:[1,0,0]
	v_cvt_scalef32_pk_f16_fp4 v200, v59, 1.0 op_sel:[1,0,0]
	v_cvt_scalef32_pk_f16_fp4 v201, v63, 1.0 op_sel:[1,0,0]
	v_dot2c_f32_f16_e32 v190, v198, v135
	v_dot2c_f32_f16_e32 v191, v199, v135
	v_dot2c_f32_f16_e32 v192, v200, v135
	v_dot2c_f32_f16_e32 v193, v201, v135
	v_cvt_scalef32_pk_f16_fp4 v198, v51, 1.0 op_sel:[0,1,0]
	v_cvt_scalef32_pk_f16_fp4 v199, v55, 1.0 op_sel:[0,1,0]
	v_cvt_scalef32_pk_f16_fp4 v200, v59, 1.0 op_sel:[0,1,0]
	v_cvt_scalef32_pk_f16_fp4 v201, v63, 1.0 op_sel:[0,1,0]
	v_dot2c_f32_f16_e32 v190, v198, v136
	v_dot2c_f32_f16_e32 v191, v199, v136
	v_dot2c_f32_f16_e32 v192, v200, v136
	v_dot2c_f32_f16_e32 v193, v201, v136
	v_cvt_scalef32_pk_f16_fp4 v198, v51, 1.0 op_sel:[1,1,0]
	v_cvt_scalef32_pk_f16_fp4 v199, v55, 1.0 op_sel:[1,1,0]
	v_cvt_scalef32_pk_f16_fp4 v200, v59, 1.0 op_sel:[1,1,0]
	v_cvt_scalef32_pk_f16_fp4 v201, v63, 1.0 op_sel:[1,1,0]
	v_dot2c_f32_f16_e32 v190, v198, v137
	v_dot2c_f32_f16_e32 v191, v199, v137
	v_dot2c_f32_f16_e32 v192, v200, v137
	v_dot2c_f32_f16_e32 v193, v201, v137
	v_cvt_scalef32_pk_f16_fp4 v198, v52, 1.0
	v_cvt_scalef32_pk_f16_fp4 v199, v56, 1.0
	v_cvt_scalef32_pk_f16_fp4 v200, v60, 1.0
	v_cvt_scalef32_pk_f16_fp4 v201, v64, 1.0
	v_dot2c_f32_f16_e32 v190, v198, v138
	v_dot2c_f32_f16_e32 v191, v199, v138
	v_dot2c_f32_f16_e32 v192, v200, v138
	v_dot2c_f32_f16_e32 v193, v201, v138
	v_cvt_scalef32_pk_f16_fp4 v198, v52, 1.0 op_sel:[1,0,0]
	v_cvt_scalef32_pk_f16_fp4 v199, v56, 1.0 op_sel:[1,0,0]
	v_cvt_scalef32_pk_f16_fp4 v200, v60, 1.0 op_sel:[1,0,0]
	v_cvt_scalef32_pk_f16_fp4 v201, v64, 1.0 op_sel:[1,0,0]
	v_dot2c_f32_f16_e32 v190, v198, v139
	v_dot2c_f32_f16_e32 v191, v199, v139
	v_dot2c_f32_f16_e32 v192, v200, v139
	v_dot2c_f32_f16_e32 v193, v201, v139
	v_cvt_scalef32_pk_f16_fp4 v198, v52, 1.0 op_sel:[0,1,0]
	v_cvt_scalef32_pk_f16_fp4 v199, v56, 1.0 op_sel:[0,1,0]
	v_cvt_scalef32_pk_f16_fp4 v200, v60, 1.0 op_sel:[0,1,0]
	v_cvt_scalef32_pk_f16_fp4 v201, v64, 1.0 op_sel:[0,1,0]
	v_dot2c_f32_f16_e32 v190, v198, v140
	v_dot2c_f32_f16_e32 v191, v199, v140
	v_dot2c_f32_f16_e32 v192, v200, v140
	v_dot2c_f32_f16_e32 v193, v201, v140
	v_cvt_scalef32_pk_f16_fp4 v198, v52, 1.0 op_sel:[1,1,0]
	v_cvt_scalef32_pk_f16_fp4 v199, v56, 1.0 op_sel:[1,1,0]
	v_cvt_scalef32_pk_f16_fp4 v200, v60, 1.0 op_sel:[1,1,0]
	v_cvt_scalef32_pk_f16_fp4 v201, v64, 1.0 op_sel:[1,1,0]
	v_dot2c_f32_f16_e32 v190, v198, v141
	v_dot2c_f32_f16_e32 v191, v199, v141
	v_dot2c_f32_f16_e32 v192, v200, v141
	v_dot2c_f32_f16_e32 v193, v201, v141
	v_cvt_scalef32_pk_f16_fp4 v198, v53, 1.0
	v_cvt_scalef32_pk_f16_fp4 v199, v57, 1.0
	v_cvt_scalef32_pk_f16_fp4 v200, v61, 1.0
	v_cvt_scalef32_pk_f16_fp4 v201, v65, 1.0
	v_dot2c_f32_f16_e32 v190, v198, v142
	v_dot2c_f32_f16_e32 v191, v199, v142
	v_dot2c_f32_f16_e32 v192, v200, v142
	v_dot2c_f32_f16_e32 v193, v201, v142
	v_cvt_scalef32_pk_f16_fp4 v198, v53, 1.0 op_sel:[1,0,0]
	v_cvt_scalef32_pk_f16_fp4 v199, v57, 1.0 op_sel:[1,0,0]
	v_cvt_scalef32_pk_f16_fp4 v200, v61, 1.0 op_sel:[1,0,0]
	v_cvt_scalef32_pk_f16_fp4 v201, v65, 1.0 op_sel:[1,0,0]
	v_dot2c_f32_f16_e32 v190, v198, v143
	v_dot2c_f32_f16_e32 v191, v199, v143
	v_dot2c_f32_f16_e32 v192, v200, v143
	v_dot2c_f32_f16_e32 v193, v201, v143
	v_cvt_scalef32_pk_f16_fp4 v198, v53, 1.0 op_sel:[0,1,0]
	v_cvt_scalef32_pk_f16_fp4 v199, v57, 1.0 op_sel:[0,1,0]
	v_cvt_scalef32_pk_f16_fp4 v200, v61, 1.0 op_sel:[0,1,0]
	v_cvt_scalef32_pk_f16_fp4 v201, v65, 1.0 op_sel:[0,1,0]
	v_dot2c_f32_f16_e32 v190, v198, v144
	v_dot2c_f32_f16_e32 v191, v199, v144
	v_dot2c_f32_f16_e32 v192, v200, v144
	v_dot2c_f32_f16_e32 v193, v201, v144
	v_cvt_scalef32_pk_f16_fp4 v198, v53, 1.0 op_sel:[1,1,0]
	v_cvt_scalef32_pk_f16_fp4 v199, v57, 1.0 op_sel:[1,1,0]
	v_cvt_scalef32_pk_f16_fp4 v200, v61, 1.0 op_sel:[1,1,0]
	v_cvt_scalef32_pk_f16_fp4 v201, v65, 1.0 op_sel:[1,1,0]
	v_dot2c_f32_f16_e32 v190, v198, v145
	v_dot2c_f32_f16_e32 v191, v199, v145
	v_dot2c_f32_f16_e32 v192, v200, v145
	v_dot2c_f32_f16_e32 v193, v201, v145
	s_nop 3
	v_cndmask_b32_e64 v194, v178, v186, s[38:39]
	v_cndmask_b32_e64 v233, v186, v178, s[38:39]
	v_cndmask_b32_e64 v195, v179, v187, s[38:39]
	v_cndmask_b32_e64 v234, v187, v179, s[38:39]
	v_cndmask_b32_e64 v196, v180, v188, s[38:39]
	v_cndmask_b32_e64 v235, v188, v180, s[38:39]
	v_cndmask_b32_e64 v197, v181, v189, s[38:39]
	v_cndmask_b32_e64 v236, v189, v181, s[38:39]
	v_cndmask_b32_e64 v198, v182, v190, s[38:39]
	v_cndmask_b32_e64 v237, v190, v182, s[38:39]
	v_cndmask_b32_e64 v199, v183, v191, s[38:39]
	v_cndmask_b32_e64 v238, v191, v183, s[38:39]
	v_cndmask_b32_e64 v200, v184, v192, s[38:39]
	v_cndmask_b32_e64 v239, v192, v184, s[38:39]
	v_cndmask_b32_e64 v201, v185, v193, s[38:39]
	v_cndmask_b32_e64 v240, v193, v185, s[38:39]
	v_add_f32_dpp v241, v233, v194 row_half_mirror row_mask:0xf bank_mask:0xf bound_ctrl:1
	v_add_f32_dpp v242, v234, v195 row_half_mirror row_mask:0xf bank_mask:0xf bound_ctrl:1
	v_add_f32_dpp v243, v235, v196 row_half_mirror row_mask:0xf bank_mask:0xf bound_ctrl:1
	v_add_f32_dpp v244, v236, v197 row_half_mirror row_mask:0xf bank_mask:0xf bound_ctrl:1
	v_add_f32_dpp v245, v237, v198 row_half_mirror row_mask:0xf bank_mask:0xf bound_ctrl:1
	v_add_f32_dpp v246, v238, v199 row_half_mirror row_mask:0xf bank_mask:0xf bound_ctrl:1
	v_add_f32_dpp v247, v239, v200 row_half_mirror row_mask:0xf bank_mask:0xf bound_ctrl:1
	v_add_f32_dpp v248, v240, v201 row_half_mirror row_mask:0xf bank_mask:0xf bound_ctrl:1
	v_cndmask_b32_e64 v194, v245, v241, s[40:41]
	v_cndmask_b32_e64 v233, v241, v245, s[40:41]
	v_cndmask_b32_e64 v195, v246, v242, s[40:41]
	v_cndmask_b32_e64 v234, v242, v246, s[40:41]
	v_cndmask_b32_e64 v196, v247, v243, s[40:41]
	v_cndmask_b32_e64 v235, v243, v247, s[40:41]
	v_cndmask_b32_e64 v197, v248, v244, s[40:41]
	v_cndmask_b32_e64 v236, v244, v248, s[40:41]
	v_add_f32_dpp v178, v233, v194 quad_perm:[2,3,0,1] row_mask:0xf bank_mask:0xf bound_ctrl:1
	v_add_f32_dpp v179, v234, v195 quad_perm:[2,3,0,1] row_mask:0xf bank_mask:0xf bound_ctrl:1
	v_add_f32_dpp v180, v235, v196 quad_perm:[2,3,0,1] row_mask:0xf bank_mask:0xf bound_ctrl:1
	v_add_f32_dpp v181, v236, v197 quad_perm:[2,3,0,1] row_mask:0xf bank_mask:0xf bound_ctrl:1
	v_cndmask_b32_e64 v194, v180, v178, s[42:43]
	v_cndmask_b32_e64 v233, v178, v180, s[42:43]
	v_cndmask_b32_e64 v195, v181, v179, s[42:43]
	v_cndmask_b32_e64 v234, v179, v181, s[42:43]
	s_nop 1
	v_add_f32_dpp v196, v233, v194 quad_perm:[1,0,3,2] row_mask:0xf bank_mask:0xf bound_ctrl:1
	v_add_f32_dpp v197, v234, v195 quad_perm:[1,0,3,2] row_mask:0xf bank_mask:0xf bound_ctrl:1
	v_cvt_pk_bf16_f32 v198, v196, v197
	global_store_dword v227, v198, s[4:5]
	s_waitcnt vmcnt(1)
	s_cmp_lt_u32 s34, 6
	s_cbranch_scc1 .Le1_B_issue
	s_cmp_lt_i32 s35, 0
	s_cbranch_scc1 .Le1_B_done
.Le1_B_issue:
	v_and_b32_e32 v194, 0xffff, v162
	v_lshrrev_b32_e32 v195, 16, v162
	v_lshl_add_u32 v194, v194, 7, v218
	v_lshl_add_u32 v195, v195, 7, v218
	global_load_dwordx4 v[2:5], v194, s[10:11]
	global_load_dwordx4 v[6:9], v195, s[10:11]
	v_and_b32_e32 v194, 0xffff, v163
	v_lshrrev_b32_e32 v195, 16, v163
	v_lshl_add_u32 v194, v194, 7, v218
	v_lshl_add_u32 v195, v195, 7, v218
	global_load_dwordx4 v[10:13], v194, s[10:11]
	global_load_dwordx4 v[14:17], v195, s[10:11]
	v_and_b32_e32 v194, 0xffff, v164
	v_lshrrev_b32_e32 v195, 16, v164
	v_lshl_add_u32 v194, v194, 7, v218
	v_lshl_add_u32 v195, v195, 7, v218
	global_load_dwordx4 v[18:21], v194, s[10:11]
	global_load_dwordx4 v[22:25], v195, s[10:11]
	v_and_b32_e32 v194, 0xffff, v165
	v_lshrrev_b32_e32 v195, 16, v165
	v_lshl_add_u32 v194, v194, 7, v218
	v_lshl_add_u32 v195, v195, 7, v218
	global_load_dwordx4 v[26:29], v194, s[10:11]
	global_load_dwordx4 v[30:33], v195, s[10:11]
	v_and_b32_e32 v194, 0xffff, v166
	v_lshrrev_b32_e32 v195, 16, v166
	v_lshl_add_u32 v194, v194, 7, v218
	v_lshl_add_u32 v195, v195, 7, v218
	global_load_dwordx4 v[34:37], v194, s[10:11]
	global_load_dwordx4 v[38:41], v195, s[10:11]
	v_and_b32_e32 v194, 0xffff, v167
	v_lshrrev_b32_e32 v195, 16, v167
	v_lshl_add_u32 v194, v194, 7, v218
	v_lshl_add_u32 v195, v195, 7, v218
	global_load_dwordx4 v[42:45], v194, s[10:11]
	global_load_dwordx4 v[46:49], v195, s[10:11]
	v_and_b32_e32 v194, 0xffff, v168
	v_lshrrev_b32_e32 v195, 16, v168
	v_lshl_add_u32 v194, v194, 7, v218
	v_lshl_add_u32 v195, v195, 7, v218
	global_load_dwordx4 v[50:53], v194, s[10:11]
	global_load_dwordx4 v[54:57], v195, s[10:11]
	v_and_b32_e32 v194, 0xffff, v169
	v_lshrrev_b32_e32 v195, 16, v169
	v_lshl_add_u32 v194, v194, 7, v218
	v_lshl_add_u32 v195, v195, 7, v218
	global_load_dwordx4 v[58:61], v194, s[10:11]
	global_load_dwordx4 v[62:65], v195, s[10:11]
	v_add_u32_e32 v196, 0x2000, v226
	global_load_dwordx4 v[130:133], v196, s[2:3]
	global_load_dwordx4 v[134:137], v196, s[2:3] offset:16
	global_load_dwordx4 v[138:141], v196, s[2:3] offset:32
	global_load_dwordx4 v[142:145], v196, s[2:3] offset:48
	s_cmp_lt_u32 s34, 6
	s_cbranch_scc0 .Le1_B_done
	global_load_dwordx4 v[170:173], v219, s[22:23] offset:256
	global_load_dwordx4 v[174:177], v219, s[22:23] offset:272
	v_add_u32_e32 v219, 0x200, v219
	s_cmp_eq_u32 s34, 4
	s_cbranch_scc0 .Le1_B_done
	s_and_saveexec_b64 s[24:25], s[44:45]
	s_cbranch_execz .Le1_B_nopub
	v_mov_b32_e32 v196, s92
	ds_write_b32 v196, v250
.Le1_B_nopub:
	s_or_b64 exec, exec, s[24:25]
	s_waitcnt lgkmcnt(0)
	s_barrier
.Le1_B_done:
	v_lshlrev_b32_e32 v194, 16, v146
	v_and_b32_e32 v195, 0xffff0000, v146
	v_cvt_pk_f16_f32 v146, v194, v195
	v_lshlrev_b32_e32 v194, 16, v147
	v_and_b32_e32 v195, 0xffff0000, v147
	v_cvt_pk_f16_f32 v147, v194, v195
	v_lshlrev_b32_e32 v194, 16, v148
	v_and_b32_e32 v195, 0xffff0000, v148
	v_cvt_pk_f16_f32 v148, v194, v195
	v_lshlrev_b32_e32 v194, 16, v149
	v_and_b32_e32 v195, 0xffff0000, v149
	v_cvt_pk_f16_f32 v149, v194, v195
	v_lshlrev_b32_e32 v194, 16, v150
	v_and_b32_e32 v195, 0xffff0000, v150
	v_cvt_pk_f16_f32 v150, v194, v195
	v_lshlrev_b32_e32 v194, 16, v151
	v_and_b32_e32 v195, 0xffff0000, v151
	v_cvt_pk_f16_f32 v151, v194, v195
	v_lshlrev_b32_e32 v194, 16, v152
	v_and_b32_e32 v195, 0xffff0000, v152
	v_cvt_pk_f16_f32 v152, v194, v195
	v_lshlrev_b32_e32 v194, 16, v153
	v_and_b32_e32 v195, 0xffff0000, v153
	v_cvt_pk_f16_f32 v153, v194, v195
	v_lshlrev_b32_e32 v194, 16, v154
	v_and_b32_e32 v195, 0xffff0000, v154
	v_cvt_pk_f16_f32 v154, v194, v195
	v_lshlrev_b32_e32 v194, 16, v155
	v_and_b32_e32 v195, 0xffff0000, v155
	v_cvt_pk_f16_f32 v155, v194, v195
	v_lshlrev_b32_e32 v194, 16, v156
	v_and_b32_e32 v195, 0xffff0000, v156
	v_cvt_pk_f16_f32 v156, v194, v195
	v_lshlrev_b32_e32 v194, 16, v157
	v_and_b32_e32 v195, 0xffff0000, v157
	v_cvt_pk_f16_f32 v157, v194, v195
	v_lshlrev_b32_e32 v194, 16, v158
	v_and_b32_e32 v195, 0xffff0000, v158
	v_cvt_pk_f16_f32 v158, v194, v195
	v_lshlrev_b32_e32 v194, 16, v159
	v_and_b32_e32 v195, 0xffff0000, v159
	v_cvt_pk_f16_f32 v159, v194, v195
	v_lshlrev_b32_e32 v194, 16, v160
	v_and_b32_e32 v195, 0xffff0000, v160
	v_cvt_pk_f16_f32 v160, v194, v195
	v_lshlrev_b32_e32 v194, 16, v161
	v_and_b32_e32 v195, 0xffff0000, v161
	v_cvt_pk_f16_f32 v161, v194, v195
	v_cvt_scalef32_pk_f16_fp4 v198, v66, 1.0
	v_cvt_scalef32_pk_f16_fp4 v199, v70, 1.0
	v_cvt_scalef32_pk_f16_fp4 v200, v74, 1.0
	v_cvt_scalef32_pk_f16_fp4 v201, v78, 1.0
	v_dot2_f32_f16 v178, v198, v146, 0
	v_dot2_f32_f16 v179, v199, v146, 0
	v_dot2_f32_f16 v180, v200, v146, 0
	v_dot2_f32_f16 v181, v201, v146, 0
	v_cvt_scalef32_pk_f16_fp4 v198, v66, 1.0 op_sel:[1,0,0]
	v_cvt_scalef32_pk_f16_fp4 v199, v70, 1.0 op_sel:[1,0,0]
	v_cvt_scalef32_pk_f16_fp4 v200, v74, 1.0 op_sel:[1,0,0]
	v_cvt_scalef32_pk_f16_fp4 v201, v78, 1.0 op_sel:[1,0,0]
	v_dot2c_f32_f16_e32 v178, v198, v147
	v_dot2c_f32_f16_e32 v179, v199, v147
	v_dot2c_f32_f16_e32 v180, v200, v147
	v_dot2c_f32_f16_e32 v181, v201, v147
	v_cvt_scalef32_pk_f16_fp4 v198, v66, 1.0 op_sel:[0,1,0]
	v_cvt_scalef32_pk_f16_fp4 v199, v70, 1.0 op_sel:[0,1,0]
	v_cvt_scalef32_pk_f16_fp4 v200, v74, 1.0 op_sel:[0,1,0]
	v_cvt_scalef32_pk_f16_fp4 v201, v78, 1.0 op_sel:[0,1,0]
	v_dot2c_f32_f16_e32 v178, v198, v148
	v_dot2c_f32_f16_e32 v179, v199, v148
	v_dot2c_f32_f16_e32 v180, v200, v148
	v_dot2c_f32_f16_e32 v181, v201, v148
	v_cvt_scalef32_pk_f16_fp4 v198, v66, 1.0 op_sel:[1,1,0]
	v_cvt_scalef32_pk_f16_fp4 v199, v70, 1.0 op_sel:[1,1,0]
	v_cvt_scalef32_pk_f16_fp4 v200, v74, 1.0 op_sel:[1,1,0]
	v_cvt_scalef32_pk_f16_fp4 v201, v78, 1.0 op_sel:[1,1,0]
	v_dot2c_f32_f16_e32 v178, v198, v149
	v_dot2c_f32_f16_e32 v179, v199, v149
	v_dot2c_f32_f16_e32 v180, v200, v149
	v_dot2c_f32_f16_e32 v181, v201, v149
	v_cvt_scalef32_pk_f16_fp4 v198, v67, 1.0
	v_cvt_scalef32_pk_f16_fp4 v199, v71, 1.0
	v_cvt_scalef32_pk_f16_fp4 v200, v75, 1.0
	v_cvt_scalef32_pk_f16_fp4 v201, v79, 1.0
	v_dot2c_f32_f16_e32 v178, v198, v150
	v_dot2c_f32_f16_e32 v179, v199, v150
	v_dot2c_f32_f16_e32 v180, v200, v150
	v_dot2c_f32_f16_e32 v181, v201, v150
	v_cvt_scalef32_pk_f16_fp4 v198, v67, 1.0 op_sel:[1,0,0]
	v_cvt_scalef32_pk_f16_fp4 v199, v71, 1.0 op_sel:[1,0,0]
	v_cvt_scalef32_pk_f16_fp4 v200, v75, 1.0 op_sel:[1,0,0]
	v_cvt_scalef32_pk_f16_fp4 v201, v79, 1.0 op_sel:[1,0,0]
	v_dot2c_f32_f16_e32 v178, v198, v151
	v_dot2c_f32_f16_e32 v179, v199, v151
	v_dot2c_f32_f16_e32 v180, v200, v151
	v_dot2c_f32_f16_e32 v181, v201, v151
	v_cvt_scalef32_pk_f16_fp4 v198, v67, 1.0 op_sel:[0,1,0]
	v_cvt_scalef32_pk_f16_fp4 v199, v71, 1.0 op_sel:[0,1,0]
	v_cvt_scalef32_pk_f16_fp4 v200, v75, 1.0 op_sel:[0,1,0]
	v_cvt_scalef32_pk_f16_fp4 v201, v79, 1.0 op_sel:[0,1,0]
	v_dot2c_f32_f16_e32 v178, v198, v152
	v_dot2c_f32_f16_e32 v179, v199, v152
	v_dot2c_f32_f16_e32 v180, v200, v152
	v_dot2c_f32_f16_e32 v181, v201, v152
	v_cvt_scalef32_pk_f16_fp4 v198, v67, 1.0 op_sel:[1,1,0]
	v_cvt_scalef32_pk_f16_fp4 v199, v71, 1.0 op_sel:[1,1,0]
	v_cvt_scalef32_pk_f16_fp4 v200, v75, 1.0 op_sel:[1,1,0]
	v_cvt_scalef32_pk_f16_fp4 v201, v79, 1.0 op_sel:[1,1,0]
	v_dot2c_f32_f16_e32 v178, v198, v153
	v_dot2c_f32_f16_e32 v179, v199, v153
	v_dot2c_f32_f16_e32 v180, v200, v153
	v_dot2c_f32_f16_e32 v181, v201, v153
	v_cvt_scalef32_pk_f16_fp4 v198, v68, 1.0
	v_cvt_scalef32_pk_f16_fp4 v199, v72, 1.0
	v_cvt_scalef32_pk_f16_fp4 v200, v76, 1.0
	v_cvt_scalef32_pk_f16_fp4 v201, v80, 1.0
	v_dot2c_f32_f16_e32 v178, v198, v154
	v_dot2c_f32_f16_e32 v179, v199, v154
	v_dot2c_f32_f16_e32 v180, v200, v154
	v_dot2c_f32_f16_e32 v181, v201, v154
	v_cvt_scalef32_pk_f16_fp4 v198, v68, 1.0 op_sel:[1,0,0]
	v_cvt_scalef32_pk_f16_fp4 v199, v72, 1.0 op_sel:[1,0,0]
	v_cvt_scalef32_pk_f16_fp4 v200, v76, 1.0 op_sel:[1,0,0]
	v_cvt_scalef32_pk_f16_fp4 v201, v80, 1.0 op_sel:[1,0,0]
	v_dot2c_f32_f16_e32 v178, v198, v155
	v_dot2c_f32_f16_e32 v179, v199, v155
	v_dot2c_f32_f16_e32 v180, v200, v155
	v_dot2c_f32_f16_e32 v181, v201, v155
	v_cvt_scalef32_pk_f16_fp4 v198, v68, 1.0 op_sel:[0,1,0]
	v_cvt_scalef32_pk_f16_fp4 v199, v72, 1.0 op_sel:[0,1,0]
	v_cvt_scalef32_pk_f16_fp4 v200, v76, 1.0 op_sel:[0,1,0]
	v_cvt_scalef32_pk_f16_fp4 v201, v80, 1.0 op_sel:[0,1,0]
	v_dot2c_f32_f16_e32 v178, v198, v156
	v_dot2c_f32_f16_e32 v179, v199, v156
	v_dot2c_f32_f16_e32 v180, v200, v156
	v_dot2c_f32_f16_e32 v181, v201, v156
	v_cvt_scalef32_pk_f16_fp4 v198, v68, 1.0 op_sel:[1,1,0]
	v_cvt_scalef32_pk_f16_fp4 v199, v72, 1.0 op_sel:[1,1,0]
	v_cvt_scalef32_pk_f16_fp4 v200, v76, 1.0 op_sel:[1,1,0]
	v_cvt_scalef32_pk_f16_fp4 v201, v80, 1.0 op_sel:[1,1,0]
	v_dot2c_f32_f16_e32 v178, v198, v157
	v_dot2c_f32_f16_e32 v179, v199, v157
	v_dot2c_f32_f16_e32 v180, v200, v157
	v_dot2c_f32_f16_e32 v181, v201, v157
	v_cvt_scalef32_pk_f16_fp4 v198, v69, 1.0
	v_cvt_scalef32_pk_f16_fp4 v199, v73, 1.0
	v_cvt_scalef32_pk_f16_fp4 v200, v77, 1.0
	v_cvt_scalef32_pk_f16_fp4 v201, v81, 1.0
	v_dot2c_f32_f16_e32 v178, v198, v158
	v_dot2c_f32_f16_e32 v179, v199, v158
	v_dot2c_f32_f16_e32 v180, v200, v158
	v_dot2c_f32_f16_e32 v181, v201, v158
	v_cvt_scalef32_pk_f16_fp4 v198, v69, 1.0 op_sel:[1,0,0]
	v_cvt_scalef32_pk_f16_fp4 v199, v73, 1.0 op_sel:[1,0,0]
	v_cvt_scalef32_pk_f16_fp4 v200, v77, 1.0 op_sel:[1,0,0]
	v_cvt_scalef32_pk_f16_fp4 v201, v81, 1.0 op_sel:[1,0,0]
	v_dot2c_f32_f16_e32 v178, v198, v159
	v_dot2c_f32_f16_e32 v179, v199, v159
	v_dot2c_f32_f16_e32 v180, v200, v159
	v_dot2c_f32_f16_e32 v181, v201, v159
	v_cvt_scalef32_pk_f16_fp4 v198, v69, 1.0 op_sel:[0,1,0]
	v_cvt_scalef32_pk_f16_fp4 v199, v73, 1.0 op_sel:[0,1,0]
	v_cvt_scalef32_pk_f16_fp4 v200, v77, 1.0 op_sel:[0,1,0]
	v_cvt_scalef32_pk_f16_fp4 v201, v81, 1.0 op_sel:[0,1,0]
	v_dot2c_f32_f16_e32 v178, v198, v160
	v_dot2c_f32_f16_e32 v179, v199, v160
	v_dot2c_f32_f16_e32 v180, v200, v160
	v_dot2c_f32_f16_e32 v181, v201, v160
	v_cvt_scalef32_pk_f16_fp4 v198, v69, 1.0 op_sel:[1,1,0]
	v_cvt_scalef32_pk_f16_fp4 v199, v73, 1.0 op_sel:[1,1,0]
	v_cvt_scalef32_pk_f16_fp4 v200, v77, 1.0 op_sel:[1,1,0]
	v_cvt_scalef32_pk_f16_fp4 v201, v81, 1.0 op_sel:[1,1,0]
	v_dot2c_f32_f16_e32 v178, v198, v161
	v_dot2c_f32_f16_e32 v179, v199, v161
	v_dot2c_f32_f16_e32 v180, v200, v161
	v_dot2c_f32_f16_e32 v181, v201, v161
	v_cvt_scalef32_pk_f16_fp4 v198, v82, 1.0
	v_cvt_scalef32_pk_f16_fp4 v199, v86, 1.0
	v_cvt_scalef32_pk_f16_fp4 v200, v90, 1.0
	v_cvt_scalef32_pk_f16_fp4 v201, v94, 1.0
	v_dot2_f32_f16 v182, v198, v146, 0
	v_dot2_f32_f16 v183, v199, v146, 0
	v_dot2_f32_f16 v184, v200, v146, 0
	v_dot2_f32_f16 v185, v201, v146, 0
	v_cvt_scalef32_pk_f16_fp4 v198, v82, 1.0 op_sel:[1,0,0]
	v_cvt_scalef32_pk_f16_fp4 v199, v86, 1.0 op_sel:[1,0,0]
	v_cvt_scalef32_pk_f16_fp4 v200, v90, 1.0 op_sel:[1,0,0]
	v_cvt_scalef32_pk_f16_fp4 v201, v94, 1.0 op_sel:[1,0,0]
	v_dot2c_f32_f16_e32 v182, v198, v147
	v_dot2c_f32_f16_e32 v183, v199, v147
	v_dot2c_f32_f16_e32 v184, v200, v147
	v_dot2c_f32_f16_e32 v185, v201, v147
	v_cvt_scalef32_pk_f16_fp4 v198, v82, 1.0 op_sel:[0,1,0]
	v_cvt_scalef32_pk_f16_fp4 v199, v86, 1.0 op_sel:[0,1,0]
	v_cvt_scalef32_pk_f16_fp4 v200, v90, 1.0 op_sel:[0,1,0]
	v_cvt_scalef32_pk_f16_fp4 v201, v94, 1.0 op_sel:[0,1,0]
	v_dot2c_f32_f16_e32 v182, v198, v148
	v_dot2c_f32_f16_e32 v183, v199, v148
	v_dot2c_f32_f16_e32 v184, v200, v148
	v_dot2c_f32_f16_e32 v185, v201, v148
	v_cvt_scalef32_pk_f16_fp4 v198, v82, 1.0 op_sel:[1,1,0]
	v_cvt_scalef32_pk_f16_fp4 v199, v86, 1.0 op_sel:[1,1,0]
	v_cvt_scalef32_pk_f16_fp4 v200, v90, 1.0 op_sel:[1,1,0]
	v_cvt_scalef32_pk_f16_fp4 v201, v94, 1.0 op_sel:[1,1,0]
	v_dot2c_f32_f16_e32 v182, v198, v149
	v_dot2c_f32_f16_e32 v183, v199, v149
	v_dot2c_f32_f16_e32 v184, v200, v149
	v_dot2c_f32_f16_e32 v185, v201, v149
	v_cvt_scalef32_pk_f16_fp4 v198, v83, 1.0
	v_cvt_scalef32_pk_f16_fp4 v199, v87, 1.0
	v_cvt_scalef32_pk_f16_fp4 v200, v91, 1.0
	v_cvt_scalef32_pk_f16_fp4 v201, v95, 1.0
	v_dot2c_f32_f16_e32 v182, v198, v150
	v_dot2c_f32_f16_e32 v183, v199, v150
	v_dot2c_f32_f16_e32 v184, v200, v150
	v_dot2c_f32_f16_e32 v185, v201, v150
	v_cvt_scalef32_pk_f16_fp4 v198, v83, 1.0 op_sel:[1,0,0]
	v_cvt_scalef32_pk_f16_fp4 v199, v87, 1.0 op_sel:[1,0,0]
	v_cvt_scalef32_pk_f16_fp4 v200, v91, 1.0 op_sel:[1,0,0]
	v_cvt_scalef32_pk_f16_fp4 v201, v95, 1.0 op_sel:[1,0,0]
	v_dot2c_f32_f16_e32 v182, v198, v151
	v_dot2c_f32_f16_e32 v183, v199, v151
	v_dot2c_f32_f16_e32 v184, v200, v151
	v_dot2c_f32_f16_e32 v185, v201, v151
	v_cvt_scalef32_pk_f16_fp4 v198, v83, 1.0 op_sel:[0,1,0]
	v_cvt_scalef32_pk_f16_fp4 v199, v87, 1.0 op_sel:[0,1,0]
	v_cvt_scalef32_pk_f16_fp4 v200, v91, 1.0 op_sel:[0,1,0]
	v_cvt_scalef32_pk_f16_fp4 v201, v95, 1.0 op_sel:[0,1,0]
	v_dot2c_f32_f16_e32 v182, v198, v152
	v_dot2c_f32_f16_e32 v183, v199, v152
	v_dot2c_f32_f16_e32 v184, v200, v152
	v_dot2c_f32_f16_e32 v185, v201, v152
	v_cvt_scalef32_pk_f16_fp4 v198, v83, 1.0 op_sel:[1,1,0]
	v_cvt_scalef32_pk_f16_fp4 v199, v87, 1.0 op_sel:[1,1,0]
	v_cvt_scalef32_pk_f16_fp4 v200, v91, 1.0 op_sel:[1,1,0]
	v_cvt_scalef32_pk_f16_fp4 v201, v95, 1.0 op_sel:[1,1,0]
	v_dot2c_f32_f16_e32 v182, v198, v153
	v_dot2c_f32_f16_e32 v183, v199, v153
	v_dot2c_f32_f16_e32 v184, v200, v153
	v_dot2c_f32_f16_e32 v185, v201, v153
	v_cvt_scalef32_pk_f16_fp4 v198, v84, 1.0
	v_cvt_scalef32_pk_f16_fp4 v199, v88, 1.0
	v_cvt_scalef32_pk_f16_fp4 v200, v92, 1.0
	v_cvt_scalef32_pk_f16_fp4 v201, v96, 1.0
	v_dot2c_f32_f16_e32 v182, v198, v154
	v_dot2c_f32_f16_e32 v183, v199, v154
	v_dot2c_f32_f16_e32 v184, v200, v154
	v_dot2c_f32_f16_e32 v185, v201, v154
	v_cvt_scalef32_pk_f16_fp4 v198, v84, 1.0 op_sel:[1,0,0]
	v_cvt_scalef32_pk_f16_fp4 v199, v88, 1.0 op_sel:[1,0,0]
	v_cvt_scalef32_pk_f16_fp4 v200, v92, 1.0 op_sel:[1,0,0]
	v_cvt_scalef32_pk_f16_fp4 v201, v96, 1.0 op_sel:[1,0,0]
	v_dot2c_f32_f16_e32 v182, v198, v155
	v_dot2c_f32_f16_e32 v183, v199, v155
	v_dot2c_f32_f16_e32 v184, v200, v155
	v_dot2c_f32_f16_e32 v185, v201, v155
	v_cvt_scalef32_pk_f16_fp4 v198, v84, 1.0 op_sel:[0,1,0]
	v_cvt_scalef32_pk_f16_fp4 v199, v88, 1.0 op_sel:[0,1,0]
	v_cvt_scalef32_pk_f16_fp4 v200, v92, 1.0 op_sel:[0,1,0]
	v_cvt_scalef32_pk_f16_fp4 v201, v96, 1.0 op_sel:[0,1,0]
	v_dot2c_f32_f16_e32 v182, v198, v156
	v_dot2c_f32_f16_e32 v183, v199, v156
	v_dot2c_f32_f16_e32 v184, v200, v156
	v_dot2c_f32_f16_e32 v185, v201, v156
	v_cvt_scalef32_pk_f16_fp4 v198, v84, 1.0 op_sel:[1,1,0]
	v_cvt_scalef32_pk_f16_fp4 v199, v88, 1.0 op_sel:[1,1,0]
	v_cvt_scalef32_pk_f16_fp4 v200, v92, 1.0 op_sel:[1,1,0]
	v_cvt_scalef32_pk_f16_fp4 v201, v96, 1.0 op_sel:[1,1,0]
	v_dot2c_f32_f16_e32 v182, v198, v157
	v_dot2c_f32_f16_e32 v183, v199, v157
	v_dot2c_f32_f16_e32 v184, v200, v157
	v_dot2c_f32_f16_e32 v185, v201, v157
	v_cvt_scalef32_pk_f16_fp4 v198, v85, 1.0
	v_cvt_scalef32_pk_f16_fp4 v199, v89, 1.0
	v_cvt_scalef32_pk_f16_fp4 v200, v93, 1.0
	v_cvt_scalef32_pk_f16_fp4 v201, v97, 1.0
	v_dot2c_f32_f16_e32 v182, v198, v158
	v_dot2c_f32_f16_e32 v183, v199, v158
	v_dot2c_f32_f16_e32 v184, v200, v158
	v_dot2c_f32_f16_e32 v185, v201, v158
	v_cvt_scalef32_pk_f16_fp4 v198, v85, 1.0 op_sel:[1,0,0]
	v_cvt_scalef32_pk_f16_fp4 v199, v89, 1.0 op_sel:[1,0,0]
	v_cvt_scalef32_pk_f16_fp4 v200, v93, 1.0 op_sel:[1,0,0]
	v_cvt_scalef32_pk_f16_fp4 v201, v97, 1.0 op_sel:[1,0,0]
	v_dot2c_f32_f16_e32 v182, v198, v159
	v_dot2c_f32_f16_e32 v183, v199, v159
	v_dot2c_f32_f16_e32 v184, v200, v159
	v_dot2c_f32_f16_e32 v185, v201, v159
	v_cvt_scalef32_pk_f16_fp4 v198, v85, 1.0 op_sel:[0,1,0]
	v_cvt_scalef32_pk_f16_fp4 v199, v89, 1.0 op_sel:[0,1,0]
	v_cvt_scalef32_pk_f16_fp4 v200, v93, 1.0 op_sel:[0,1,0]
	v_cvt_scalef32_pk_f16_fp4 v201, v97, 1.0 op_sel:[0,1,0]
	v_dot2c_f32_f16_e32 v182, v198, v160
	v_dot2c_f32_f16_e32 v183, v199, v160
	v_dot2c_f32_f16_e32 v184, v200, v160
	v_dot2c_f32_f16_e32 v185, v201, v160
	v_cvt_scalef32_pk_f16_fp4 v198, v85, 1.0 op_sel:[1,1,0]
	v_cvt_scalef32_pk_f16_fp4 v199, v89, 1.0 op_sel:[1,1,0]
	v_cvt_scalef32_pk_f16_fp4 v200, v93, 1.0 op_sel:[1,1,0]
	v_cvt_scalef32_pk_f16_fp4 v201, v97, 1.0 op_sel:[1,1,0]
	v_dot2c_f32_f16_e32 v182, v198, v161
	v_dot2c_f32_f16_e32 v183, v199, v161
	v_dot2c_f32_f16_e32 v184, v200, v161
	v_dot2c_f32_f16_e32 v185, v201, v161
	v_cvt_scalef32_pk_f16_fp4 v198, v98, 1.0
	v_cvt_scalef32_pk_f16_fp4 v199, v102, 1.0
	v_cvt_scalef32_pk_f16_fp4 v200, v106, 1.0
	v_cvt_scalef32_pk_f16_fp4 v201, v110, 1.0
	v_dot2_f32_f16 v186, v198, v146, 0
	v_dot2_f32_f16 v187, v199, v146, 0
	v_dot2_f32_f16 v188, v200, v146, 0
	v_dot2_f32_f16 v189, v201, v146, 0
	v_cvt_scalef32_pk_f16_fp4 v198, v98, 1.0 op_sel:[1,0,0]
	v_cvt_scalef32_pk_f16_fp4 v199, v102, 1.0 op_sel:[1,0,0]
	v_cvt_scalef32_pk_f16_fp4 v200, v106, 1.0 op_sel:[1,0,0]
	v_cvt_scalef32_pk_f16_fp4 v201, v110, 1.0 op_sel:[1,0,0]
	v_dot2c_f32_f16_e32 v186, v198, v147
	v_dot2c_f32_f16_e32 v187, v199, v147
	v_dot2c_f32_f16_e32 v188, v200, v147
	v_dot2c_f32_f16_e32 v189, v201, v147
	v_cvt_scalef32_pk_f16_fp4 v198, v98, 1.0 op_sel:[0,1,0]
	v_cvt_scalef32_pk_f16_fp4 v199, v102, 1.0 op_sel:[0,1,0]
	v_cvt_scalef32_pk_f16_fp4 v200, v106, 1.0 op_sel:[0,1,0]
	v_cvt_scalef32_pk_f16_fp4 v201, v110, 1.0 op_sel:[0,1,0]
	v_dot2c_f32_f16_e32 v186, v198, v148
	v_dot2c_f32_f16_e32 v187, v199, v148
	v_dot2c_f32_f16_e32 v188, v200, v148
	v_dot2c_f32_f16_e32 v189, v201, v148
	v_cvt_scalef32_pk_f16_fp4 v198, v98, 1.0 op_sel:[1,1,0]
	v_cvt_scalef32_pk_f16_fp4 v199, v102, 1.0 op_sel:[1,1,0]
	v_cvt_scalef32_pk_f16_fp4 v200, v106, 1.0 op_sel:[1,1,0]
	v_cvt_scalef32_pk_f16_fp4 v201, v110, 1.0 op_sel:[1,1,0]
	v_dot2c_f32_f16_e32 v186, v198, v149
	v_dot2c_f32_f16_e32 v187, v199, v149
	v_dot2c_f32_f16_e32 v188, v200, v149
	v_dot2c_f32_f16_e32 v189, v201, v149
	v_cvt_scalef32_pk_f16_fp4 v198, v99, 1.0
	v_cvt_scalef32_pk_f16_fp4 v199, v103, 1.0
	v_cvt_scalef32_pk_f16_fp4 v200, v107, 1.0
	v_cvt_scalef32_pk_f16_fp4 v201, v111, 1.0
	v_dot2c_f32_f16_e32 v186, v198, v150
	v_dot2c_f32_f16_e32 v187, v199, v150
	v_dot2c_f32_f16_e32 v188, v200, v150
	v_dot2c_f32_f16_e32 v189, v201, v150
	v_cvt_scalef32_pk_f16_fp4 v198, v99, 1.0 op_sel:[1,0,0]
	v_cvt_scalef32_pk_f16_fp4 v199, v103, 1.0 op_sel:[1,0,0]
	v_cvt_scalef32_pk_f16_fp4 v200, v107, 1.0 op_sel:[1,0,0]
	v_cvt_scalef32_pk_f16_fp4 v201, v111, 1.0 op_sel:[1,0,0]
	v_dot2c_f32_f16_e32 v186, v198, v151
	v_dot2c_f32_f16_e32 v187, v199, v151
	v_dot2c_f32_f16_e32 v188, v200, v151
	v_dot2c_f32_f16_e32 v189, v201, v151
	v_cvt_scalef32_pk_f16_fp4 v198, v99, 1.0 op_sel:[0,1,0]
	v_cvt_scalef32_pk_f16_fp4 v199, v103, 1.0 op_sel:[0,1,0]
	v_cvt_scalef32_pk_f16_fp4 v200, v107, 1.0 op_sel:[0,1,0]
	v_cvt_scalef32_pk_f16_fp4 v201, v111, 1.0 op_sel:[0,1,0]
	v_dot2c_f32_f16_e32 v186, v198, v152
	v_dot2c_f32_f16_e32 v187, v199, v152
	v_dot2c_f32_f16_e32 v188, v200, v152
	v_dot2c_f32_f16_e32 v189, v201, v152
	v_cvt_scalef32_pk_f16_fp4 v198, v99, 1.0 op_sel:[1,1,0]
	v_cvt_scalef32_pk_f16_fp4 v199, v103, 1.0 op_sel:[1,1,0]
	v_cvt_scalef32_pk_f16_fp4 v200, v107, 1.0 op_sel:[1,1,0]
	v_cvt_scalef32_pk_f16_fp4 v201, v111, 1.0 op_sel:[1,1,0]
	v_dot2c_f32_f16_e32 v186, v198, v153
	v_dot2c_f32_f16_e32 v187, v199, v153
	v_dot2c_f32_f16_e32 v188, v200, v153
	v_dot2c_f32_f16_e32 v189, v201, v153
	v_cvt_scalef32_pk_f16_fp4 v198, v100, 1.0
	v_cvt_scalef32_pk_f16_fp4 v199, v104, 1.0
	v_cvt_scalef32_pk_f16_fp4 v200, v108, 1.0
	v_cvt_scalef32_pk_f16_fp4 v201, v112, 1.0
	v_dot2c_f32_f16_e32 v186, v198, v154
	v_dot2c_f32_f16_e32 v187, v199, v154
	v_dot2c_f32_f16_e32 v188, v200, v154
	v_dot2c_f32_f16_e32 v189, v201, v154
	v_cvt_scalef32_pk_f16_fp4 v198, v100, 1.0 op_sel:[1,0,0]
	v_cvt_scalef32_pk_f16_fp4 v199, v104, 1.0 op_sel:[1,0,0]
	v_cvt_scalef32_pk_f16_fp4 v200, v108, 1.0 op_sel:[1,0,0]
	v_cvt_scalef32_pk_f16_fp4 v201, v112, 1.0 op_sel:[1,0,0]
	v_dot2c_f32_f16_e32 v186, v198, v155
	v_dot2c_f32_f16_e32 v187, v199, v155
	v_dot2c_f32_f16_e32 v188, v200, v155
	v_dot2c_f32_f16_e32 v189, v201, v155
	v_cvt_scalef32_pk_f16_fp4 v198, v100, 1.0 op_sel:[0,1,0]
	v_cvt_scalef32_pk_f16_fp4 v199, v104, 1.0 op_sel:[0,1,0]
	v_cvt_scalef32_pk_f16_fp4 v200, v108, 1.0 op_sel:[0,1,0]
	v_cvt_scalef32_pk_f16_fp4 v201, v112, 1.0 op_sel:[0,1,0]
	v_dot2c_f32_f16_e32 v186, v198, v156
	v_dot2c_f32_f16_e32 v187, v199, v156
	v_dot2c_f32_f16_e32 v188, v200, v156
	v_dot2c_f32_f16_e32 v189, v201, v156
	v_cvt_scalef32_pk_f16_fp4 v198, v100, 1.0 op_sel:[1,1,0]
	v_cvt_scalef32_pk_f16_fp4 v199, v104, 1.0 op_sel:[1,1,0]
	v_cvt_scalef32_pk_f16_fp4 v200, v108, 1.0 op_sel:[1,1,0]
	v_cvt_scalef32_pk_f16_fp4 v201, v112, 1.0 op_sel:[1,1,0]
	v_dot2c_f32_f16_e32 v186, v198, v157
	v_dot2c_f32_f16_e32 v187, v199, v157
	v_dot2c_f32_f16_e32 v188, v200, v157
	v_dot2c_f32_f16_e32 v189, v201, v157
	v_cvt_scalef32_pk_f16_fp4 v198, v101, 1.0
	v_cvt_scalef32_pk_f16_fp4 v199, v105, 1.0
	v_cvt_scalef32_pk_f16_fp4 v200, v109, 1.0
	v_cvt_scalef32_pk_f16_fp4 v201, v113, 1.0
	v_dot2c_f32_f16_e32 v186, v198, v158
	v_dot2c_f32_f16_e32 v187, v199, v158
	v_dot2c_f32_f16_e32 v188, v200, v158
	v_dot2c_f32_f16_e32 v189, v201, v158
	v_cvt_scalef32_pk_f16_fp4 v198, v101, 1.0 op_sel:[1,0,0]
	v_cvt_scalef32_pk_f16_fp4 v199, v105, 1.0 op_sel:[1,0,0]
	v_cvt_scalef32_pk_f16_fp4 v200, v109, 1.0 op_sel:[1,0,0]
	v_cvt_scalef32_pk_f16_fp4 v201, v113, 1.0 op_sel:[1,0,0]
	v_dot2c_f32_f16_e32 v186, v198, v159
	v_dot2c_f32_f16_e32 v187, v199, v159
	v_dot2c_f32_f16_e32 v188, v200, v159
	v_dot2c_f32_f16_e32 v189, v201, v159
	v_cvt_scalef32_pk_f16_fp4 v198, v101, 1.0 op_sel:[0,1,0]
	v_cvt_scalef32_pk_f16_fp4 v199, v105, 1.0 op_sel:[0,1,0]
	v_cvt_scalef32_pk_f16_fp4 v200, v109, 1.0 op_sel:[0,1,0]
	v_cvt_scalef32_pk_f16_fp4 v201, v113, 1.0 op_sel:[0,1,0]
	v_dot2c_f32_f16_e32 v186, v198, v160
	v_dot2c_f32_f16_e32 v187, v199, v160
	v_dot2c_f32_f16_e32 v188, v200, v160
	v_dot2c_f32_f16_e32 v189, v201, v160
	v_cvt_scalef32_pk_f16_fp4 v198, v101, 1.0 op_sel:[1,1,0]
	v_cvt_scalef32_pk_f16_fp4 v199, v105, 1.0 op_sel:[1,1,0]
	v_cvt_scalef32_pk_f16_fp4 v200, v109, 1.0 op_sel:[1,1,0]
	v_cvt_scalef32_pk_f16_fp4 v201, v113, 1.0 op_sel:[1,1,0]
	v_dot2c_f32_f16_e32 v186, v198, v161
	v_dot2c_f32_f16_e32 v187, v199, v161
	v_dot2c_f32_f16_e32 v188, v200, v161
	v_dot2c_f32_f16_e32 v189, v201, v161
	v_cvt_scalef32_pk_f16_fp4 v198, v114, 1.0
	v_cvt_scalef32_pk_f16_fp4 v199, v118, 1.0
	v_cvt_scalef32_pk_f16_fp4 v200, v122, 1.0
	v_cvt_scalef32_pk_f16_fp4 v201, v126, 1.0
	v_dot2_f32_f16 v190, v198, v146, 0
	v_dot2_f32_f16 v191, v199, v146, 0
	v_dot2_f32_f16 v192, v200, v146, 0
	v_dot2_f32_f16 v193, v201, v146, 0
	v_cvt_scalef32_pk_f16_fp4 v198, v114, 1.0 op_sel:[1,0,0]
	v_cvt_scalef32_pk_f16_fp4 v199, v118, 1.0 op_sel:[1,0,0]
	v_cvt_scalef32_pk_f16_fp4 v200, v122, 1.0 op_sel:[1,0,0]
	v_cvt_scalef32_pk_f16_fp4 v201, v126, 1.0 op_sel:[1,0,0]
	v_dot2c_f32_f16_e32 v190, v198, v147
	v_dot2c_f32_f16_e32 v191, v199, v147
	v_dot2c_f32_f16_e32 v192, v200, v147
	v_dot2c_f32_f16_e32 v193, v201, v147
	v_cvt_scalef32_pk_f16_fp4 v198, v114, 1.0 op_sel:[0,1,0]
	v_cvt_scalef32_pk_f16_fp4 v199, v118, 1.0 op_sel:[0,1,0]
	v_cvt_scalef32_pk_f16_fp4 v200, v122, 1.0 op_sel:[0,1,0]
	v_cvt_scalef32_pk_f16_fp4 v201, v126, 1.0 op_sel:[0,1,0]
	v_dot2c_f32_f16_e32 v190, v198, v148
	v_dot2c_f32_f16_e32 v191, v199, v148
	v_dot2c_f32_f16_e32 v192, v200, v148
	v_dot2c_f32_f16_e32 v193, v201, v148
	v_cvt_scalef32_pk_f16_fp4 v198, v114, 1.0 op_sel:[1,1,0]
	v_cvt_scalef32_pk_f16_fp4 v199, v118, 1.0 op_sel:[1,1,0]
	v_cvt_scalef32_pk_f16_fp4 v200, v122, 1.0 op_sel:[1,1,0]
	v_cvt_scalef32_pk_f16_fp4 v201, v126, 1.0 op_sel:[1,1,0]
	v_dot2c_f32_f16_e32 v190, v198, v149
	v_dot2c_f32_f16_e32 v191, v199, v149
	v_dot2c_f32_f16_e32 v192, v200, v149
	v_dot2c_f32_f16_e32 v193, v201, v149
	v_cvt_scalef32_pk_f16_fp4 v198, v115, 1.0
	v_cvt_scalef32_pk_f16_fp4 v199, v119, 1.0
	v_cvt_scalef32_pk_f16_fp4 v200, v123, 1.0
	v_cvt_scalef32_pk_f16_fp4 v201, v127, 1.0
	v_dot2c_f32_f16_e32 v190, v198, v150
	v_dot2c_f32_f16_e32 v191, v199, v150
	v_dot2c_f32_f16_e32 v192, v200, v150
	v_dot2c_f32_f16_e32 v193, v201, v150
	v_cvt_scalef32_pk_f16_fp4 v198, v115, 1.0 op_sel:[1,0,0]
	v_cvt_scalef32_pk_f16_fp4 v199, v119, 1.0 op_sel:[1,0,0]
	v_cvt_scalef32_pk_f16_fp4 v200, v123, 1.0 op_sel:[1,0,0]
	v_cvt_scalef32_pk_f16_fp4 v201, v127, 1.0 op_sel:[1,0,0]
	v_dot2c_f32_f16_e32 v190, v198, v151
	v_dot2c_f32_f16_e32 v191, v199, v151
	v_dot2c_f32_f16_e32 v192, v200, v151
	v_dot2c_f32_f16_e32 v193, v201, v151
	v_cvt_scalef32_pk_f16_fp4 v198, v115, 1.0 op_sel:[0,1,0]
	v_cvt_scalef32_pk_f16_fp4 v199, v119, 1.0 op_sel:[0,1,0]
	v_cvt_scalef32_pk_f16_fp4 v200, v123, 1.0 op_sel:[0,1,0]
	v_cvt_scalef32_pk_f16_fp4 v201, v127, 1.0 op_sel:[0,1,0]
	v_dot2c_f32_f16_e32 v190, v198, v152
	v_dot2c_f32_f16_e32 v191, v199, v152
	v_dot2c_f32_f16_e32 v192, v200, v152
	v_dot2c_f32_f16_e32 v193, v201, v152
	v_cvt_scalef32_pk_f16_fp4 v198, v115, 1.0 op_sel:[1,1,0]
	v_cvt_scalef32_pk_f16_fp4 v199, v119, 1.0 op_sel:[1,1,0]
	v_cvt_scalef32_pk_f16_fp4 v200, v123, 1.0 op_sel:[1,1,0]
	v_cvt_scalef32_pk_f16_fp4 v201, v127, 1.0 op_sel:[1,1,0]
	v_dot2c_f32_f16_e32 v190, v198, v153
	v_dot2c_f32_f16_e32 v191, v199, v153
	v_dot2c_f32_f16_e32 v192, v200, v153
	v_dot2c_f32_f16_e32 v193, v201, v153
	v_cvt_scalef32_pk_f16_fp4 v198, v116, 1.0
	v_cvt_scalef32_pk_f16_fp4 v199, v120, 1.0
	v_cvt_scalef32_pk_f16_fp4 v200, v124, 1.0
	v_cvt_scalef32_pk_f16_fp4 v201, v128, 1.0
	v_dot2c_f32_f16_e32 v190, v198, v154
	v_dot2c_f32_f16_e32 v191, v199, v154
	v_dot2c_f32_f16_e32 v192, v200, v154
	v_dot2c_f32_f16_e32 v193, v201, v154
	v_cvt_scalef32_pk_f16_fp4 v198, v116, 1.0 op_sel:[1,0,0]
	v_cvt_scalef32_pk_f16_fp4 v199, v120, 1.0 op_sel:[1,0,0]
	v_cvt_scalef32_pk_f16_fp4 v200, v124, 1.0 op_sel:[1,0,0]
	v_cvt_scalef32_pk_f16_fp4 v201, v128, 1.0 op_sel:[1,0,0]
	v_dot2c_f32_f16_e32 v190, v198, v155
	v_dot2c_f32_f16_e32 v191, v199, v155
	v_dot2c_f32_f16_e32 v192, v200, v155
	v_dot2c_f32_f16_e32 v193, v201, v155
	v_cvt_scalef32_pk_f16_fp4 v198, v116, 1.0 op_sel:[0,1,0]
	v_cvt_scalef32_pk_f16_fp4 v199, v120, 1.0 op_sel:[0,1,0]
	v_cvt_scalef32_pk_f16_fp4 v200, v124, 1.0 op_sel:[0,1,0]
	v_cvt_scalef32_pk_f16_fp4 v201, v128, 1.0 op_sel:[0,1,0]
	v_dot2c_f32_f16_e32 v190, v198, v156
	v_dot2c_f32_f16_e32 v191, v199, v156
	v_dot2c_f32_f16_e32 v192, v200, v156
	v_dot2c_f32_f16_e32 v193, v201, v156
	v_cvt_scalef32_pk_f16_fp4 v198, v116, 1.0 op_sel:[1,1,0]
	v_cvt_scalef32_pk_f16_fp4 v199, v120, 1.0 op_sel:[1,1,0]
	v_cvt_scalef32_pk_f16_fp4 v200, v124, 1.0 op_sel:[1,1,0]
	v_cvt_scalef32_pk_f16_fp4 v201, v128, 1.0 op_sel:[1,1,0]
	v_dot2c_f32_f16_e32 v190, v198, v157
	v_dot2c_f32_f16_e32 v191, v199, v157
	v_dot2c_f32_f16_e32 v192, v200, v157
	v_dot2c_f32_f16_e32 v193, v201, v157
	v_cvt_scalef32_pk_f16_fp4 v198, v117, 1.0
	v_cvt_scalef32_pk_f16_fp4 v199, v121, 1.0
	v_cvt_scalef32_pk_f16_fp4 v200, v125, 1.0
	v_cvt_scalef32_pk_f16_fp4 v201, v129, 1.0
	v_dot2c_f32_f16_e32 v190, v198, v158
	v_dot2c_f32_f16_e32 v191, v199, v158
	v_dot2c_f32_f16_e32 v192, v200, v158
	v_dot2c_f32_f16_e32 v193, v201, v158
	v_cvt_scalef32_pk_f16_fp4 v198, v117, 1.0 op_sel:[1,0,0]
	v_cvt_scalef32_pk_f16_fp4 v199, v121, 1.0 op_sel:[1,0,0]
	v_cvt_scalef32_pk_f16_fp4 v200, v125, 1.0 op_sel:[1,0,0]
	v_cvt_scalef32_pk_f16_fp4 v201, v129, 1.0 op_sel:[1,0,0]
	v_dot2c_f32_f16_e32 v190, v198, v159
	v_dot2c_f32_f16_e32 v191, v199, v159
	v_dot2c_f32_f16_e32 v192, v200, v159
	v_dot2c_f32_f16_e32 v193, v201, v159
	v_cvt_scalef32_pk_f16_fp4 v198, v117, 1.0 op_sel:[0,1,0]
	v_cvt_scalef32_pk_f16_fp4 v199, v121, 1.0 op_sel:[0,1,0]
	v_cvt_scalef32_pk_f16_fp4 v200, v125, 1.0 op_sel:[0,1,0]
	v_cvt_scalef32_pk_f16_fp4 v201, v129, 1.0 op_sel:[0,1,0]
	v_dot2c_f32_f16_e32 v190, v198, v160
	v_dot2c_f32_f16_e32 v191, v199, v160
	v_dot2c_f32_f16_e32 v192, v200, v160
	v_dot2c_f32_f16_e32 v193, v201, v160
	v_cvt_scalef32_pk_f16_fp4 v198, v117, 1.0 op_sel:[1,1,0]
	v_cvt_scalef32_pk_f16_fp4 v199, v121, 1.0 op_sel:[1,1,0]
	v_cvt_scalef32_pk_f16_fp4 v200, v125, 1.0 op_sel:[1,1,0]
	v_cvt_scalef32_pk_f16_fp4 v201, v129, 1.0 op_sel:[1,1,0]
	v_dot2c_f32_f16_e32 v190, v198, v161
	v_dot2c_f32_f16_e32 v191, v199, v161
	v_dot2c_f32_f16_e32 v192, v200, v161
	v_dot2c_f32_f16_e32 v193, v201, v161
	s_nop 3
	v_cndmask_b32_e64 v194, v178, v186, s[38:39]
	v_cndmask_b32_e64 v233, v186, v178, s[38:39]
	v_cndmask_b32_e64 v195, v179, v187, s[38:39]
	v_cndmask_b32_e64 v234, v187, v179, s[38:39]
	v_cndmask_b32_e64 v196, v180, v188, s[38:39]
	v_cndmask_b32_e64 v235, v188, v180, s[38:39]
	v_cndmask_b32_e64 v197, v181, v189, s[38:39]
	v_cndmask_b32_e64 v236, v189, v181, s[38:39]
	v_cndmask_b32_e64 v198, v182, v190, s[38:39]
	v_cndmask_b32_e64 v237, v190, v182, s[38:39]
	v_cndmask_b32_e64 v199, v183, v191, s[38:39]
	v_cndmask_b32_e64 v238, v191, v183, s[38:39]
	v_cndmask_b32_e64 v200, v184, v192, s[38:39]
	v_cndmask_b32_e64 v239, v192, v184, s[38:39]
	v_cndmask_b32_e64 v201, v185, v193, s[38:39]
	v_cndmask_b32_e64 v240, v193, v185, s[38:39]
	v_add_f32_dpp v241, v233, v194 row_half_mirror row_mask:0xf bank_mask:0xf bound_ctrl:1
	v_add_f32_dpp v242, v234, v195 row_half_mirror row_mask:0xf bank_mask:0xf bound_ctrl:1
	v_add_f32_dpp v243, v235, v196 row_half_mirror row_mask:0xf bank_mask:0xf bound_ctrl:1
	v_add_f32_dpp v244, v236, v197 row_half_mirror row_mask:0xf bank_mask:0xf bound_ctrl:1
	v_add_f32_dpp v245, v237, v198 row_half_mirror row_mask:0xf bank_mask:0xf bound_ctrl:1
	v_add_f32_dpp v246, v238, v199 row_half_mirror row_mask:0xf bank_mask:0xf bound_ctrl:1
	v_add_f32_dpp v247, v239, v200 row_half_mirror row_mask:0xf bank_mask:0xf bound_ctrl:1
	v_add_f32_dpp v248, v240, v201 row_half_mirror row_mask:0xf bank_mask:0xf bound_ctrl:1
	v_cndmask_b32_e64 v194, v245, v241, s[40:41]
	v_cndmask_b32_e64 v233, v241, v245, s[40:41]
	v_cndmask_b32_e64 v195, v246, v242, s[40:41]
	v_cndmask_b32_e64 v234, v242, v246, s[40:41]
	v_cndmask_b32_e64 v196, v247, v243, s[40:41]
	v_cndmask_b32_e64 v235, v243, v247, s[40:41]
	v_cndmask_b32_e64 v197, v248, v244, s[40:41]
	v_cndmask_b32_e64 v236, v244, v248, s[40:41]
	v_add_f32_dpp v178, v233, v194 quad_perm:[2,3,0,1] row_mask:0xf bank_mask:0xf bound_ctrl:1
	v_add_f32_dpp v179, v234, v195 quad_perm:[2,3,0,1] row_mask:0xf bank_mask:0xf bound_ctrl:1
	v_add_f32_dpp v180, v235, v196 quad_perm:[2,3,0,1] row_mask:0xf bank_mask:0xf bound_ctrl:1
	v_add_f32_dpp v181, v236, v197 quad_perm:[2,3,0,1] row_mask:0xf bank_mask:0xf bound_ctrl:1
	v_cndmask_b32_e64 v194, v180, v178, s[42:43]
	v_cndmask_b32_e64 v233, v178, v180, s[42:43]
	v_cndmask_b32_e64 v195, v181, v179, s[42:43]
	v_cndmask_b32_e64 v234, v179, v181, s[42:43]
	s_nop 1
	v_add_f32_dpp v196, v233, v194 quad_perm:[1,0,3,2] row_mask:0xf bank_mask:0xf bound_ctrl:1
	v_add_f32_dpp v197, v234, v195 quad_perm:[1,0,3,2] row_mask:0xf bank_mask:0xf bound_ctrl:1
	v_cvt_pk_bf16_f32 v198, v196, v197
	global_store_dword v227, v198, s[4:5] offset:256
	v_add_u32_e32 v227, 0x200, v227
	v_add_u32_e32 v226, 0x2000, v226
	s_add_i32 s34, s34, 2
	s_cmp_lt_u32 s34, 8
	s_cbranch_scc1 .Le1_loop
	s_cmp_lt_i32 s35, 0
	s_cbranch_scc1 .Le1_chain_end
	v_mov_b32_e32 v227, v251
	s_mov_b32 s34, 0
	s_branch .Le1_loop
.Le1_chain_end:
	s_branch .LBB0_722

.Le2_loop:
	s_waitcnt vmcnt(1)
	v_and_b32_e32 v194, 0xffff, v170
	v_lshrrev_b32_e32 v195, 16, v170
	v_lshl_add_u32 v194, v194, 7, v218
	v_lshl_add_u32 v195, v195, 7, v218
	global_load_dwordx4 v[66:69], v194, s[40:41]
	global_load_dwordx4 v[70:73], v195, s[40:41]
	v_and_b32_e32 v194, 0xffff, v171
	v_lshrrev_b32_e32 v195, 16, v171
	v_lshl_add_u32 v194, v194, 7, v218
	v_lshl_add_u32 v195, v195, 7, v218
	global_load_dwordx4 v[74:77], v194, s[40:41]
	global_load_dwordx4 v[78:81], v195, s[40:41]
	v_and_b32_e32 v194, 0xffff, v172
	v_lshrrev_b32_e32 v195, 16, v172
	v_lshl_add_u32 v194, v194, 7, v218
	v_lshl_add_u32 v195, v195, 7, v218
	global_load_dwordx4 v[82:85], v194, s[40:41]
	global_load_dwordx4 v[86:89], v195, s[40:41]
	v_and_b32_e32 v194, 0xffff, v173
	v_lshrrev_b32_e32 v195, 16, v173
	v_lshl_add_u32 v194, v194, 7, v218
	v_lshl_add_u32 v195, v195, 7, v218
	global_load_dwordx4 v[90:93], v194, s[40:41]
	global_load_dwordx4 v[94:97], v195, s[40:41]
	v_and_b32_e32 v194, 0xffff, v174
	v_lshrrev_b32_e32 v195, 16, v174
	v_lshl_add_u32 v194, v194, 7, v218
	v_lshl_add_u32 v195, v195, 7, v218
	global_load_dwordx4 v[98:101], v194, s[40:41]
	global_load_dwordx4 v[102:105], v195, s[40:41]
	v_and_b32_e32 v194, 0xffff, v175
	v_lshrrev_b32_e32 v195, 16, v175
	v_lshl_add_u32 v194, v194, 7, v218
	v_lshl_add_u32 v195, v195, 7, v218
	global_load_dwordx4 v[106:109], v194, s[40:41]
	global_load_dwordx4 v[110:113], v195, s[40:41]
	v_and_b32_e32 v194, 0xffff, v176
	v_lshrrev_b32_e32 v195, 16, v176
	v_lshl_add_u32 v194, v194, 7, v218
	v_lshl_add_u32 v195, v195, 7, v218
	global_load_dwordx4 v[114:117], v194, s[40:41]
	global_load_dwordx4 v[118:121], v195, s[40:41]
	v_and_b32_e32 v194, 0xffff, v177
	v_lshrrev_b32_e32 v195, 16, v177
	v_lshl_add_u32 v194, v194, 7, v218
	v_lshl_add_u32 v195, v195, 7, v218
	global_load_dwordx4 v[122:125], v194, s[40:41]
	global_load_dwordx4 v[126:129], v195, s[40:41]
	global_load_dwordx4 v[138:141], v219, s[56:57] offset:-528
	global_load_dwordx4 v[142:145], v219, s[56:57] offset:-512
	v_add_u32_e32 v250, 1, v226
	v_mul_hi_i32 v242, v250, s69
	v_lshrrev_b32_e32 v243, 31, v242
	v_ashrrev_i32_e32 v242, 13, v242
	v_add_u32_e32 v243, v242, v243
	v_mul_i32_i24_e32 v246, 0xffffbf00, v243
	v_add_u32_e32 v242, v250, v246
	v_cmp_gt_i32_e32 vcc, s68, v242
	v_cmp_lt_i32_e64 s[0:1], s21, v242
	s_and_saveexec_b64 s[2:3], s[0:1]
	s_xor_b64 s[0:1], exec, s[2:3]
	v_lshl_add_u32 v242, v243, 14, v246
	v_add3_u32 v242, v250, v242, s88
	s_or_saveexec_b64 s[0:1], s[0:1]
	v_mov_b64_e32 v[244:245], s[18:19]
	s_xor_b64 exec, exec, s[0:1]
	v_lshlrev_b32_e32 v242, 8, v243
	v_add3_u32 v242, v246, v250, v242
	v_mov_b64_e32 v[244:245], s[72:73]
	s_or_b64 exec, exec, s[0:1]
	v_mul_i32_i24_e32 v243, 0x3000, v243
	v_cndmask_b32_e32 v246, v243, v223, vcc
	v_ashrrev_i32_e32 v247, 31, v246
	v_lshl_add_u64 v[246:247], v[246:247], 2, s[10:11]
	v_ashrrev_i32_e32 v243, 31, v242
	v_lshl_add_u64 v[248:249], v[246:247], 0, v[236:237]
	v_lshlrev_b64 v[242:243], 13, v[242:243]
	v_lshl_add_u64 v[242:243], v[244:245], 0, v[242:243]
	v_add_co_u32_e32 v248, vcc, s94, v248
	v_lshl_add_u64 v[240:241], v[242:243], 0, v[236:237]
	s_nop 0
	v_addc_co_u32_e32 v249, vcc, 0, v249, vcc
	global_load_dwordx4 v[154:157], v[240:241], off
	global_load_dwordx4 v[158:161], v[248:249], off
	s_cmp_lt_u32 s33, 6
	s_cbranch_scc0 .Le2_A_last
	global_load_dwordx4 v[162:165], v219, s[22:23]
	global_load_dwordx4 v[166:169], v219, s[22:23] offset:16
	s_cmp_eq_u32 s33, 4
	s_cbranch_scc0 .Le2_A_done
	s_barrier
	s_and_saveexec_b64 s[0:1], s[44:45]
	s_cbranch_execz .Le2_A_noatom
	global_atomic_add v251, v211, v1, s[24:25] sc0
.Le2_A_noatom:
	s_or_b64 exec, exec, s[0:1]
	s_branch .Le2_A_done
.Le2_A_last:
	v_mov_b32_e32 v198, s92
	ds_read_b32 v198, v198
	s_waitcnt lgkmcnt(0)
	v_readfirstlane_b32 s35, v198
	s_cmp_ge_i32 s35, s60
	s_cbranch_scc1 .Le2_A_nonext
	s_lshl_b32 s98, s35, 6
	s_and_b32 s99, s35, 0xffffff00
	s_add_i32 s99, s99, 0x100
	s_and_b64 s[0:1], s[30:31], exec
	s_cselect_b32 s99, 0, s99
	s_add_i32 s98, s98, s99
	v_lshrrev_b32_e32 v243, 6, v0
	v_bfe_u32 v244, v0, 3, 3
	v_lshl_add_u32 v245, v243, 3, s98
	v_lshlrev_b32_e32 v219, 8, v245
	v_lshl_add_u32 v219, v244, 5, v219
	v_add_u32_e32 v226, -2, v245
	global_load_dwordx4 v[162:165], v219, s[22:23]
	global_load_dwordx4 v[166:169], v219, s[22:23] offset:16
	global_load_dwordx4 v[170:173], v219, s[22:23] offset:256
	global_load_dwordx4 v[174:177], v219, s[22:23] offset:272
	s_branch .Le2_A_done

.Le2_A_done:
	v_mul_u32_u24_sdwa v202, v130, s93 dst_sel:DWORD dst_unused:UNUSED_PAD src0_sel:WORD_0 src1_sel:DWORD
	v_cvt_scalef32_pk_f16_fp4 v194, v2, 1.0
	v_cvt_scalef32_pk_f16_fp4 v195, v2, 1.0 op_sel:[1,0,0]
	v_cvt_scalef32_pk_f16_fp4 v196, v2, 1.0 op_sel:[0,1,0]
	v_pk_fma_f16 v178, v194, v202, 0
	v_cvt_scalef32_pk_f16_fp4 v197, v2, 1.0 op_sel:[1,1,0]
	v_pk_fma_f16 v179, v195, v202, 0
	v_cvt_scalef32_pk_f16_fp4 v194, v3, 1.0
	v_pk_fma_f16 v180, v196, v202, 0
	v_cvt_scalef32_pk_f16_fp4 v195, v3, 1.0 op_sel:[1,0,0]
	v_pk_fma_f16 v181, v197, v202, 0
	v_cvt_scalef32_pk_f16_fp4 v196, v3, 1.0 op_sel:[0,1,0]
	v_pk_fma_f16 v182, v194, v202, 0
	v_cvt_scalef32_pk_f16_fp4 v197, v3, 1.0 op_sel:[1,1,0]
	v_pk_fma_f16 v183, v195, v202, 0
	v_cvt_scalef32_pk_f16_fp4 v194, v4, 1.0
	v_pk_fma_f16 v184, v196, v202, 0
	v_cvt_scalef32_pk_f16_fp4 v195, v4, 1.0 op_sel:[1,0,0]
	v_pk_fma_f16 v185, v197, v202, 0
	v_cvt_scalef32_pk_f16_fp4 v196, v4, 1.0 op_sel:[0,1,0]
	v_pk_fma_f16 v186, v194, v202, 0
	v_cvt_scalef32_pk_f16_fp4 v197, v4, 1.0 op_sel:[1,1,0]
	v_pk_fma_f16 v187, v195, v202, 0
	v_cvt_scalef32_pk_f16_fp4 v194, v5, 1.0
	v_pk_fma_f16 v188, v196, v202, 0
	v_cvt_scalef32_pk_f16_fp4 v195, v5, 1.0 op_sel:[1,0,0]
	v_pk_fma_f16 v189, v197, v202, 0
	v_cvt_scalef32_pk_f16_fp4 v196, v5, 1.0 op_sel:[0,1,0]
	v_pk_fma_f16 v190, v194, v202, 0
	v_cvt_scalef32_pk_f16_fp4 v197, v5, 1.0 op_sel:[1,1,0]
	v_pk_fma_f16 v191, v195, v202, 0
	v_pk_fma_f16 v192, v196, v202, 0
	v_pk_fma_f16 v193, v197, v202, 0
	v_mul_u32_u24_sdwa v203, v130, s93 dst_sel:DWORD dst_unused:UNUSED_PAD src0_sel:WORD_1 src1_sel:DWORD
	v_cvt_scalef32_pk_f16_fp4 v194, v6, 1.0
	v_cvt_scalef32_pk_f16_fp4 v195, v6, 1.0 op_sel:[1,0,0]
	v_cvt_scalef32_pk_f16_fp4 v196, v6, 1.0 op_sel:[0,1,0]
	v_pk_fma_f16 v178, v194, v203, v178
	v_cvt_scalef32_pk_f16_fp4 v197, v6, 1.0 op_sel:[1,1,0]
	v_pk_fma_f16 v179, v195, v203, v179
	v_cvt_scalef32_pk_f16_fp4 v194, v7, 1.0
	v_pk_fma_f16 v180, v196, v203, v180
	v_cvt_scalef32_pk_f16_fp4 v195, v7, 1.0 op_sel:[1,0,0]
	v_pk_fma_f16 v181, v197, v203, v181
	v_cvt_scalef32_pk_f16_fp4 v196, v7, 1.0 op_sel:[0,1,0]
	v_pk_fma_f16 v182, v194, v203, v182
	v_cvt_scalef32_pk_f16_fp4 v197, v7, 1.0 op_sel:[1,1,0]
	v_pk_fma_f16 v183, v195, v203, v183
	v_cvt_scalef32_pk_f16_fp4 v194, v8, 1.0
	v_pk_fma_f16 v184, v196, v203, v184
	v_cvt_scalef32_pk_f16_fp4 v195, v8, 1.0 op_sel:[1,0,0]
	v_pk_fma_f16 v185, v197, v203, v185
	v_cvt_scalef32_pk_f16_fp4 v196, v8, 1.0 op_sel:[0,1,0]
	v_pk_fma_f16 v186, v194, v203, v186
	v_cvt_scalef32_pk_f16_fp4 v197, v8, 1.0 op_sel:[1,1,0]
	v_pk_fma_f16 v187, v195, v203, v187
	v_cvt_scalef32_pk_f16_fp4 v194, v9, 1.0
	v_pk_fma_f16 v188, v196, v203, v188
	v_cvt_scalef32_pk_f16_fp4 v195, v9, 1.0 op_sel:[1,0,0]
	v_pk_fma_f16 v189, v197, v203, v189
	v_cvt_scalef32_pk_f16_fp4 v196, v9, 1.0 op_sel:[0,1,0]
	v_pk_fma_f16 v190, v194, v203, v190
	v_cvt_scalef32_pk_f16_fp4 v197, v9, 1.0 op_sel:[1,1,0]
	v_pk_fma_f16 v191, v195, v203, v191
	v_pk_fma_f16 v192, v196, v203, v192
	v_pk_fma_f16 v193, v197, v203, v193
	v_mul_u32_u24_sdwa v202, v131, s93 dst_sel:DWORD dst_unused:UNUSED_PAD src0_sel:WORD_0 src1_sel:DWORD
	v_cvt_scalef32_pk_f16_fp4 v194, v10, 1.0
	v_cvt_scalef32_pk_f16_fp4 v195, v10, 1.0 op_sel:[1,0,0]
	v_cvt_scalef32_pk_f16_fp4 v196, v10, 1.0 op_sel:[0,1,0]
	v_pk_fma_f16 v178, v194, v202, v178
	v_cvt_scalef32_pk_f16_fp4 v197, v10, 1.0 op_sel:[1,1,0]
	v_pk_fma_f16 v179, v195, v202, v179
	v_cvt_scalef32_pk_f16_fp4 v194, v11, 1.0
	v_pk_fma_f16 v180, v196, v202, v180
	v_cvt_scalef32_pk_f16_fp4 v195, v11, 1.0 op_sel:[1,0,0]
	v_pk_fma_f16 v181, v197, v202, v181
	v_cvt_scalef32_pk_f16_fp4 v196, v11, 1.0 op_sel:[0,1,0]
	v_pk_fma_f16 v182, v194, v202, v182
	v_cvt_scalef32_pk_f16_fp4 v197, v11, 1.0 op_sel:[1,1,0]
	v_pk_fma_f16 v183, v195, v202, v183
	v_cvt_scalef32_pk_f16_fp4 v194, v12, 1.0
	v_pk_fma_f16 v184, v196, v202, v184
	v_cvt_scalef32_pk_f16_fp4 v195, v12, 1.0 op_sel:[1,0,0]
	v_pk_fma_f16 v185, v197, v202, v185
	v_cvt_scalef32_pk_f16_fp4 v196, v12, 1.0 op_sel:[0,1,0]
	v_pk_fma_f16 v186, v194, v202, v186
	v_cvt_scalef32_pk_f16_fp4 v197, v12, 1.0 op_sel:[1,1,0]
	v_pk_fma_f16 v187, v195, v202, v187
	v_cvt_scalef32_pk_f16_fp4 v194, v13, 1.0
	v_pk_fma_f16 v188, v196, v202, v188
	v_cvt_scalef32_pk_f16_fp4 v195, v13, 1.0 op_sel:[1,0,0]
	v_pk_fma_f16 v189, v197, v202, v189
	v_cvt_scalef32_pk_f16_fp4 v196, v13, 1.0 op_sel:[0,1,0]
	v_pk_fma_f16 v190, v194, v202, v190
	v_cvt_scalef32_pk_f16_fp4 v197, v13, 1.0 op_sel:[1,1,0]
	v_pk_fma_f16 v191, v195, v202, v191
	v_pk_fma_f16 v192, v196, v202, v192
	v_pk_fma_f16 v193, v197, v202, v193
	v_mul_u32_u24_sdwa v203, v131, s93 dst_sel:DWORD dst_unused:UNUSED_PAD src0_sel:WORD_1 src1_sel:DWORD
	v_cvt_scalef32_pk_f16_fp4 v194, v14, 1.0
	v_cvt_scalef32_pk_f16_fp4 v195, v14, 1.0 op_sel:[1,0,0]
	v_cvt_scalef32_pk_f16_fp4 v196, v14, 1.0 op_sel:[0,1,0]
	v_pk_fma_f16 v178, v194, v203, v178
	v_cvt_scalef32_pk_f16_fp4 v197, v14, 1.0 op_sel:[1,1,0]
	v_pk_fma_f16 v179, v195, v203, v179
	v_cvt_scalef32_pk_f16_fp4 v194, v15, 1.0
	v_pk_fma_f16 v180, v196, v203, v180
	v_cvt_scalef32_pk_f16_fp4 v195, v15, 1.0 op_sel:[1,0,0]
	v_pk_fma_f16 v181, v197, v203, v181
	v_cvt_scalef32_pk_f16_fp4 v196, v15, 1.0 op_sel:[0,1,0]
	v_pk_fma_f16 v182, v194, v203, v182
	v_cvt_scalef32_pk_f16_fp4 v197, v15, 1.0 op_sel:[1,1,0]
	v_pk_fma_f16 v183, v195, v203, v183
	v_cvt_scalef32_pk_f16_fp4 v194, v16, 1.0
	v_pk_fma_f16 v184, v196, v203, v184
	v_cvt_scalef32_pk_f16_fp4 v195, v16, 1.0 op_sel:[1,0,0]
	v_pk_fma_f16 v185, v197, v203, v185
	v_cvt_scalef32_pk_f16_fp4 v196, v16, 1.0 op_sel:[0,1,0]
	v_pk_fma_f16 v186, v194, v203, v186
	v_cvt_scalef32_pk_f16_fp4 v197, v16, 1.0 op_sel:[1,1,0]
	v_pk_fma_f16 v187, v195, v203, v187
	v_cvt_scalef32_pk_f16_fp4 v194, v17, 1.0
	v_pk_fma_f16 v188, v196, v203, v188
	v_cvt_scalef32_pk_f16_fp4 v195, v17, 1.0 op_sel:[1,0,0]
	v_pk_fma_f16 v189, v197, v203, v189
	v_cvt_scalef32_pk_f16_fp4 v196, v17, 1.0 op_sel:[0,1,0]
	v_pk_fma_f16 v190, v194, v203, v190
	v_cvt_scalef32_pk_f16_fp4 v197, v17, 1.0 op_sel:[1,1,0]
	v_pk_fma_f16 v191, v195, v203, v191
	v_pk_fma_f16 v192, v196, v203, v192
	v_pk_fma_f16 v193, v197, v203, v193
	v_mul_u32_u24_sdwa v202, v132, s93 dst_sel:DWORD dst_unused:UNUSED_PAD src0_sel:WORD_0 src1_sel:DWORD
	v_cvt_scalef32_pk_f16_fp4 v194, v18, 1.0
	v_cvt_scalef32_pk_f16_fp4 v195, v18, 1.0 op_sel:[1,0,0]
	v_cvt_scalef32_pk_f16_fp4 v196, v18, 1.0 op_sel:[0,1,0]
	v_pk_fma_f16 v178, v194, v202, v178
	v_cvt_scalef32_pk_f16_fp4 v197, v18, 1.0 op_sel:[1,1,0]
	v_pk_fma_f16 v179, v195, v202, v179
	v_cvt_scalef32_pk_f16_fp4 v194, v19, 1.0
	v_pk_fma_f16 v180, v196, v202, v180
	v_cvt_scalef32_pk_f16_fp4 v195, v19, 1.0 op_sel:[1,0,0]
	v_pk_fma_f16 v181, v197, v202, v181
	v_cvt_scalef32_pk_f16_fp4 v196, v19, 1.0 op_sel:[0,1,0]
	v_pk_fma_f16 v182, v194, v202, v182
	v_cvt_scalef32_pk_f16_fp4 v197, v19, 1.0 op_sel:[1,1,0]
	v_pk_fma_f16 v183, v195, v202, v183
	v_cvt_scalef32_pk_f16_fp4 v194, v20, 1.0
	v_pk_fma_f16 v184, v196, v202, v184
	v_cvt_scalef32_pk_f16_fp4 v195, v20, 1.0 op_sel:[1,0,0]
	v_pk_fma_f16 v185, v197, v202, v185
	v_cvt_scalef32_pk_f16_fp4 v196, v20, 1.0 op_sel:[0,1,0]
	v_pk_fma_f16 v186, v194, v202, v186
	v_cvt_scalef32_pk_f16_fp4 v197, v20, 1.0 op_sel:[1,1,0]
	v_pk_fma_f16 v187, v195, v202, v187
	v_cvt_scalef32_pk_f16_fp4 v194, v21, 1.0
	v_pk_fma_f16 v188, v196, v202, v188
	v_cvt_scalef32_pk_f16_fp4 v195, v21, 1.0 op_sel:[1,0,0]
	v_pk_fma_f16 v189, v197, v202, v189
	v_cvt_scalef32_pk_f16_fp4 v196, v21, 1.0 op_sel:[0,1,0]
	v_pk_fma_f16 v190, v194, v202, v190
	v_cvt_scalef32_pk_f16_fp4 v197, v21, 1.0 op_sel:[1,1,0]
	v_pk_fma_f16 v191, v195, v202, v191
	v_pk_fma_f16 v192, v196, v202, v192
	v_pk_fma_f16 v193, v197, v202, v193
	v_mul_u32_u24_sdwa v203, v132, s93 dst_sel:DWORD dst_unused:UNUSED_PAD src0_sel:WORD_1 src1_sel:DWORD
	v_cvt_scalef32_pk_f16_fp4 v194, v22, 1.0
	v_cvt_scalef32_pk_f16_fp4 v195, v22, 1.0 op_sel:[1,0,0]
	v_cvt_scalef32_pk_f16_fp4 v196, v22, 1.0 op_sel:[0,1,0]
	v_pk_fma_f16 v178, v194, v203, v178
	v_cvt_scalef32_pk_f16_fp4 v197, v22, 1.0 op_sel:[1,1,0]
	v_pk_fma_f16 v179, v195, v203, v179
	v_cvt_scalef32_pk_f16_fp4 v194, v23, 1.0
	v_pk_fma_f16 v180, v196, v203, v180
	v_cvt_scalef32_pk_f16_fp4 v195, v23, 1.0 op_sel:[1,0,0]
	v_pk_fma_f16 v181, v197, v203, v181
	v_cvt_scalef32_pk_f16_fp4 v196, v23, 1.0 op_sel:[0,1,0]
	v_pk_fma_f16 v182, v194, v203, v182
	v_cvt_scalef32_pk_f16_fp4 v197, v23, 1.0 op_sel:[1,1,0]
	v_pk_fma_f16 v183, v195, v203, v183
	v_cvt_scalef32_pk_f16_fp4 v194, v24, 1.0
	v_pk_fma_f16 v184, v196, v203, v184
	v_cvt_scalef32_pk_f16_fp4 v195, v24, 1.0 op_sel:[1,0,0]
	v_pk_fma_f16 v185, v197, v203, v185
	v_cvt_scalef32_pk_f16_fp4 v196, v24, 1.0 op_sel:[0,1,0]
	v_pk_fma_f16 v186, v194, v203, v186
	v_cvt_scalef32_pk_f16_fp4 v197, v24, 1.0 op_sel:[1,1,0]
	v_pk_fma_f16 v187, v195, v203, v187
	v_cvt_scalef32_pk_f16_fp4 v194, v25, 1.0
	v_pk_fma_f16 v188, v196, v203, v188
	v_cvt_scalef32_pk_f16_fp4 v195, v25, 1.0 op_sel:[1,0,0]
	v_pk_fma_f16 v189, v197, v203, v189
	v_cvt_scalef32_pk_f16_fp4 v196, v25, 1.0 op_sel:[0,1,0]
	v_pk_fma_f16 v190, v194, v203, v190
	v_cvt_scalef32_pk_f16_fp4 v197, v25, 1.0 op_sel:[1,1,0]
	v_pk_fma_f16 v191, v195, v203, v191
	v_pk_fma_f16 v192, v196, v203, v192
	v_pk_fma_f16 v193, v197, v203, v193
	v_mul_u32_u24_sdwa v202, v133, s93 dst_sel:DWORD dst_unused:UNUSED_PAD src0_sel:WORD_0 src1_sel:DWORD
	v_cvt_scalef32_pk_f16_fp4 v194, v26, 1.0
	v_cvt_scalef32_pk_f16_fp4 v195, v26, 1.0 op_sel:[1,0,0]
	v_cvt_scalef32_pk_f16_fp4 v196, v26, 1.0 op_sel:[0,1,0]
	v_pk_fma_f16 v178, v194, v202, v178
	v_cvt_scalef32_pk_f16_fp4 v197, v26, 1.0 op_sel:[1,1,0]
	v_pk_fma_f16 v179, v195, v202, v179
	v_cvt_scalef32_pk_f16_fp4 v194, v27, 1.0
	v_pk_fma_f16 v180, v196, v202, v180
	v_cvt_scalef32_pk_f16_fp4 v195, v27, 1.0 op_sel:[1,0,0]
	v_pk_fma_f16 v181, v197, v202, v181
	v_cvt_scalef32_pk_f16_fp4 v196, v27, 1.0 op_sel:[0,1,0]
	v_pk_fma_f16 v182, v194, v202, v182
	v_cvt_scalef32_pk_f16_fp4 v197, v27, 1.0 op_sel:[1,1,0]
	v_pk_fma_f16 v183, v195, v202, v183
	v_cvt_scalef32_pk_f16_fp4 v194, v28, 1.0
	v_pk_fma_f16 v184, v196, v202, v184
	v_cvt_scalef32_pk_f16_fp4 v195, v28, 1.0 op_sel:[1,0,0]
	v_pk_fma_f16 v185, v197, v202, v185
	v_cvt_scalef32_pk_f16_fp4 v196, v28, 1.0 op_sel:[0,1,0]
	v_pk_fma_f16 v186, v194, v202, v186
	v_cvt_scalef32_pk_f16_fp4 v197, v28, 1.0 op_sel:[1,1,0]
	v_pk_fma_f16 v187, v195, v202, v187
	v_cvt_scalef32_pk_f16_fp4 v194, v29, 1.0
	v_pk_fma_f16 v188, v196, v202, v188
	v_cvt_scalef32_pk_f16_fp4 v195, v29, 1.0 op_sel:[1,0,0]
	v_pk_fma_f16 v189, v197, v202, v189
	v_cvt_scalef32_pk_f16_fp4 v196, v29, 1.0 op_sel:[0,1,0]
	v_pk_fma_f16 v190, v194, v202, v190
	v_cvt_scalef32_pk_f16_fp4 v197, v29, 1.0 op_sel:[1,1,0]
	v_pk_fma_f16 v191, v195, v202, v191
	v_pk_fma_f16 v192, v196, v202, v192
	v_pk_fma_f16 v193, v197, v202, v193
	v_mul_u32_u24_sdwa v203, v133, s93 dst_sel:DWORD dst_unused:UNUSED_PAD src0_sel:WORD_1 src1_sel:DWORD
	v_cvt_scalef32_pk_f16_fp4 v194, v30, 1.0
	v_cvt_scalef32_pk_f16_fp4 v195, v30, 1.0 op_sel:[1,0,0]
	v_cvt_scalef32_pk_f16_fp4 v196, v30, 1.0 op_sel:[0,1,0]
	v_pk_fma_f16 v178, v194, v203, v178
	v_cvt_scalef32_pk_f16_fp4 v197, v30, 1.0 op_sel:[1,1,0]
	v_pk_fma_f16 v179, v195, v203, v179
	v_cvt_scalef32_pk_f16_fp4 v194, v31, 1.0
	v_pk_fma_f16 v180, v196, v203, v180
	v_cvt_scalef32_pk_f16_fp4 v195, v31, 1.0 op_sel:[1,0,0]
	v_pk_fma_f16 v181, v197, v203, v181
	v_cvt_scalef32_pk_f16_fp4 v196, v31, 1.0 op_sel:[0,1,0]
	v_pk_fma_f16 v182, v194, v203, v182
	v_cvt_scalef32_pk_f16_fp4 v197, v31, 1.0 op_sel:[1,1,0]
	v_pk_fma_f16 v183, v195, v203, v183
	v_cvt_scalef32_pk_f16_fp4 v194, v32, 1.0
	v_pk_fma_f16 v184, v196, v203, v184
	v_cvt_scalef32_pk_f16_fp4 v195, v32, 1.0 op_sel:[1,0,0]
	v_pk_fma_f16 v185, v197, v203, v185
	v_cvt_scalef32_pk_f16_fp4 v196, v32, 1.0 op_sel:[0,1,0]
	v_pk_fma_f16 v186, v194, v203, v186
	v_cvt_scalef32_pk_f16_fp4 v197, v32, 1.0 op_sel:[1,1,0]
	v_pk_fma_f16 v187, v195, v203, v187
	v_cvt_scalef32_pk_f16_fp4 v194, v33, 1.0
	v_pk_fma_f16 v188, v196, v203, v188
	v_cvt_scalef32_pk_f16_fp4 v195, v33, 1.0 op_sel:[1,0,0]
	v_pk_fma_f16 v189, v197, v203, v189
	v_cvt_scalef32_pk_f16_fp4 v196, v33, 1.0 op_sel:[0,1,0]
	v_pk_fma_f16 v190, v194, v203, v190
	v_cvt_scalef32_pk_f16_fp4 v197, v33, 1.0 op_sel:[1,1,0]
	v_pk_fma_f16 v191, v195, v203, v191
	v_pk_fma_f16 v192, v196, v203, v192
	v_pk_fma_f16 v193, v197, v203, v193
	v_mul_u32_u24_sdwa v202, v134, s93 dst_sel:DWORD dst_unused:UNUSED_PAD src0_sel:WORD_0 src1_sel:DWORD
	v_cvt_scalef32_pk_f16_fp4 v194, v34, 1.0
	v_cvt_scalef32_pk_f16_fp4 v195, v34, 1.0 op_sel:[1,0,0]
	v_cvt_scalef32_pk_f16_fp4 v196, v34, 1.0 op_sel:[0,1,0]
	v_pk_fma_f16 v178, v194, v202, v178
	v_cvt_scalef32_pk_f16_fp4 v197, v34, 1.0 op_sel:[1,1,0]
	v_pk_fma_f16 v179, v195, v202, v179
	v_cvt_scalef32_pk_f16_fp4 v194, v35, 1.0
	v_pk_fma_f16 v180, v196, v202, v180
	v_cvt_scalef32_pk_f16_fp4 v195, v35, 1.0 op_sel:[1,0,0]
	v_pk_fma_f16 v181, v197, v202, v181
	v_cvt_scalef32_pk_f16_fp4 v196, v35, 1.0 op_sel:[0,1,0]
	v_pk_fma_f16 v182, v194, v202, v182
	v_cvt_scalef32_pk_f16_fp4 v197, v35, 1.0 op_sel:[1,1,0]
	v_pk_fma_f16 v183, v195, v202, v183
	v_cvt_scalef32_pk_f16_fp4 v194, v36, 1.0
	v_pk_fma_f16 v184, v196, v202, v184
	v_cvt_scalef32_pk_f16_fp4 v195, v36, 1.0 op_sel:[1,0,0]
	v_pk_fma_f16 v185, v197, v202, v185
	v_cvt_scalef32_pk_f16_fp4 v196, v36, 1.0 op_sel:[0,1,0]
	v_pk_fma_f16 v186, v194, v202, v186
	v_cvt_scalef32_pk_f16_fp4 v197, v36, 1.0 op_sel:[1,1,0]
	v_pk_fma_f16 v187, v195, v202, v187
	v_cvt_scalef32_pk_f16_fp4 v194, v37, 1.0
	v_pk_fma_f16 v188, v196, v202, v188
	v_cvt_scalef32_pk_f16_fp4 v195, v37, 1.0 op_sel:[1,0,0]
	v_pk_fma_f16 v189, v197, v202, v189
	v_cvt_scalef32_pk_f16_fp4 v196, v37, 1.0 op_sel:[0,1,0]
	v_pk_fma_f16 v190, v194, v202, v190
	v_cvt_scalef32_pk_f16_fp4 v197, v37, 1.0 op_sel:[1,1,0]
	v_pk_fma_f16 v191, v195, v202, v191
	v_pk_fma_f16 v192, v196, v202, v192
	v_pk_fma_f16 v193, v197, v202, v193
	v_mul_u32_u24_sdwa v203, v134, s93 dst_sel:DWORD dst_unused:UNUSED_PAD src0_sel:WORD_1 src1_sel:DWORD
	v_cvt_scalef32_pk_f16_fp4 v194, v38, 1.0
	v_cvt_scalef32_pk_f16_fp4 v195, v38, 1.0 op_sel:[1,0,0]
	v_cvt_scalef32_pk_f16_fp4 v196, v38, 1.0 op_sel:[0,1,0]
	v_pk_fma_f16 v178, v194, v203, v178
	v_cvt_scalef32_pk_f16_fp4 v197, v38, 1.0 op_sel:[1,1,0]
	v_pk_fma_f16 v179, v195, v203, v179
	v_cvt_scalef32_pk_f16_fp4 v194, v39, 1.0
	v_pk_fma_f16 v180, v196, v203, v180
	v_cvt_scalef32_pk_f16_fp4 v195, v39, 1.0 op_sel:[1,0,0]
	v_pk_fma_f16 v181, v197, v203, v181
	v_cvt_scalef32_pk_f16_fp4 v196, v39, 1.0 op_sel:[0,1,0]
	v_pk_fma_f16 v182, v194, v203, v182
	v_cvt_scalef32_pk_f16_fp4 v197, v39, 1.0 op_sel:[1,1,0]
	v_pk_fma_f16 v183, v195, v203, v183
	v_cvt_scalef32_pk_f16_fp4 v194, v40, 1.0
	v_pk_fma_f16 v184, v196, v203, v184
	v_cvt_scalef32_pk_f16_fp4 v195, v40, 1.0 op_sel:[1,0,0]
	v_pk_fma_f16 v185, v197, v203, v185
	v_cvt_scalef32_pk_f16_fp4 v196, v40, 1.0 op_sel:[0,1,0]
	v_pk_fma_f16 v186, v194, v203, v186
	v_cvt_scalef32_pk_f16_fp4 v197, v40, 1.0 op_sel:[1,1,0]
	v_pk_fma_f16 v187, v195, v203, v187
	v_cvt_scalef32_pk_f16_fp4 v194, v41, 1.0
	v_pk_fma_f16 v188, v196, v203, v188
	v_cvt_scalef32_pk_f16_fp4 v195, v41, 1.0 op_sel:[1,0,0]
	v_pk_fma_f16 v189, v197, v203, v189
	v_cvt_scalef32_pk_f16_fp4 v196, v41, 1.0 op_sel:[0,1,0]
	v_pk_fma_f16 v190, v194, v203, v190
	v_cvt_scalef32_pk_f16_fp4 v197, v41, 1.0 op_sel:[1,1,0]
	v_pk_fma_f16 v191, v195, v203, v191
	v_pk_fma_f16 v192, v196, v203, v192
	v_pk_fma_f16 v193, v197, v203, v193
	v_mul_u32_u24_sdwa v202, v135, s93 dst_sel:DWORD dst_unused:UNUSED_PAD src0_sel:WORD_0 src1_sel:DWORD
	v_cvt_scalef32_pk_f16_fp4 v194, v42, 1.0
	v_cvt_scalef32_pk_f16_fp4 v195, v42, 1.0 op_sel:[1,0,0]
	v_cvt_scalef32_pk_f16_fp4 v196, v42, 1.0 op_sel:[0,1,0]
	v_pk_fma_f16 v178, v194, v202, v178
	v_cvt_scalef32_pk_f16_fp4 v197, v42, 1.0 op_sel:[1,1,0]
	v_pk_fma_f16 v179, v195, v202, v179
	v_cvt_scalef32_pk_f16_fp4 v194, v43, 1.0
	v_pk_fma_f16 v180, v196, v202, v180
	v_cvt_scalef32_pk_f16_fp4 v195, v43, 1.0 op_sel:[1,0,0]
	v_pk_fma_f16 v181, v197, v202, v181
	v_cvt_scalef32_pk_f16_fp4 v196, v43, 1.0 op_sel:[0,1,0]
	v_pk_fma_f16 v182, v194, v202, v182
	v_cvt_scalef32_pk_f16_fp4 v197, v43, 1.0 op_sel:[1,1,0]
	v_pk_fma_f16 v183, v195, v202, v183
	v_cvt_scalef32_pk_f16_fp4 v194, v44, 1.0
	v_pk_fma_f16 v184, v196, v202, v184
	v_cvt_scalef32_pk_f16_fp4 v195, v44, 1.0 op_sel:[1,0,0]
	v_pk_fma_f16 v185, v197, v202, v185
	v_cvt_scalef32_pk_f16_fp4 v196, v44, 1.0 op_sel:[0,1,0]
	v_pk_fma_f16 v186, v194, v202, v186
	v_cvt_scalef32_pk_f16_fp4 v197, v44, 1.0 op_sel:[1,1,0]
	v_pk_fma_f16 v187, v195, v202, v187
	v_cvt_scalef32_pk_f16_fp4 v194, v45, 1.0
	v_pk_fma_f16 v188, v196, v202, v188
	v_cvt_scalef32_pk_f16_fp4 v195, v45, 1.0 op_sel:[1,0,0]
	v_pk_fma_f16 v189, v197, v202, v189
	v_cvt_scalef32_pk_f16_fp4 v196, v45, 1.0 op_sel:[0,1,0]
	v_pk_fma_f16 v190, v194, v202, v190
	v_cvt_scalef32_pk_f16_fp4 v197, v45, 1.0 op_sel:[1,1,0]
	v_pk_fma_f16 v191, v195, v202, v191
	v_pk_fma_f16 v192, v196, v202, v192
	v_pk_fma_f16 v193, v197, v202, v193
	v_mul_u32_u24_sdwa v203, v135, s93 dst_sel:DWORD dst_unused:UNUSED_PAD src0_sel:WORD_1 src1_sel:DWORD
	v_cvt_scalef32_pk_f16_fp4 v194, v46, 1.0
	v_cvt_scalef32_pk_f16_fp4 v195, v46, 1.0 op_sel:[1,0,0]
	v_cvt_scalef32_pk_f16_fp4 v196, v46, 1.0 op_sel:[0,1,0]
	v_pk_fma_f16 v178, v194, v203, v178
	v_cvt_scalef32_pk_f16_fp4 v197, v46, 1.0 op_sel:[1,1,0]
	v_pk_fma_f16 v179, v195, v203, v179
	v_cvt_scalef32_pk_f16_fp4 v194, v47, 1.0
	v_pk_fma_f16 v180, v196, v203, v180
	v_cvt_scalef32_pk_f16_fp4 v195, v47, 1.0 op_sel:[1,0,0]
	v_pk_fma_f16 v181, v197, v203, v181
	v_cvt_scalef32_pk_f16_fp4 v196, v47, 1.0 op_sel:[0,1,0]
	v_pk_fma_f16 v182, v194, v203, v182
	v_cvt_scalef32_pk_f16_fp4 v197, v47, 1.0 op_sel:[1,1,0]
	v_pk_fma_f16 v183, v195, v203, v183
	v_cvt_scalef32_pk_f16_fp4 v194, v48, 1.0
	v_pk_fma_f16 v184, v196, v203, v184
	v_cvt_scalef32_pk_f16_fp4 v195, v48, 1.0 op_sel:[1,0,0]
	v_pk_fma_f16 v185, v197, v203, v185
	v_cvt_scalef32_pk_f16_fp4 v196, v48, 1.0 op_sel:[0,1,0]
	v_pk_fma_f16 v186, v194, v203, v186
	v_cvt_scalef32_pk_f16_fp4 v197, v48, 1.0 op_sel:[1,1,0]
	v_pk_fma_f16 v187, v195, v203, v187
	v_cvt_scalef32_pk_f16_fp4 v194, v49, 1.0
	v_pk_fma_f16 v188, v196, v203, v188
	v_cvt_scalef32_pk_f16_fp4 v195, v49, 1.0 op_sel:[1,0,0]
	v_pk_fma_f16 v189, v197, v203, v189
	v_cvt_scalef32_pk_f16_fp4 v196, v49, 1.0 op_sel:[0,1,0]
	v_pk_fma_f16 v190, v194, v203, v190
	v_cvt_scalef32_pk_f16_fp4 v197, v49, 1.0 op_sel:[1,1,0]
	v_pk_fma_f16 v191, v195, v203, v191
	v_pk_fma_f16 v192, v196, v203, v192
	v_pk_fma_f16 v193, v197, v203, v193
	v_mul_u32_u24_sdwa v202, v136, s93 dst_sel:DWORD dst_unused:UNUSED_PAD src0_sel:WORD_0 src1_sel:DWORD
	v_cvt_scalef32_pk_f16_fp4 v194, v50, 1.0
	v_cvt_scalef32_pk_f16_fp4 v195, v50, 1.0 op_sel:[1,0,0]
	v_cvt_scalef32_pk_f16_fp4 v196, v50, 1.0 op_sel:[0,1,0]
	v_pk_fma_f16 v178, v194, v202, v178
	v_cvt_scalef32_pk_f16_fp4 v197, v50, 1.0 op_sel:[1,1,0]
	v_pk_fma_f16 v179, v195, v202, v179
	v_cvt_scalef32_pk_f16_fp4 v194, v51, 1.0
	v_pk_fma_f16 v180, v196, v202, v180
	v_cvt_scalef32_pk_f16_fp4 v195, v51, 1.0 op_sel:[1,0,0]
	v_pk_fma_f16 v181, v197, v202, v181
	v_cvt_scalef32_pk_f16_fp4 v196, v51, 1.0 op_sel:[0,1,0]
	v_pk_fma_f16 v182, v194, v202, v182
	v_cvt_scalef32_pk_f16_fp4 v197, v51, 1.0 op_sel:[1,1,0]
	v_pk_fma_f16 v183, v195, v202, v183
	v_cvt_scalef32_pk_f16_fp4 v194, v52, 1.0
	v_pk_fma_f16 v184, v196, v202, v184
	v_cvt_scalef32_pk_f16_fp4 v195, v52, 1.0 op_sel:[1,0,0]
	v_pk_fma_f16 v185, v197, v202, v185
	v_cvt_scalef32_pk_f16_fp4 v196, v52, 1.0 op_sel:[0,1,0]
	v_pk_fma_f16 v186, v194, v202, v186
	v_cvt_scalef32_pk_f16_fp4 v197, v52, 1.0 op_sel:[1,1,0]
	v_pk_fma_f16 v187, v195, v202, v187
	v_cvt_scalef32_pk_f16_fp4 v194, v53, 1.0
	v_pk_fma_f16 v188, v196, v202, v188
	v_cvt_scalef32_pk_f16_fp4 v195, v53, 1.0 op_sel:[1,0,0]
	v_pk_fma_f16 v189, v197, v202, v189
	v_cvt_scalef32_pk_f16_fp4 v196, v53, 1.0 op_sel:[0,1,0]
	v_pk_fma_f16 v190, v194, v202, v190
	v_cvt_scalef32_pk_f16_fp4 v197, v53, 1.0 op_sel:[1,1,0]
	v_pk_fma_f16 v191, v195, v202, v191
	v_pk_fma_f16 v192, v196, v202, v192
	v_pk_fma_f16 v193, v197, v202, v193
	v_mul_u32_u24_sdwa v203, v136, s93 dst_sel:DWORD dst_unused:UNUSED_PAD src0_sel:WORD_1 src1_sel:DWORD
	v_cvt_scalef32_pk_f16_fp4 v194, v54, 1.0
	v_cvt_scalef32_pk_f16_fp4 v195, v54, 1.0 op_sel:[1,0,0]
	v_cvt_scalef32_pk_f16_fp4 v196, v54, 1.0 op_sel:[0,1,0]
	v_pk_fma_f16 v178, v194, v203, v178
	v_cvt_scalef32_pk_f16_fp4 v197, v54, 1.0 op_sel:[1,1,0]
	v_pk_fma_f16 v179, v195, v203, v179
	v_cvt_scalef32_pk_f16_fp4 v194, v55, 1.0
	v_pk_fma_f16 v180, v196, v203, v180
	v_cvt_scalef32_pk_f16_fp4 v195, v55, 1.0 op_sel:[1,0,0]
	v_pk_fma_f16 v181, v197, v203, v181
	v_cvt_scalef32_pk_f16_fp4 v196, v55, 1.0 op_sel:[0,1,0]
	v_pk_fma_f16 v182, v194, v203, v182
	v_cvt_scalef32_pk_f16_fp4 v197, v55, 1.0 op_sel:[1,1,0]
	v_pk_fma_f16 v183, v195, v203, v183
	v_cvt_scalef32_pk_f16_fp4 v194, v56, 1.0
	v_pk_fma_f16 v184, v196, v203, v184
	v_cvt_scalef32_pk_f16_fp4 v195, v56, 1.0 op_sel:[1,0,0]
	v_pk_fma_f16 v185, v197, v203, v185
	v_cvt_scalef32_pk_f16_fp4 v196, v56, 1.0 op_sel:[0,1,0]
	v_pk_fma_f16 v186, v194, v203, v186
	v_cvt_scalef32_pk_f16_fp4 v197, v56, 1.0 op_sel:[1,1,0]
	v_pk_fma_f16 v187, v195, v203, v187
	v_cvt_scalef32_pk_f16_fp4 v194, v57, 1.0
	v_pk_fma_f16 v188, v196, v203, v188
	v_cvt_scalef32_pk_f16_fp4 v195, v57, 1.0 op_sel:[1,0,0]
	v_pk_fma_f16 v189, v197, v203, v189
	v_cvt_scalef32_pk_f16_fp4 v196, v57, 1.0 op_sel:[0,1,0]
	v_pk_fma_f16 v190, v194, v203, v190
	v_cvt_scalef32_pk_f16_fp4 v197, v57, 1.0 op_sel:[1,1,0]
	v_pk_fma_f16 v191, v195, v203, v191
	v_pk_fma_f16 v192, v196, v203, v192
	v_pk_fma_f16 v193, v197, v203, v193
	v_mul_u32_u24_sdwa v202, v137, s93 dst_sel:DWORD dst_unused:UNUSED_PAD src0_sel:WORD_0 src1_sel:DWORD
	v_cvt_scalef32_pk_f16_fp4 v194, v58, 1.0
	v_cvt_scalef32_pk_f16_fp4 v195, v58, 1.0 op_sel:[1,0,0]
	v_cvt_scalef32_pk_f16_fp4 v196, v58, 1.0 op_sel:[0,1,0]
	v_pk_fma_f16 v178, v194, v202, v178
	v_cvt_scalef32_pk_f16_fp4 v197, v58, 1.0 op_sel:[1,1,0]
	v_pk_fma_f16 v179, v195, v202, v179
	v_cvt_scalef32_pk_f16_fp4 v194, v59, 1.0
	v_pk_fma_f16 v180, v196, v202, v180
	v_cvt_scalef32_pk_f16_fp4 v195, v59, 1.0 op_sel:[1,0,0]
	v_pk_fma_f16 v181, v197, v202, v181
	v_cvt_scalef32_pk_f16_fp4 v196, v59, 1.0 op_sel:[0,1,0]
	v_pk_fma_f16 v182, v194, v202, v182
	v_cvt_scalef32_pk_f16_fp4 v197, v59, 1.0 op_sel:[1,1,0]
	v_pk_fma_f16 v183, v195, v202, v183
	v_cvt_scalef32_pk_f16_fp4 v194, v60, 1.0
	v_pk_fma_f16 v184, v196, v202, v184
	v_cvt_scalef32_pk_f16_fp4 v195, v60, 1.0 op_sel:[1,0,0]
	v_pk_fma_f16 v185, v197, v202, v185
	v_cvt_scalef32_pk_f16_fp4 v196, v60, 1.0 op_sel:[0,1,0]
	v_pk_fma_f16 v186, v194, v202, v186
	v_cvt_scalef32_pk_f16_fp4 v197, v60, 1.0 op_sel:[1,1,0]
	v_pk_fma_f16 v187, v195, v202, v187
	v_cvt_scalef32_pk_f16_fp4 v194, v61, 1.0
	v_pk_fma_f16 v188, v196, v202, v188
	v_cvt_scalef32_pk_f16_fp4 v195, v61, 1.0 op_sel:[1,0,0]
	v_pk_fma_f16 v189, v197, v202, v189
	v_cvt_scalef32_pk_f16_fp4 v196, v61, 1.0 op_sel:[0,1,0]
	v_pk_fma_f16 v190, v194, v202, v190
	v_cvt_scalef32_pk_f16_fp4 v197, v61, 1.0 op_sel:[1,1,0]
	v_pk_fma_f16 v191, v195, v202, v191
	v_pk_fma_f16 v192, v196, v202, v192
	v_pk_fma_f16 v193, v197, v202, v193
	v_mul_u32_u24_sdwa v203, v137, s93 dst_sel:DWORD dst_unused:UNUSED_PAD src0_sel:WORD_1 src1_sel:DWORD
	v_cvt_scalef32_pk_f16_fp4 v194, v62, 1.0
	v_cvt_scalef32_pk_f16_fp4 v195, v62, 1.0 op_sel:[1,0,0]
	v_cvt_scalef32_pk_f16_fp4 v196, v62, 1.0 op_sel:[0,1,0]
	v_pk_fma_f16 v178, v194, v203, v178
	v_cvt_scalef32_pk_f16_fp4 v197, v62, 1.0 op_sel:[1,1,0]
	v_pk_fma_f16 v179, v195, v203, v179
	v_cvt_scalef32_pk_f16_fp4 v194, v63, 1.0
	v_pk_fma_f16 v180, v196, v203, v180
	v_cvt_scalef32_pk_f16_fp4 v195, v63, 1.0 op_sel:[1,0,0]
	v_pk_fma_f16 v181, v197, v203, v181
	v_cvt_scalef32_pk_f16_fp4 v196, v63, 1.0 op_sel:[0,1,0]
	v_pk_fma_f16 v182, v194, v203, v182
	v_cvt_scalef32_pk_f16_fp4 v197, v63, 1.0 op_sel:[1,1,0]
	v_pk_fma_f16 v183, v195, v203, v183
	v_cvt_scalef32_pk_f16_fp4 v194, v64, 1.0
	v_pk_fma_f16 v184, v196, v203, v184
	v_cvt_scalef32_pk_f16_fp4 v195, v64, 1.0 op_sel:[1,0,0]
	v_pk_fma_f16 v185, v197, v203, v185
	v_cvt_scalef32_pk_f16_fp4 v196, v64, 1.0 op_sel:[0,1,0]
	v_pk_fma_f16 v186, v194, v203, v186
	v_cvt_scalef32_pk_f16_fp4 v197, v64, 1.0 op_sel:[1,1,0]
	v_pk_fma_f16 v187, v195, v203, v187
	v_cvt_scalef32_pk_f16_fp4 v194, v65, 1.0
	v_pk_fma_f16 v188, v196, v203, v188
	v_cvt_scalef32_pk_f16_fp4 v195, v65, 1.0 op_sel:[1,0,0]
	v_pk_fma_f16 v189, v197, v203, v189
	v_cvt_scalef32_pk_f16_fp4 v196, v65, 1.0 op_sel:[0,1,0]
	v_pk_fma_f16 v190, v194, v203, v190
	v_cvt_scalef32_pk_f16_fp4 v197, v65, 1.0 op_sel:[1,1,0]
	v_pk_fma_f16 v191, v195, v203, v191
	v_pk_fma_f16 v192, v196, v203, v192
	v_pk_fma_f16 v193, v197, v203, v193
	s_nop 1
	v_permlane32_swap_b32_e32 v178, v186
	v_permlane32_swap_b32_e32 v179, v187
	v_permlane32_swap_b32_e32 v180, v188
	v_permlane32_swap_b32_e32 v181, v189
	v_permlane32_swap_b32_e32 v182, v190
	v_permlane32_swap_b32_e32 v183, v191
	v_permlane32_swap_b32_e32 v184, v192
	v_permlane32_swap_b32_e32 v185, v193
	v_pk_add_f16 v2, v178, v186
	v_pk_add_f16 v3, v179, v187
	v_pk_add_f16 v4, v180, v188
	v_pk_add_f16 v5, v181, v189
	v_pk_add_f16 v6, v182, v190
	v_pk_add_f16 v7, v183, v191
	v_pk_add_f16 v8, v184, v192
	v_pk_add_f16 v9, v185, v193
	v_cvt_f32_f16_e32 v10, v2
	v_cvt_f32_f16_sdwa v11, v2 dst_sel:DWORD dst_unused:UNUSED_PAD src0_sel:WORD_1
	v_cvt_f32_f16_e32 v12, v3
	v_cvt_f32_f16_sdwa v13, v3 dst_sel:DWORD dst_unused:UNUSED_PAD src0_sel:WORD_1
	v_cvt_f32_f16_e32 v14, v4
	v_cvt_f32_f16_sdwa v15, v4 dst_sel:DWORD dst_unused:UNUSED_PAD src0_sel:WORD_1
	v_cvt_f32_f16_e32 v16, v5
	v_cvt_f32_f16_sdwa v17, v5 dst_sel:DWORD dst_unused:UNUSED_PAD src0_sel:WORD_1
	v_cvt_f32_f16_e32 v18, v6
	v_cvt_f32_f16_sdwa v19, v6 dst_sel:DWORD dst_unused:UNUSED_PAD src0_sel:WORD_1
	v_cvt_f32_f16_e32 v20, v7
	v_cvt_f32_f16_sdwa v21, v7 dst_sel:DWORD dst_unused:UNUSED_PAD src0_sel:WORD_1
	v_cvt_f32_f16_e32 v22, v8
	v_cvt_f32_f16_sdwa v23, v8 dst_sel:DWORD dst_unused:UNUSED_PAD src0_sel:WORD_1
	v_cvt_f32_f16_e32 v24, v9
	v_cvt_f32_f16_sdwa v25, v9 dst_sel:DWORD dst_unused:UNUSED_PAD src0_sel:WORD_1
	s_nop 1
	v_permlane16_swap_b32_e32 v10, v18
	v_permlane16_swap_b32_e32 v11, v19
	v_permlane16_swap_b32_e32 v12, v20
	v_permlane16_swap_b32_e32 v13, v21
	v_permlane16_swap_b32_e32 v14, v22
	v_permlane16_swap_b32_e32 v15, v23
	v_permlane16_swap_b32_e32 v16, v24
	v_permlane16_swap_b32_e32 v17, v25
	v_add_f32_e32 v26, v10, v18
	v_add_f32_e32 v27, v11, v19
	v_add_f32_e32 v28, v12, v20
	v_add_f32_e32 v29, v13, v21
	v_add_f32_e32 v30, v14, v22
	v_add_f32_e32 v31, v15, v23
	v_add_f32_e32 v32, v16, v24
	v_add_f32_e32 v33, v17, v25
	s_nop 1
	v_add_f32_dpp v34, v26, v26 row_ror:8 row_mask:0xf bank_mask:0xf bound_ctrl:1
	v_add_f32_dpp v35, v30, v30 row_ror:8 row_mask:0xf bank_mask:0xf bound_ctrl:1
	v_add_f32_dpp v36, v27, v27 row_ror:8 row_mask:0xf bank_mask:0xf bound_ctrl:1
	v_add_f32_dpp v37, v31, v31 row_ror:8 row_mask:0xf bank_mask:0xf bound_ctrl:1
	v_add_f32_dpp v38, v28, v28 row_ror:8 row_mask:0xf bank_mask:0xf bound_ctrl:1
	v_add_f32_dpp v39, v32, v32 row_ror:8 row_mask:0xf bank_mask:0xf bound_ctrl:1
	v_add_f32_dpp v40, v29, v29 row_ror:8 row_mask:0xf bank_mask:0xf bound_ctrl:1
	v_add_f32_dpp v41, v33, v33 row_ror:8 row_mask:0xf bank_mask:0xf bound_ctrl:1
	v_cndmask_b32_e64 v42, v35, v34, s[38:39]
	v_cndmask_b32_e64 v43, v37, v36, s[38:39]
	v_cndmask_b32_e64 v44, v39, v38, s[38:39]
	v_cndmask_b32_e64 v45, v41, v40, s[38:39]
	v_fma_f32 v46, v150, v42, v146
	v_fma_f32 v47, v151, v43, v147
	v_fma_f32 v48, v152, v44, v148
	v_fma_f32 v49, v153, v45, v149
	global_store_dwordx4 v[238:239], v[46:49], off
	s_waitcnt vmcnt(1)
	s_cmp_lt_u32 s33, 6
	s_cbranch_scc1 .Le2_B_issue
	s_cmp_lt_i32 s35, 0
	s_cbranch_scc1 .Le2_B_done
.Le2_B_issue:
	v_and_b32_e32 v194, 0xffff, v162
	v_lshrrev_b32_e32 v195, 16, v162
	v_lshl_add_u32 v194, v194, 7, v218
	v_lshl_add_u32 v195, v195, 7, v218
	global_load_dwordx4 v[2:5], v194, s[40:41]
	global_load_dwordx4 v[6:9], v195, s[40:41]
	v_and_b32_e32 v194, 0xffff, v163
	v_lshrrev_b32_e32 v195, 16, v163
	v_lshl_add_u32 v194, v194, 7, v218
	v_lshl_add_u32 v195, v195, 7, v218
	global_load_dwordx4 v[10:13], v194, s[40:41]
	global_load_dwordx4 v[14:17], v195, s[40:41]
	v_and_b32_e32 v194, 0xffff, v164
	v_lshrrev_b32_e32 v195, 16, v164
	v_lshl_add_u32 v194, v194, 7, v218
	v_lshl_add_u32 v195, v195, 7, v218
	global_load_dwordx4 v[18:21], v194, s[40:41]
	global_load_dwordx4 v[22:25], v195, s[40:41]
	v_and_b32_e32 v194, 0xffff, v165
	v_lshrrev_b32_e32 v195, 16, v165
	v_lshl_add_u32 v194, v194, 7, v218
	v_lshl_add_u32 v195, v195, 7, v218
	global_load_dwordx4 v[26:29], v194, s[40:41]
	global_load_dwordx4 v[30:33], v195, s[40:41]
	v_and_b32_e32 v194, 0xffff, v166
	v_lshrrev_b32_e32 v195, 16, v166
	v_lshl_add_u32 v194, v194, 7, v218
	v_lshl_add_u32 v195, v195, 7, v218
	global_load_dwordx4 v[34:37], v194, s[40:41]
	global_load_dwordx4 v[38:41], v195, s[40:41]
	v_and_b32_e32 v194, 0xffff, v167
	v_lshrrev_b32_e32 v195, 16, v167
	v_lshl_add_u32 v194, v194, 7, v218
	v_lshl_add_u32 v195, v195, 7, v218
	global_load_dwordx4 v[42:45], v194, s[40:41]
	global_load_dwordx4 v[46:49], v195, s[40:41]
	v_and_b32_e32 v194, 0xffff, v168
	v_lshrrev_b32_e32 v195, 16, v168
	v_lshl_add_u32 v194, v194, 7, v218
	v_lshl_add_u32 v195, v195, 7, v218
	global_load_dwordx4 v[50:53], v194, s[40:41]
	global_load_dwordx4 v[54:57], v195, s[40:41]
	v_and_b32_e32 v194, 0xffff, v169
	v_lshrrev_b32_e32 v195, 16, v169
	v_lshl_add_u32 v194, v194, 7, v218
	v_lshl_add_u32 v195, v195, 7, v218
	global_load_dwordx4 v[58:61], v194, s[40:41]
	global_load_dwordx4 v[62:65], v195, s[40:41]
	global_load_dwordx4 v[130:133], v219, s[56:57] offset:-272
	global_load_dwordx4 v[134:137], v219, s[56:57] offset:-256
	v_add_u32_e32 v250, 2, v226
	v_mul_hi_i32 v242, v250, s69
	v_lshrrev_b32_e32 v243, 31, v242
	v_ashrrev_i32_e32 v242, 13, v242
	v_add_u32_e32 v243, v242, v243
	v_mul_i32_i24_e32 v246, 0xffffbf00, v243
	v_add_u32_e32 v242, v250, v246
	v_cmp_gt_i32_e32 vcc, s68, v242
	v_cmp_lt_i32_e64 s[0:1], s21, v242
	s_and_saveexec_b64 s[2:3], s[0:1]
	s_xor_b64 s[0:1], exec, s[2:3]
	v_lshl_add_u32 v242, v243, 14, v246
	v_add3_u32 v242, v250, v242, s88
	s_or_saveexec_b64 s[0:1], s[0:1]
	v_mov_b64_e32 v[244:245], s[18:19]
	s_xor_b64 exec, exec, s[0:1]
	v_lshlrev_b32_e32 v242, 8, v243
	v_add3_u32 v242, v246, v250, v242
	v_mov_b64_e32 v[244:245], s[72:73]
	s_or_b64 exec, exec, s[0:1]
	v_mul_i32_i24_e32 v243, 0x3000, v243
	v_cndmask_b32_e32 v246, v243, v223, vcc
	v_ashrrev_i32_e32 v247, 31, v246
	v_lshl_add_u64 v[246:247], v[246:247], 2, s[10:11]
	v_ashrrev_i32_e32 v243, 31, v242
	v_lshl_add_u64 v[248:249], v[246:247], 0, v[236:237]
	v_lshlrev_b64 v[242:243], 13, v[242:243]
	v_lshl_add_u64 v[242:243], v[244:245], 0, v[242:243]
	v_add_co_u32_e32 v248, vcc, s94, v248
	v_lshl_add_u64 v[238:239], v[242:243], 0, v[236:237]
	s_nop 0
	v_addc_co_u32_e32 v249, vcc, 0, v249, vcc
	global_load_dwordx4 v[146:149], v[238:239], off
	global_load_dwordx4 v[150:153], v[248:249], off
	s_cmp_lt_u32 s33, 6
	s_cbranch_scc0 .Le2_B_noids
	global_load_dwordx4 v[170:173], v219, s[22:23] offset:256
	global_load_dwordx4 v[174:177], v219, s[22:23] offset:272
.Le2_B_noids:
	v_add_u32_e32 v219, 0x200, v219
	s_cmp_eq_u32 s33, 4
	s_cbranch_scc0 .Le2_B_done
	s_and_saveexec_b64 s[0:1], s[44:45]
	s_cbranch_execz .Le2_B_nopub
	v_mov_b32_e32 v198, s92
	ds_write_b32 v198, v251
.Le2_B_nopub:
	s_or_b64 exec, exec, s[0:1]
	s_waitcnt lgkmcnt(0)
	s_barrier
.Le2_B_done:
	v_mul_u32_u24_sdwa v202, v138, s93 dst_sel:DWORD dst_unused:UNUSED_PAD src0_sel:WORD_0 src1_sel:DWORD
	v_cvt_scalef32_pk_f16_fp4 v194, v66, 1.0
	v_cvt_scalef32_pk_f16_fp4 v195, v66, 1.0 op_sel:[1,0,0]
	v_cvt_scalef32_pk_f16_fp4 v196, v66, 1.0 op_sel:[0,1,0]
	v_pk_fma_f16 v178, v194, v202, 0
	v_cvt_scalef32_pk_f16_fp4 v197, v66, 1.0 op_sel:[1,1,0]
	v_pk_fma_f16 v179, v195, v202, 0
	v_cvt_scalef32_pk_f16_fp4 v194, v67, 1.0
	v_pk_fma_f16 v180, v196, v202, 0
	v_cvt_scalef32_pk_f16_fp4 v195, v67, 1.0 op_sel:[1,0,0]
	v_pk_fma_f16 v181, v197, v202, 0
	v_cvt_scalef32_pk_f16_fp4 v196, v67, 1.0 op_sel:[0,1,0]
	v_pk_fma_f16 v182, v194, v202, 0
	v_cvt_scalef32_pk_f16_fp4 v197, v67, 1.0 op_sel:[1,1,0]
	v_pk_fma_f16 v183, v195, v202, 0
	v_cvt_scalef32_pk_f16_fp4 v194, v68, 1.0
	v_pk_fma_f16 v184, v196, v202, 0
	v_cvt_scalef32_pk_f16_fp4 v195, v68, 1.0 op_sel:[1,0,0]
	v_pk_fma_f16 v185, v197, v202, 0
	v_cvt_scalef32_pk_f16_fp4 v196, v68, 1.0 op_sel:[0,1,0]
	v_pk_fma_f16 v186, v194, v202, 0
	v_cvt_scalef32_pk_f16_fp4 v197, v68, 1.0 op_sel:[1,1,0]
	v_pk_fma_f16 v187, v195, v202, 0
	v_cvt_scalef32_pk_f16_fp4 v194, v69, 1.0
	v_pk_fma_f16 v188, v196, v202, 0
	v_cvt_scalef32_pk_f16_fp4 v195, v69, 1.0 op_sel:[1,0,0]
	v_pk_fma_f16 v189, v197, v202, 0
	v_cvt_scalef32_pk_f16_fp4 v196, v69, 1.0 op_sel:[0,1,0]
	v_pk_fma_f16 v190, v194, v202, 0
	v_cvt_scalef32_pk_f16_fp4 v197, v69, 1.0 op_sel:[1,1,0]
	v_pk_fma_f16 v191, v195, v202, 0
	v_pk_fma_f16 v192, v196, v202, 0
	v_pk_fma_f16 v193, v197, v202, 0
	v_mul_u32_u24_sdwa v203, v138, s93 dst_sel:DWORD dst_unused:UNUSED_PAD src0_sel:WORD_1 src1_sel:DWORD
	v_cvt_scalef32_pk_f16_fp4 v194, v70, 1.0
	v_cvt_scalef32_pk_f16_fp4 v195, v70, 1.0 op_sel:[1,0,0]
	v_cvt_scalef32_pk_f16_fp4 v196, v70, 1.0 op_sel:[0,1,0]
	v_pk_fma_f16 v178, v194, v203, v178
	v_cvt_scalef32_pk_f16_fp4 v197, v70, 1.0 op_sel:[1,1,0]
	v_pk_fma_f16 v179, v195, v203, v179
	v_cvt_scalef32_pk_f16_fp4 v194, v71, 1.0
	v_pk_fma_f16 v180, v196, v203, v180
	v_cvt_scalef32_pk_f16_fp4 v195, v71, 1.0 op_sel:[1,0,0]
	v_pk_fma_f16 v181, v197, v203, v181
	v_cvt_scalef32_pk_f16_fp4 v196, v71, 1.0 op_sel:[0,1,0]
	v_pk_fma_f16 v182, v194, v203, v182
	v_cvt_scalef32_pk_f16_fp4 v197, v71, 1.0 op_sel:[1,1,0]
	v_pk_fma_f16 v183, v195, v203, v183
	v_cvt_scalef32_pk_f16_fp4 v194, v72, 1.0
	v_pk_fma_f16 v184, v196, v203, v184
	v_cvt_scalef32_pk_f16_fp4 v195, v72, 1.0 op_sel:[1,0,0]
	v_pk_fma_f16 v185, v197, v203, v185
	v_cvt_scalef32_pk_f16_fp4 v196, v72, 1.0 op_sel:[0,1,0]
	v_pk_fma_f16 v186, v194, v203, v186
	v_cvt_scalef32_pk_f16_fp4 v197, v72, 1.0 op_sel:[1,1,0]
	v_pk_fma_f16 v187, v195, v203, v187
	v_cvt_scalef32_pk_f16_fp4 v194, v73, 1.0
	v_pk_fma_f16 v188, v196, v203, v188
	v_cvt_scalef32_pk_f16_fp4 v195, v73, 1.0 op_sel:[1,0,0]
	v_pk_fma_f16 v189, v197, v203, v189
	v_cvt_scalef32_pk_f16_fp4 v196, v73, 1.0 op_sel:[0,1,0]
	v_pk_fma_f16 v190, v194, v203, v190
	v_cvt_scalef32_pk_f16_fp4 v197, v73, 1.0 op_sel:[1,1,0]
	v_pk_fma_f16 v191, v195, v203, v191
	v_pk_fma_f16 v192, v196, v203, v192
	v_pk_fma_f16 v193, v197, v203, v193
	v_mul_u32_u24_sdwa v202, v139, s93 dst_sel:DWORD dst_unused:UNUSED_PAD src0_sel:WORD_0 src1_sel:DWORD
	v_cvt_scalef32_pk_f16_fp4 v194, v74, 1.0
	v_cvt_scalef32_pk_f16_fp4 v195, v74, 1.0 op_sel:[1,0,0]
	v_cvt_scalef32_pk_f16_fp4 v196, v74, 1.0 op_sel:[0,1,0]
	v_pk_fma_f16 v178, v194, v202, v178
	v_cvt_scalef32_pk_f16_fp4 v197, v74, 1.0 op_sel:[1,1,0]
	v_pk_fma_f16 v179, v195, v202, v179
	v_cvt_scalef32_pk_f16_fp4 v194, v75, 1.0
	v_pk_fma_f16 v180, v196, v202, v180
	v_cvt_scalef32_pk_f16_fp4 v195, v75, 1.0 op_sel:[1,0,0]
	v_pk_fma_f16 v181, v197, v202, v181
	v_cvt_scalef32_pk_f16_fp4 v196, v75, 1.0 op_sel:[0,1,0]
	v_pk_fma_f16 v182, v194, v202, v182
	v_cvt_scalef32_pk_f16_fp4 v197, v75, 1.0 op_sel:[1,1,0]
	v_pk_fma_f16 v183, v195, v202, v183
	v_cvt_scalef32_pk_f16_fp4 v194, v76, 1.0
	v_pk_fma_f16 v184, v196, v202, v184
	v_cvt_scalef32_pk_f16_fp4 v195, v76, 1.0 op_sel:[1,0,0]
	v_pk_fma_f16 v185, v197, v202, v185
	v_cvt_scalef32_pk_f16_fp4 v196, v76, 1.0 op_sel:[0,1,0]
	v_pk_fma_f16 v186, v194, v202, v186
	v_cvt_scalef32_pk_f16_fp4 v197, v76, 1.0 op_sel:[1,1,0]
	v_pk_fma_f16 v187, v195, v202, v187
	v_cvt_scalef32_pk_f16_fp4 v194, v77, 1.0
	v_pk_fma_f16 v188, v196, v202, v188
	v_cvt_scalef32_pk_f16_fp4 v195, v77, 1.0 op_sel:[1,0,0]
	v_pk_fma_f16 v189, v197, v202, v189
	v_cvt_scalef32_pk_f16_fp4 v196, v77, 1.0 op_sel:[0,1,0]
	v_pk_fma_f16 v190, v194, v202, v190
	v_cvt_scalef32_pk_f16_fp4 v197, v77, 1.0 op_sel:[1,1,0]
	v_pk_fma_f16 v191, v195, v202, v191
	v_pk_fma_f16 v192, v196, v202, v192
	v_pk_fma_f16 v193, v197, v202, v193
	v_mul_u32_u24_sdwa v203, v139, s93 dst_sel:DWORD dst_unused:UNUSED_PAD src0_sel:WORD_1 src1_sel:DWORD
	v_cvt_scalef32_pk_f16_fp4 v194, v78, 1.0
	v_cvt_scalef32_pk_f16_fp4 v195, v78, 1.0 op_sel:[1,0,0]
	v_cvt_scalef32_pk_f16_fp4 v196, v78, 1.0 op_sel:[0,1,0]
	v_pk_fma_f16 v178, v194, v203, v178
	v_cvt_scalef32_pk_f16_fp4 v197, v78, 1.0 op_sel:[1,1,0]
	v_pk_fma_f16 v179, v195, v203, v179
	v_cvt_scalef32_pk_f16_fp4 v194, v79, 1.0
	v_pk_fma_f16 v180, v196, v203, v180
	v_cvt_scalef32_pk_f16_fp4 v195, v79, 1.0 op_sel:[1,0,0]
	v_pk_fma_f16 v181, v197, v203, v181
	v_cvt_scalef32_pk_f16_fp4 v196, v79, 1.0 op_sel:[0,1,0]
	v_pk_fma_f16 v182, v194, v203, v182
	v_cvt_scalef32_pk_f16_fp4 v197, v79, 1.0 op_sel:[1,1,0]
	v_pk_fma_f16 v183, v195, v203, v183
	v_cvt_scalef32_pk_f16_fp4 v194, v80, 1.0
	v_pk_fma_f16 v184, v196, v203, v184
	v_cvt_scalef32_pk_f16_fp4 v195, v80, 1.0 op_sel:[1,0,0]
	v_pk_fma_f16 v185, v197, v203, v185
	v_cvt_scalef32_pk_f16_fp4 v196, v80, 1.0 op_sel:[0,1,0]
	v_pk_fma_f16 v186, v194, v203, v186
	v_cvt_scalef32_pk_f16_fp4 v197, v80, 1.0 op_sel:[1,1,0]
	v_pk_fma_f16 v187, v195, v203, v187
	v_cvt_scalef32_pk_f16_fp4 v194, v81, 1.0
	v_pk_fma_f16 v188, v196, v203, v188
	v_cvt_scalef32_pk_f16_fp4 v195, v81, 1.0 op_sel:[1,0,0]
	v_pk_fma_f16 v189, v197, v203, v189
	v_cvt_scalef32_pk_f16_fp4 v196, v81, 1.0 op_sel:[0,1,0]
	v_pk_fma_f16 v190, v194, v203, v190
	v_cvt_scalef32_pk_f16_fp4 v197, v81, 1.0 op_sel:[1,1,0]
	v_pk_fma_f16 v191, v195, v203, v191
	v_pk_fma_f16 v192, v196, v203, v192
	v_pk_fma_f16 v193, v197, v203, v193
	v_mul_u32_u24_sdwa v202, v140, s93 dst_sel:DWORD dst_unused:UNUSED_PAD src0_sel:WORD_0 src1_sel:DWORD
	v_cvt_scalef32_pk_f16_fp4 v194, v82, 1.0
	v_cvt_scalef32_pk_f16_fp4 v195, v82, 1.0 op_sel:[1,0,0]
	v_cvt_scalef32_pk_f16_fp4 v196, v82, 1.0 op_sel:[0,1,0]
	v_pk_fma_f16 v178, v194, v202, v178
	v_cvt_scalef32_pk_f16_fp4 v197, v82, 1.0 op_sel:[1,1,0]
	v_pk_fma_f16 v179, v195, v202, v179
	v_cvt_scalef32_pk_f16_fp4 v194, v83, 1.0
	v_pk_fma_f16 v180, v196, v202, v180
	v_cvt_scalef32_pk_f16_fp4 v195, v83, 1.0 op_sel:[1,0,0]
	v_pk_fma_f16 v181, v197, v202, v181
	v_cvt_scalef32_pk_f16_fp4 v196, v83, 1.0 op_sel:[0,1,0]
	v_pk_fma_f16 v182, v194, v202, v182
	v_cvt_scalef32_pk_f16_fp4 v197, v83, 1.0 op_sel:[1,1,0]
	v_pk_fma_f16 v183, v195, v202, v183
	v_cvt_scalef32_pk_f16_fp4 v194, v84, 1.0
	v_pk_fma_f16 v184, v196, v202, v184
	v_cvt_scalef32_pk_f16_fp4 v195, v84, 1.0 op_sel:[1,0,0]
	v_pk_fma_f16 v185, v197, v202, v185
	v_cvt_scalef32_pk_f16_fp4 v196, v84, 1.0 op_sel:[0,1,0]
	v_pk_fma_f16 v186, v194, v202, v186
	v_cvt_scalef32_pk_f16_fp4 v197, v84, 1.0 op_sel:[1,1,0]
	v_pk_fma_f16 v187, v195, v202, v187
	v_cvt_scalef32_pk_f16_fp4 v194, v85, 1.0
	v_pk_fma_f16 v188, v196, v202, v188
	v_cvt_scalef32_pk_f16_fp4 v195, v85, 1.0 op_sel:[1,0,0]
	v_pk_fma_f16 v189, v197, v202, v189
	v_cvt_scalef32_pk_f16_fp4 v196, v85, 1.0 op_sel:[0,1,0]
	v_pk_fma_f16 v190, v194, v202, v190
	v_cvt_scalef32_pk_f16_fp4 v197, v85, 1.0 op_sel:[1,1,0]
	v_pk_fma_f16 v191, v195, v202, v191
	v_pk_fma_f16 v192, v196, v202, v192
	v_pk_fma_f16 v193, v197, v202, v193
	v_mul_u32_u24_sdwa v203, v140, s93 dst_sel:DWORD dst_unused:UNUSED_PAD src0_sel:WORD_1 src1_sel:DWORD
	v_cvt_scalef32_pk_f16_fp4 v194, v86, 1.0
	v_cvt_scalef32_pk_f16_fp4 v195, v86, 1.0 op_sel:[1,0,0]
	v_cvt_scalef32_pk_f16_fp4 v196, v86, 1.0 op_sel:[0,1,0]
	v_pk_fma_f16 v178, v194, v203, v178
	v_cvt_scalef32_pk_f16_fp4 v197, v86, 1.0 op_sel:[1,1,0]
	v_pk_fma_f16 v179, v195, v203, v179
	v_cvt_scalef32_pk_f16_fp4 v194, v87, 1.0
	v_pk_fma_f16 v180, v196, v203, v180
	v_cvt_scalef32_pk_f16_fp4 v195, v87, 1.0 op_sel:[1,0,0]
	v_pk_fma_f16 v181, v197, v203, v181
	v_cvt_scalef32_pk_f16_fp4 v196, v87, 1.0 op_sel:[0,1,0]
	v_pk_fma_f16 v182, v194, v203, v182
	v_cvt_scalef32_pk_f16_fp4 v197, v87, 1.0 op_sel:[1,1,0]
	v_pk_fma_f16 v183, v195, v203, v183
	v_cvt_scalef32_pk_f16_fp4 v194, v88, 1.0
	v_pk_fma_f16 v184, v196, v203, v184
	v_cvt_scalef32_pk_f16_fp4 v195, v88, 1.0 op_sel:[1,0,0]
	v_pk_fma_f16 v185, v197, v203, v185
	v_cvt_scalef32_pk_f16_fp4 v196, v88, 1.0 op_sel:[0,1,0]
	v_pk_fma_f16 v186, v194, v203, v186
	v_cvt_scalef32_pk_f16_fp4 v197, v88, 1.0 op_sel:[1,1,0]
	v_pk_fma_f16 v187, v195, v203, v187
	v_cvt_scalef32_pk_f16_fp4 v194, v89, 1.0
	v_pk_fma_f16 v188, v196, v203, v188
	v_cvt_scalef32_pk_f16_fp4 v195, v89, 1.0 op_sel:[1,0,0]
	v_pk_fma_f16 v189, v197, v203, v189
	v_cvt_scalef32_pk_f16_fp4 v196, v89, 1.0 op_sel:[0,1,0]
	v_pk_fma_f16 v190, v194, v203, v190
	v_cvt_scalef32_pk_f16_fp4 v197, v89, 1.0 op_sel:[1,1,0]
	v_pk_fma_f16 v191, v195, v203, v191
	v_pk_fma_f16 v192, v196, v203, v192
	v_pk_fma_f16 v193, v197, v203, v193
	v_mul_u32_u24_sdwa v202, v141, s93 dst_sel:DWORD dst_unused:UNUSED_PAD src0_sel:WORD_0 src1_sel:DWORD
	v_cvt_scalef32_pk_f16_fp4 v194, v90, 1.0
	v_cvt_scalef32_pk_f16_fp4 v195, v90, 1.0 op_sel:[1,0,0]
	v_cvt_scalef32_pk_f16_fp4 v196, v90, 1.0 op_sel:[0,1,0]
	v_pk_fma_f16 v178, v194, v202, v178
	v_cvt_scalef32_pk_f16_fp4 v197, v90, 1.0 op_sel:[1,1,0]
	v_pk_fma_f16 v179, v195, v202, v179
	v_cvt_scalef32_pk_f16_fp4 v194, v91, 1.0
	v_pk_fma_f16 v180, v196, v202, v180
	v_cvt_scalef32_pk_f16_fp4 v195, v91, 1.0 op_sel:[1,0,0]
	v_pk_fma_f16 v181, v197, v202, v181
	v_cvt_scalef32_pk_f16_fp4 v196, v91, 1.0 op_sel:[0,1,0]
	v_pk_fma_f16 v182, v194, v202, v182
	v_cvt_scalef32_pk_f16_fp4 v197, v91, 1.0 op_sel:[1,1,0]
	v_pk_fma_f16 v183, v195, v202, v183
	v_cvt_scalef32_pk_f16_fp4 v194, v92, 1.0
	v_pk_fma_f16 v184, v196, v202, v184
	v_cvt_scalef32_pk_f16_fp4 v195, v92, 1.0 op_sel:[1,0,0]
	v_pk_fma_f16 v185, v197, v202, v185
	v_cvt_scalef32_pk_f16_fp4 v196, v92, 1.0 op_sel:[0,1,0]
	v_pk_fma_f16 v186, v194, v202, v186
	v_cvt_scalef32_pk_f16_fp4 v197, v92, 1.0 op_sel:[1,1,0]
	v_pk_fma_f16 v187, v195, v202, v187
	v_cvt_scalef32_pk_f16_fp4 v194, v93, 1.0
	v_pk_fma_f16 v188, v196, v202, v188
	v_cvt_scalef32_pk_f16_fp4 v195, v93, 1.0 op_sel:[1,0,0]
	v_pk_fma_f16 v189, v197, v202, v189
	v_cvt_scalef32_pk_f16_fp4 v196, v93, 1.0 op_sel:[0,1,0]
	v_pk_fma_f16 v190, v194, v202, v190
	v_cvt_scalef32_pk_f16_fp4 v197, v93, 1.0 op_sel:[1,1,0]
	v_pk_fma_f16 v191, v195, v202, v191
	v_pk_fma_f16 v192, v196, v202, v192
	v_pk_fma_f16 v193, v197, v202, v193
	v_mul_u32_u24_sdwa v203, v141, s93 dst_sel:DWORD dst_unused:UNUSED_PAD src0_sel:WORD_1 src1_sel:DWORD
	v_cvt_scalef32_pk_f16_fp4 v194, v94, 1.0
	v_cvt_scalef32_pk_f16_fp4 v195, v94, 1.0 op_sel:[1,0,0]
	v_cvt_scalef32_pk_f16_fp4 v196, v94, 1.0 op_sel:[0,1,0]
	v_pk_fma_f16 v178, v194, v203, v178
	v_cvt_scalef32_pk_f16_fp4 v197, v94, 1.0 op_sel:[1,1,0]
	v_pk_fma_f16 v179, v195, v203, v179
	v_cvt_scalef32_pk_f16_fp4 v194, v95, 1.0
	v_pk_fma_f16 v180, v196, v203, v180
	v_cvt_scalef32_pk_f16_fp4 v195, v95, 1.0 op_sel:[1,0,0]
	v_pk_fma_f16 v181, v197, v203, v181
	v_cvt_scalef32_pk_f16_fp4 v196, v95, 1.0 op_sel:[0,1,0]
	v_pk_fma_f16 v182, v194, v203, v182
	v_cvt_scalef32_pk_f16_fp4 v197, v95, 1.0 op_sel:[1,1,0]
	v_pk_fma_f16 v183, v195, v203, v183
	v_cvt_scalef32_pk_f16_fp4 v194, v96, 1.0
	v_pk_fma_f16 v184, v196, v203, v184
	v_cvt_scalef32_pk_f16_fp4 v195, v96, 1.0 op_sel:[1,0,0]
	v_pk_fma_f16 v185, v197, v203, v185
	v_cvt_scalef32_pk_f16_fp4 v196, v96, 1.0 op_sel:[0,1,0]
	v_pk_fma_f16 v186, v194, v203, v186
	v_cvt_scalef32_pk_f16_fp4 v197, v96, 1.0 op_sel:[1,1,0]
	v_pk_fma_f16 v187, v195, v203, v187
	v_cvt_scalef32_pk_f16_fp4 v194, v97, 1.0
	v_pk_fma_f16 v188, v196, v203, v188
	v_cvt_scalef32_pk_f16_fp4 v195, v97, 1.0 op_sel:[1,0,0]
	v_pk_fma_f16 v189, v197, v203, v189
	v_cvt_scalef32_pk_f16_fp4 v196, v97, 1.0 op_sel:[0,1,0]
	v_pk_fma_f16 v190, v194, v203, v190
	v_cvt_scalef32_pk_f16_fp4 v197, v97, 1.0 op_sel:[1,1,0]
	v_pk_fma_f16 v191, v195, v203, v191
	v_pk_fma_f16 v192, v196, v203, v192
	v_pk_fma_f16 v193, v197, v203, v193
	v_mul_u32_u24_sdwa v202, v142, s93 dst_sel:DWORD dst_unused:UNUSED_PAD src0_sel:WORD_0 src1_sel:DWORD
	v_cvt_scalef32_pk_f16_fp4 v194, v98, 1.0
	v_cvt_scalef32_pk_f16_fp4 v195, v98, 1.0 op_sel:[1,0,0]
	v_cvt_scalef32_pk_f16_fp4 v196, v98, 1.0 op_sel:[0,1,0]
	v_pk_fma_f16 v178, v194, v202, v178
	v_cvt_scalef32_pk_f16_fp4 v197, v98, 1.0 op_sel:[1,1,0]
	v_pk_fma_f16 v179, v195, v202, v179
	v_cvt_scalef32_pk_f16_fp4 v194, v99, 1.0
	v_pk_fma_f16 v180, v196, v202, v180
	v_cvt_scalef32_pk_f16_fp4 v195, v99, 1.0 op_sel:[1,0,0]
	v_pk_fma_f16 v181, v197, v202, v181
	v_cvt_scalef32_pk_f16_fp4 v196, v99, 1.0 op_sel:[0,1,0]
	v_pk_fma_f16 v182, v194, v202, v182
	v_cvt_scalef32_pk_f16_fp4 v197, v99, 1.0 op_sel:[1,1,0]
	v_pk_fma_f16 v183, v195, v202, v183
	v_cvt_scalef32_pk_f16_fp4 v194, v100, 1.0
	v_pk_fma_f16 v184, v196, v202, v184
	v_cvt_scalef32_pk_f16_fp4 v195, v100, 1.0 op_sel:[1,0,0]
	v_pk_fma_f16 v185, v197, v202, v185
	v_cvt_scalef32_pk_f16_fp4 v196, v100, 1.0 op_sel:[0,1,0]
	v_pk_fma_f16 v186, v194, v202, v186
	v_cvt_scalef32_pk_f16_fp4 v197, v100, 1.0 op_sel:[1,1,0]
	v_pk_fma_f16 v187, v195, v202, v187
	v_cvt_scalef32_pk_f16_fp4 v194, v101, 1.0
	v_pk_fma_f16 v188, v196, v202, v188
	v_cvt_scalef32_pk_f16_fp4 v195, v101, 1.0 op_sel:[1,0,0]
	v_pk_fma_f16 v189, v197, v202, v189
	v_cvt_scalef32_pk_f16_fp4 v196, v101, 1.0 op_sel:[0,1,0]
	v_pk_fma_f16 v190, v194, v202, v190
	v_cvt_scalef32_pk_f16_fp4 v197, v101, 1.0 op_sel:[1,1,0]
	v_pk_fma_f16 v191, v195, v202, v191
	v_pk_fma_f16 v192, v196, v202, v192
	v_pk_fma_f16 v193, v197, v202, v193
	v_mul_u32_u24_sdwa v203, v142, s93 dst_sel:DWORD dst_unused:UNUSED_PAD src0_sel:WORD_1 src1_sel:DWORD
	v_cvt_scalef32_pk_f16_fp4 v194, v102, 1.0
	v_cvt_scalef32_pk_f16_fp4 v195, v102, 1.0 op_sel:[1,0,0]
	v_cvt_scalef32_pk_f16_fp4 v196, v102, 1.0 op_sel:[0,1,0]
	v_pk_fma_f16 v178, v194, v203, v178
	v_cvt_scalef32_pk_f16_fp4 v197, v102, 1.0 op_sel:[1,1,0]
	v_pk_fma_f16 v179, v195, v203, v179
	v_cvt_scalef32_pk_f16_fp4 v194, v103, 1.0
	v_pk_fma_f16 v180, v196, v203, v180
	v_cvt_scalef32_pk_f16_fp4 v195, v103, 1.0 op_sel:[1,0,0]
	v_pk_fma_f16 v181, v197, v203, v181
	v_cvt_scalef32_pk_f16_fp4 v196, v103, 1.0 op_sel:[0,1,0]
	v_pk_fma_f16 v182, v194, v203, v182
	v_cvt_scalef32_pk_f16_fp4 v197, v103, 1.0 op_sel:[1,1,0]
	v_pk_fma_f16 v183, v195, v203, v183
	v_cvt_scalef32_pk_f16_fp4 v194, v104, 1.0
	v_pk_fma_f16 v184, v196, v203, v184
	v_cvt_scalef32_pk_f16_fp4 v195, v104, 1.0 op_sel:[1,0,0]
	v_pk_fma_f16 v185, v197, v203, v185
	v_cvt_scalef32_pk_f16_fp4 v196, v104, 1.0 op_sel:[0,1,0]
	v_pk_fma_f16 v186, v194, v203, v186
	v_cvt_scalef32_pk_f16_fp4 v197, v104, 1.0 op_sel:[1,1,0]
	v_pk_fma_f16 v187, v195, v203, v187
	v_cvt_scalef32_pk_f16_fp4 v194, v105, 1.0
	v_pk_fma_f16 v188, v196, v203, v188
	v_cvt_scalef32_pk_f16_fp4 v195, v105, 1.0 op_sel:[1,0,0]
	v_pk_fma_f16 v189, v197, v203, v189
	v_cvt_scalef32_pk_f16_fp4 v196, v105, 1.0 op_sel:[0,1,0]
	v_pk_fma_f16 v190, v194, v203, v190
	v_cvt_scalef32_pk_f16_fp4 v197, v105, 1.0 op_sel:[1,1,0]
	v_pk_fma_f16 v191, v195, v203, v191
	v_pk_fma_f16 v192, v196, v203, v192
	v_pk_fma_f16 v193, v197, v203, v193
	v_mul_u32_u24_sdwa v202, v143, s93 dst_sel:DWORD dst_unused:UNUSED_PAD src0_sel:WORD_0 src1_sel:DWORD
	v_cvt_scalef32_pk_f16_fp4 v194, v106, 1.0
	v_cvt_scalef32_pk_f16_fp4 v195, v106, 1.0 op_sel:[1,0,0]
	v_cvt_scalef32_pk_f16_fp4 v196, v106, 1.0 op_sel:[0,1,0]
	v_pk_fma_f16 v178, v194, v202, v178
	v_cvt_scalef32_pk_f16_fp4 v197, v106, 1.0 op_sel:[1,1,0]
	v_pk_fma_f16 v179, v195, v202, v179
	v_cvt_scalef32_pk_f16_fp4 v194, v107, 1.0
	v_pk_fma_f16 v180, v196, v202, v180
	v_cvt_scalef32_pk_f16_fp4 v195, v107, 1.0 op_sel:[1,0,0]
	v_pk_fma_f16 v181, v197, v202, v181
	v_cvt_scalef32_pk_f16_fp4 v196, v107, 1.0 op_sel:[0,1,0]
	v_pk_fma_f16 v182, v194, v202, v182
	v_cvt_scalef32_pk_f16_fp4 v197, v107, 1.0 op_sel:[1,1,0]
	v_pk_fma_f16 v183, v195, v202, v183
	v_cvt_scalef32_pk_f16_fp4 v194, v108, 1.0
	v_pk_fma_f16 v184, v196, v202, v184
	v_cvt_scalef32_pk_f16_fp4 v195, v108, 1.0 op_sel:[1,0,0]
	v_pk_fma_f16 v185, v197, v202, v185
	v_cvt_scalef32_pk_f16_fp4 v196, v108, 1.0 op_sel:[0,1,0]
	v_pk_fma_f16 v186, v194, v202, v186
	v_cvt_scalef32_pk_f16_fp4 v197, v108, 1.0 op_sel:[1,1,0]
	v_pk_fma_f16 v187, v195, v202, v187
	v_cvt_scalef32_pk_f16_fp4 v194, v109, 1.0
	v_pk_fma_f16 v188, v196, v202, v188
	v_cvt_scalef32_pk_f16_fp4 v195, v109, 1.0 op_sel:[1,0,0]
	v_pk_fma_f16 v189, v197, v202, v189
	v_cvt_scalef32_pk_f16_fp4 v196, v109, 1.0 op_sel:[0,1,0]
	v_pk_fma_f16 v190, v194, v202, v190
	v_cvt_scalef32_pk_f16_fp4 v197, v109, 1.0 op_sel:[1,1,0]
	v_pk_fma_f16 v191, v195, v202, v191
	v_pk_fma_f16 v192, v196, v202, v192
	v_pk_fma_f16 v193, v197, v202, v193
	v_mul_u32_u24_sdwa v203, v143, s93 dst_sel:DWORD dst_unused:UNUSED_PAD src0_sel:WORD_1 src1_sel:DWORD
	v_cvt_scalef32_pk_f16_fp4 v194, v110, 1.0
	v_cvt_scalef32_pk_f16_fp4 v195, v110, 1.0 op_sel:[1,0,0]
	v_cvt_scalef32_pk_f16_fp4 v196, v110, 1.0 op_sel:[0,1,0]
	v_pk_fma_f16 v178, v194, v203, v178
	v_cvt_scalef32_pk_f16_fp4 v197, v110, 1.0 op_sel:[1,1,0]
	v_pk_fma_f16 v179, v195, v203, v179
	v_cvt_scalef32_pk_f16_fp4 v194, v111, 1.0
	v_pk_fma_f16 v180, v196, v203, v180
	v_cvt_scalef32_pk_f16_fp4 v195, v111, 1.0 op_sel:[1,0,0]
	v_pk_fma_f16 v181, v197, v203, v181
	v_cvt_scalef32_pk_f16_fp4 v196, v111, 1.0 op_sel:[0,1,0]
	v_pk_fma_f16 v182, v194, v203, v182
	v_cvt_scalef32_pk_f16_fp4 v197, v111, 1.0 op_sel:[1,1,0]
	v_pk_fma_f16 v183, v195, v203, v183
	v_cvt_scalef32_pk_f16_fp4 v194, v112, 1.0
	v_pk_fma_f16 v184, v196, v203, v184
	v_cvt_scalef32_pk_f16_fp4 v195, v112, 1.0 op_sel:[1,0,0]
	v_pk_fma_f16 v185, v197, v203, v185
	v_cvt_scalef32_pk_f16_fp4 v196, v112, 1.0 op_sel:[0,1,0]
	v_pk_fma_f16 v186, v194, v203, v186
	v_cvt_scalef32_pk_f16_fp4 v197, v112, 1.0 op_sel:[1,1,0]
	v_pk_fma_f16 v187, v195, v203, v187
	v_cvt_scalef32_pk_f16_fp4 v194, v113, 1.0
	v_pk_fma_f16 v188, v196, v203, v188
	v_cvt_scalef32_pk_f16_fp4 v195, v113, 1.0 op_sel:[1,0,0]
	v_pk_fma_f16 v189, v197, v203, v189
	v_cvt_scalef32_pk_f16_fp4 v196, v113, 1.0 op_sel:[0,1,0]
	v_pk_fma_f16 v190, v194, v203, v190
	v_cvt_scalef32_pk_f16_fp4 v197, v113, 1.0 op_sel:[1,1,0]
	v_pk_fma_f16 v191, v195, v203, v191
	v_pk_fma_f16 v192, v196, v203, v192
	v_pk_fma_f16 v193, v197, v203, v193
	v_mul_u32_u24_sdwa v202, v144, s93 dst_sel:DWORD dst_unused:UNUSED_PAD src0_sel:WORD_0 src1_sel:DWORD
	v_cvt_scalef32_pk_f16_fp4 v194, v114, 1.0
	v_cvt_scalef32_pk_f16_fp4 v195, v114, 1.0 op_sel:[1,0,0]
	v_cvt_scalef32_pk_f16_fp4 v196, v114, 1.0 op_sel:[0,1,0]
	v_pk_fma_f16 v178, v194, v202, v178
	v_cvt_scalef32_pk_f16_fp4 v197, v114, 1.0 op_sel:[1,1,0]
	v_pk_fma_f16 v179, v195, v202, v179
	v_cvt_scalef32_pk_f16_fp4 v194, v115, 1.0
	v_pk_fma_f16 v180, v196, v202, v180
	v_cvt_scalef32_pk_f16_fp4 v195, v115, 1.0 op_sel:[1,0,0]
	v_pk_fma_f16 v181, v197, v202, v181
	v_cvt_scalef32_pk_f16_fp4 v196, v115, 1.0 op_sel:[0,1,0]
	v_pk_fma_f16 v182, v194, v202, v182
	v_cvt_scalef32_pk_f16_fp4 v197, v115, 1.0 op_sel:[1,1,0]
	v_pk_fma_f16 v183, v195, v202, v183
	v_cvt_scalef32_pk_f16_fp4 v194, v116, 1.0
	v_pk_fma_f16 v184, v196, v202, v184
	v_cvt_scalef32_pk_f16_fp4 v195, v116, 1.0 op_sel:[1,0,0]
	v_pk_fma_f16 v185, v197, v202, v185
	v_cvt_scalef32_pk_f16_fp4 v196, v116, 1.0 op_sel:[0,1,0]
	v_pk_fma_f16 v186, v194, v202, v186
	v_cvt_scalef32_pk_f16_fp4 v197, v116, 1.0 op_sel:[1,1,0]
	v_pk_fma_f16 v187, v195, v202, v187
	v_cvt_scalef32_pk_f16_fp4 v194, v117, 1.0
	v_pk_fma_f16 v188, v196, v202, v188
	v_cvt_scalef32_pk_f16_fp4 v195, v117, 1.0 op_sel:[1,0,0]
	v_pk_fma_f16 v189, v197, v202, v189
	v_cvt_scalef32_pk_f16_fp4 v196, v117, 1.0 op_sel:[0,1,0]
	v_pk_fma_f16 v190, v194, v202, v190
	v_cvt_scalef32_pk_f16_fp4 v197, v117, 1.0 op_sel:[1,1,0]
	v_pk_fma_f16 v191, v195, v202, v191
	v_pk_fma_f16 v192, v196, v202, v192
	v_pk_fma_f16 v193, v197, v202, v193
	v_mul_u32_u24_sdwa v203, v144, s93 dst_sel:DWORD dst_unused:UNUSED_PAD src0_sel:WORD_1 src1_sel:DWORD
	v_cvt_scalef32_pk_f16_fp4 v194, v118, 1.0
	v_cvt_scalef32_pk_f16_fp4 v195, v118, 1.0 op_sel:[1,0,0]
	v_cvt_scalef32_pk_f16_fp4 v196, v118, 1.0 op_sel:[0,1,0]
	v_pk_fma_f16 v178, v194, v203, v178
	v_cvt_scalef32_pk_f16_fp4 v197, v118, 1.0 op_sel:[1,1,0]
	v_pk_fma_f16 v179, v195, v203, v179
	v_cvt_scalef32_pk_f16_fp4 v194, v119, 1.0
	v_pk_fma_f16 v180, v196, v203, v180
	v_cvt_scalef32_pk_f16_fp4 v195, v119, 1.0 op_sel:[1,0,0]
	v_pk_fma_f16 v181, v197, v203, v181
	v_cvt_scalef32_pk_f16_fp4 v196, v119, 1.0 op_sel:[0,1,0]
	v_pk_fma_f16 v182, v194, v203, v182
	v_cvt_scalef32_pk_f16_fp4 v197, v119, 1.0 op_sel:[1,1,0]
	v_pk_fma_f16 v183, v195, v203, v183
	v_cvt_scalef32_pk_f16_fp4 v194, v120, 1.0
	v_pk_fma_f16 v184, v196, v203, v184
	v_cvt_scalef32_pk_f16_fp4 v195, v120, 1.0 op_sel:[1,0,0]
	v_pk_fma_f16 v185, v197, v203, v185
	v_cvt_scalef32_pk_f16_fp4 v196, v120, 1.0 op_sel:[0,1,0]
	v_pk_fma_f16 v186, v194, v203, v186
	v_cvt_scalef32_pk_f16_fp4 v197, v120, 1.0 op_sel:[1,1,0]
	v_pk_fma_f16 v187, v195, v203, v187
	v_cvt_scalef32_pk_f16_fp4 v194, v121, 1.0
	v_pk_fma_f16 v188, v196, v203, v188
	v_cvt_scalef32_pk_f16_fp4 v195, v121, 1.0 op_sel:[1,0,0]
	v_pk_fma_f16 v189, v197, v203, v189
	v_cvt_scalef32_pk_f16_fp4 v196, v121, 1.0 op_sel:[0,1,0]
	v_pk_fma_f16 v190, v194, v203, v190
	v_cvt_scalef32_pk_f16_fp4 v197, v121, 1.0 op_sel:[1,1,0]
	v_pk_fma_f16 v191, v195, v203, v191
	v_pk_fma_f16 v192, v196, v203, v192
	v_pk_fma_f16 v193, v197, v203, v193
	v_mul_u32_u24_sdwa v202, v145, s93 dst_sel:DWORD dst_unused:UNUSED_PAD src0_sel:WORD_0 src1_sel:DWORD
	v_cvt_scalef32_pk_f16_fp4 v194, v122, 1.0
	v_cvt_scalef32_pk_f16_fp4 v195, v122, 1.0 op_sel:[1,0,0]
	v_cvt_scalef32_pk_f16_fp4 v196, v122, 1.0 op_sel:[0,1,0]
	v_pk_fma_f16 v178, v194, v202, v178
	v_cvt_scalef32_pk_f16_fp4 v197, v122, 1.0 op_sel:[1,1,0]
	v_pk_fma_f16 v179, v195, v202, v179
	v_cvt_scalef32_pk_f16_fp4 v194, v123, 1.0
	v_pk_fma_f16 v180, v196, v202, v180
	v_cvt_scalef32_pk_f16_fp4 v195, v123, 1.0 op_sel:[1,0,0]
	v_pk_fma_f16 v181, v197, v202, v181
	v_cvt_scalef32_pk_f16_fp4 v196, v123, 1.0 op_sel:[0,1,0]
	v_pk_fma_f16 v182, v194, v202, v182
	v_cvt_scalef32_pk_f16_fp4 v197, v123, 1.0 op_sel:[1,1,0]
	v_pk_fma_f16 v183, v195, v202, v183
	v_cvt_scalef32_pk_f16_fp4 v194, v124, 1.0
	v_pk_fma_f16 v184, v196, v202, v184
	v_cvt_scalef32_pk_f16_fp4 v195, v124, 1.0 op_sel:[1,0,0]
	v_pk_fma_f16 v185, v197, v202, v185
	v_cvt_scalef32_pk_f16_fp4 v196, v124, 1.0 op_sel:[0,1,0]
	v_pk_fma_f16 v186, v194, v202, v186
	v_cvt_scalef32_pk_f16_fp4 v197, v124, 1.0 op_sel:[1,1,0]
	v_pk_fma_f16 v187, v195, v202, v187
	v_cvt_scalef32_pk_f16_fp4 v194, v125, 1.0
	v_pk_fma_f16 v188, v196, v202, v188
	v_cvt_scalef32_pk_f16_fp4 v195, v125, 1.0 op_sel:[1,0,0]
	v_pk_fma_f16 v189, v197, v202, v189
	v_cvt_scalef32_pk_f16_fp4 v196, v125, 1.0 op_sel:[0,1,0]
	v_pk_fma_f16 v190, v194, v202, v190
	v_cvt_scalef32_pk_f16_fp4 v197, v125, 1.0 op_sel:[1,1,0]
	v_pk_fma_f16 v191, v195, v202, v191
	v_pk_fma_f16 v192, v196, v202, v192
	v_pk_fma_f16 v193, v197, v202, v193
	v_mul_u32_u24_sdwa v203, v145, s93 dst_sel:DWORD dst_unused:UNUSED_PAD src0_sel:WORD_1 src1_sel:DWORD
	v_cvt_scalef32_pk_f16_fp4 v194, v126, 1.0
	v_cvt_scalef32_pk_f16_fp4 v195, v126, 1.0 op_sel:[1,0,0]
	v_cvt_scalef32_pk_f16_fp4 v196, v126, 1.0 op_sel:[0,1,0]
	v_pk_fma_f16 v178, v194, v203, v178
	v_cvt_scalef32_pk_f16_fp4 v197, v126, 1.0 op_sel:[1,1,0]
	v_pk_fma_f16 v179, v195, v203, v179
	v_cvt_scalef32_pk_f16_fp4 v194, v127, 1.0
	v_pk_fma_f16 v180, v196, v203, v180
	v_cvt_scalef32_pk_f16_fp4 v195, v127, 1.0 op_sel:[1,0,0]
	v_pk_fma_f16 v181, v197, v203, v181
	v_cvt_scalef32_pk_f16_fp4 v196, v127, 1.0 op_sel:[0,1,0]
	v_pk_fma_f16 v182, v194, v203, v182
	v_cvt_scalef32_pk_f16_fp4 v197, v127, 1.0 op_sel:[1,1,0]
	v_pk_fma_f16 v183, v195, v203, v183
	v_cvt_scalef32_pk_f16_fp4 v194, v128, 1.0
	v_pk_fma_f16 v184, v196, v203, v184
	v_cvt_scalef32_pk_f16_fp4 v195, v128, 1.0 op_sel:[1,0,0]
	v_pk_fma_f16 v185, v197, v203, v185
	v_cvt_scalef32_pk_f16_fp4 v196, v128, 1.0 op_sel:[0,1,0]
	v_pk_fma_f16 v186, v194, v203, v186
	v_cvt_scalef32_pk_f16_fp4 v197, v128, 1.0 op_sel:[1,1,0]
	v_pk_fma_f16 v187, v195, v203, v187
	v_cvt_scalef32_pk_f16_fp4 v194, v129, 1.0
	v_pk_fma_f16 v188, v196, v203, v188
	v_cvt_scalef32_pk_f16_fp4 v195, v129, 1.0 op_sel:[1,0,0]
	v_pk_fma_f16 v189, v197, v203, v189
	v_cvt_scalef32_pk_f16_fp4 v196, v129, 1.0 op_sel:[0,1,0]
	v_pk_fma_f16 v190, v194, v203, v190
	v_cvt_scalef32_pk_f16_fp4 v197, v129, 1.0 op_sel:[1,1,0]
	v_pk_fma_f16 v191, v195, v203, v191
	v_pk_fma_f16 v192, v196, v203, v192
	v_pk_fma_f16 v193, v197, v203, v193
	s_nop 1
	v_permlane32_swap_b32_e32 v178, v186
	v_permlane32_swap_b32_e32 v179, v187
	v_permlane32_swap_b32_e32 v180, v188
	v_permlane32_swap_b32_e32 v181, v189
	v_permlane32_swap_b32_e32 v182, v190
	v_permlane32_swap_b32_e32 v183, v191
	v_permlane32_swap_b32_e32 v184, v192
	v_permlane32_swap_b32_e32 v185, v193
	v_pk_add_f16 v66, v178, v186
	v_pk_add_f16 v67, v179, v187
	v_pk_add_f16 v68, v180, v188
	v_pk_add_f16 v69, v181, v189
	v_pk_add_f16 v70, v182, v190
	v_pk_add_f16 v71, v183, v191
	v_pk_add_f16 v72, v184, v192
	v_pk_add_f16 v73, v185, v193
	v_cvt_f32_f16_e32 v74, v66
	v_cvt_f32_f16_sdwa v75, v66 dst_sel:DWORD dst_unused:UNUSED_PAD src0_sel:WORD_1
	v_cvt_f32_f16_e32 v76, v67
	v_cvt_f32_f16_sdwa v77, v67 dst_sel:DWORD dst_unused:UNUSED_PAD src0_sel:WORD_1
	v_cvt_f32_f16_e32 v78, v68
	v_cvt_f32_f16_sdwa v79, v68 dst_sel:DWORD dst_unused:UNUSED_PAD src0_sel:WORD_1
	v_cvt_f32_f16_e32 v80, v69
	v_cvt_f32_f16_sdwa v81, v69 dst_sel:DWORD dst_unused:UNUSED_PAD src0_sel:WORD_1
	v_cvt_f32_f16_e32 v82, v70
	v_cvt_f32_f16_sdwa v83, v70 dst_sel:DWORD dst_unused:UNUSED_PAD src0_sel:WORD_1
	v_cvt_f32_f16_e32 v84, v71
	v_cvt_f32_f16_sdwa v85, v71 dst_sel:DWORD dst_unused:UNUSED_PAD src0_sel:WORD_1
	v_cvt_f32_f16_e32 v86, v72
	v_cvt_f32_f16_sdwa v87, v72 dst_sel:DWORD dst_unused:UNUSED_PAD src0_sel:WORD_1
	v_cvt_f32_f16_e32 v88, v73
	v_cvt_f32_f16_sdwa v89, v73 dst_sel:DWORD dst_unused:UNUSED_PAD src0_sel:WORD_1
	s_nop 1
	v_permlane16_swap_b32_e32 v74, v82
	v_permlane16_swap_b32_e32 v75, v83
	v_permlane16_swap_b32_e32 v76, v84
	v_permlane16_swap_b32_e32 v77, v85
	v_permlane16_swap_b32_e32 v78, v86
	v_permlane16_swap_b32_e32 v79, v87
	v_permlane16_swap_b32_e32 v80, v88
	v_permlane16_swap_b32_e32 v81, v89
	v_add_f32_e32 v90, v74, v82
	v_add_f32_e32 v91, v75, v83
	v_add_f32_e32 v92, v76, v84
	v_add_f32_e32 v93, v77, v85
	v_add_f32_e32 v94, v78, v86
	v_add_f32_e32 v95, v79, v87
	v_add_f32_e32 v96, v80, v88
	v_add_f32_e32 v97, v81, v89
	s_nop 1
	v_add_f32_dpp v98, v90, v90 row_ror:8 row_mask:0xf bank_mask:0xf bound_ctrl:1
	v_add_f32_dpp v99, v94, v94 row_ror:8 row_mask:0xf bank_mask:0xf bound_ctrl:1
	v_add_f32_dpp v100, v91, v91 row_ror:8 row_mask:0xf bank_mask:0xf bound_ctrl:1
	v_add_f32_dpp v101, v95, v95 row_ror:8 row_mask:0xf bank_mask:0xf bound_ctrl:1
	v_add_f32_dpp v102, v92, v92 row_ror:8 row_mask:0xf bank_mask:0xf bound_ctrl:1
	v_add_f32_dpp v103, v96, v96 row_ror:8 row_mask:0xf bank_mask:0xf bound_ctrl:1
	v_add_f32_dpp v104, v93, v93 row_ror:8 row_mask:0xf bank_mask:0xf bound_ctrl:1
	v_add_f32_dpp v105, v97, v97 row_ror:8 row_mask:0xf bank_mask:0xf bound_ctrl:1
	v_cndmask_b32_e64 v106, v99, v98, s[38:39]
	v_cndmask_b32_e64 v107, v101, v100, s[38:39]
	v_cndmask_b32_e64 v108, v103, v102, s[38:39]
	v_cndmask_b32_e64 v109, v105, v104, s[38:39]
	v_fma_f32 v110, v158, v106, v154
	v_fma_f32 v111, v159, v107, v155
	v_fma_f32 v112, v160, v108, v156
	v_fma_f32 v113, v161, v109, v157
	global_store_dwordx4 v[240:241], v[110:113], off
	v_add_u32_e32 v226, 2, v226
	s_add_i32 s33, s33, 2
	s_cmp_lt_u32 s33, 8
	s_cbranch_scc1 .Le2_loop
	s_cmp_lt_i32 s35, 0
	s_cbranch_scc1 .Le2_chain_end
	s_mov_b32 s33, 0
	s_branch .Le2_loop
